# baseline (speedup 1.0000x reference)
.LBB2_3:
	s_lshl_b32 s3, s2, 2
	s_and_b32 s3, s3, 28
	s_bfe_u32 s2, s2, 0x20003
	s_load_dwordx2 s[12:13], s[0:1], 0x8
	s_load_dwordx2 s[4:5], s[0:1], 0x28
	s_or_b32 s6, s3, s2
	s_lshl_b32 s2, s6, 8
	s_lshl_b32 s3, s9, 6
	s_or_b32 s3, s3, s2
	s_lshl_b32 s2, s3, 10
	s_waitcnt lgkmcnt(0)
	s_add_u32 s12, s12, s2
	s_addc_u32 s13, s13, 0
	v_lshl_add_u64 v[132:133], s[12:13], 0, v[130:131]
	s_movk_i32 s2, 0x1000
	v_add_co_u32_e32 v6, vcc, s2, v132
	s_movk_i32 s2, 0x2000
	s_nop 0
	v_addc_co_u32_e32 v7, vcc, 0, v133, vcc
	v_add_co_u32_e32 v8, vcc, s2, v132
	global_load_dwordx4 v[66:69], v130, s[12:13] offset:1024
	global_load_dwordx4 v[74:77], v130, s[12:13] offset:2048
	v_addc_co_u32_e32 v9, vcc, 0, v133, vcc
	global_load_dwordx4 v[78:81], v130, s[12:13] offset:3072
	global_load_dwordx4 v[82:85], v[8:9], off offset:-4096
	global_load_dwordx4 v[106:109], v[6:7], off offset:1024
	global_load_dwordx4 v[114:117], v[6:7], off offset:2048
	global_load_dwordx4 v[2:5], v130, s[12:13]
	global_load_dwordx4 v[118:121], v[6:7], off offset:3072
	global_load_dwordx4 v[122:125], v[8:9], off
	global_load_dwordx4 v[102:105], v[8:9], off offset:1024
	global_load_dwordx4 v[86:89], v[8:9], off offset:2048
	global_load_dwordx4 v[70:73], v[8:9], off offset:3072
	s_barrier
	ds_read_b128 v[6:9], v130
	ds_read_b128 v[10:13], v130 offset:4096
	ds_read_b128 v[14:17], v130 offset:8192
	ds_read_b128 v[94:97], v130 offset:12288
	ds_read_b128 v[98:101], v130 offset:1024
	s_waitcnt vmcnt(5) lgkmcnt(4)
	v_mfma_f32_32x32x16_f16 v[50:65], v[6:9], v[2:5], 0
	s_movk_i32 s2, 0x4000
	v_add_co_u32_e32 v146, vcc, s2, v132
	ds_read_b128 v[110:113], v130 offset:5120
	s_nop 0
	v_addc_co_u32_e32 v147, vcc, 0, v133, vcc
	global_load_dwordx4 v[90:93], v[146:147], off offset:-4096
	s_movk_i32 s2, 0x3000
	v_add_co_u32_e32 v148, vcc, s2, v132
	s_waitcnt lgkmcnt(4)
	v_mfma_f32_32x32x16_f16 v[34:49], v[10:13], v[2:5], 0
	v_addc_co_u32_e32 v149, vcc, 0, v133, vcc
	ds_read_b128 v[126:129], v130 offset:9216
	s_waitcnt lgkmcnt(4)
	v_mfma_f32_32x32x16_f16 v[18:33], v[14:17], v[2:5], 0
	s_waitcnt lgkmcnt(3)
	v_mfma_f32_32x32x16_f16 v[2:17], v[94:97], v[2:5], 0
	ds_read_b128 v[134:137], v130 offset:13312
	ds_read_b128 v[138:141], v130 offset:2048
	s_waitcnt lgkmcnt(4)
	v_mfma_f32_32x32x16_f16 v[50:65], v[98:101], v[66:69], v[50:65]
	ds_read_b128 v[150:153], v130 offset:3072
	global_load_dwordx4 v[94:97], v[148:149], off offset:1024
	ds_read_b128 v[98:101], v130 offset:6144
	s_waitcnt lgkmcnt(5)
	v_mfma_f32_32x32x16_f16 v[34:49], v[110:113], v[66:69], v[34:49]
	ds_read_b128 v[142:145], v130 offset:10240
	ds_read_b128 v[154:157], v130 offset:7168
	s_waitcnt lgkmcnt(6)
	v_mfma_f32_32x32x16_f16 v[18:33], v[126:129], v[66:69], v[18:33]
	ds_read_b128 v[158:161], v130 offset:11264
	s_waitcnt lgkmcnt(6)
	v_mfma_f32_32x32x16_f16 v[2:17], v[134:137], v[66:69], v[2:17]
	ds_read_b128 v[126:129], v130 offset:14336
	ds_read_b128 v[162:165], v130 offset:15360
	s_waitcnt lgkmcnt(7)
	v_mfma_f32_32x32x16_f16 v[50:65], v[138:141], v[74:77], v[50:65]
	global_load_dwordx4 v[110:113], v[148:149], off offset:2048
	s_waitcnt lgkmcnt(5)
	v_mfma_f32_32x32x16_f16 v[34:49], v[98:101], v[74:77], v[34:49]
	s_waitcnt lgkmcnt(4)
	v_mfma_f32_32x32x16_f16 v[18:33], v[142:145], v[74:77], v[18:33]
	s_waitcnt lgkmcnt(1)
	v_mfma_f32_32x32x16_f16 v[2:17], v[126:129], v[74:77], v[2:17]
	global_load_dwordx4 v[98:101], v[148:149], off offset:3072
	v_mfma_f32_32x32x16_f16 v[50:65], v[150:153], v[78:81], v[50:65]
	s_waitcnt lgkmcnt(0)
	s_barrier
	ds_read_b128 v[66:69], v130 offset:16384
	ds_read_b128 v[126:129], v130 offset:20480
	v_mfma_f32_32x32x16_f16 v[34:49], v[154:157], v[78:81], v[34:49]
	ds_read_b128 v[134:137], v130 offset:24576
	v_mfma_f32_32x32x16_f16 v[18:33], v[158:161], v[78:81], v[18:33]
	v_mfma_f32_32x32x16_f16 v[2:17], v[162:165], v[78:81], v[2:17]
	ds_read_b128 v[138:141], v130 offset:28672
	ds_read_b128 v[78:81], v130 offset:17408
	s_waitcnt lgkmcnt(4)
	v_mfma_f32_32x32x16_f16 v[50:65], v[66:69], v[82:85], v[50:65]
	global_load_dwordx4 v[74:77], v[146:147], off
	ds_read_b128 v[66:69], v130 offset:21504
	s_waitcnt lgkmcnt(4)
	v_mfma_f32_32x32x16_f16 v[34:49], v[126:129], v[82:85], v[34:49]
	ds_read_b128 v[126:129], v130 offset:25600
	s_waitcnt lgkmcnt(4)
	v_mfma_f32_32x32x16_f16 v[18:33], v[134:137], v[82:85], v[18:33]
	s_waitcnt lgkmcnt(3)
	v_mfma_f32_32x32x16_f16 v[2:17], v[138:141], v[82:85], v[2:17]
	ds_read_b128 v[134:137], v130 offset:29696
	ds_read_b128 v[82:85], v130 offset:18432
	s_waitcnt lgkmcnt(4)
	v_mfma_f32_32x32x16_f16 v[50:65], v[78:81], v[106:109], v[50:65]
	ds_read_b128 v[150:153], v130 offset:19456
	global_load_dwordx4 v[78:81], v[146:147], off offset:1024
	ds_read_b128 v[138:141], v130 offset:22528
	s_waitcnt lgkmcnt(5)
	v_mfma_f32_32x32x16_f16 v[34:49], v[66:69], v[106:109], v[34:49]
	ds_read_b128 v[66:69], v130 offset:26624
	ds_read_b128 v[154:157], v130 offset:23552
	s_waitcnt lgkmcnt(6)
	v_mfma_f32_32x32x16_f16 v[18:33], v[126:129], v[106:109], v[18:33]
	ds_read_b128 v[158:161], v130 offset:27648
	s_waitcnt lgkmcnt(6)
	v_mfma_f32_32x32x16_f16 v[2:17], v[134:137], v[106:109], v[2:17]
	ds_read_b128 v[126:129], v130 offset:30720
	ds_read_b128 v[162:165], v130 offset:31744
	s_waitcnt lgkmcnt(7)
	v_mfma_f32_32x32x16_f16 v[50:65], v[82:85], v[114:117], v[50:65]
	global_load_dwordx4 v[82:85], v[146:147], off offset:2048
	s_waitcnt lgkmcnt(5)
	v_mfma_f32_32x32x16_f16 v[34:49], v[138:141], v[114:117], v[34:49]
	s_waitcnt lgkmcnt(4)
	v_mfma_f32_32x32x16_f16 v[18:33], v[66:69], v[114:117], v[18:33]
	s_waitcnt lgkmcnt(1)
	v_mfma_f32_32x32x16_f16 v[2:17], v[126:129], v[114:117], v[2:17]
	global_load_dwordx4 v[66:69], v[146:147], off offset:3072
	s_waitcnt vmcnt(12)
	v_mfma_f32_32x32x16_f16 v[50:65], v[150:153], v[118:121], v[50:65]
	s_waitcnt lgkmcnt(0)
	s_barrier
	ds_read_b128 v[106:109], v130
	ds_read_b128 v[114:117], v130 offset:4096
	v_mfma_f32_32x32x16_f16 v[34:49], v[154:157], v[118:121], v[34:49]
	ds_read_b128 v[126:129], v130 offset:8192
	v_mfma_f32_32x32x16_f16 v[18:33], v[158:161], v[118:121], v[18:33]
	v_mfma_f32_32x32x16_f16 v[2:17], v[162:165], v[118:121], v[2:17]
	ds_read_b128 v[134:137], v130 offset:12288
	ds_read_b128 v[118:121], v130 offset:1024
	s_waitcnt vmcnt(11) lgkmcnt(4)
	v_mfma_f32_32x32x16_f16 v[50:65], v[106:109], v[122:125], v[50:65]
	s_movk_i32 s2, 0x6000
	v_add_co_u32_e32 v146, vcc, s2, v132
	ds_read_b128 v[138:141], v130 offset:5120
	s_nop 0
	v_addc_co_u32_e32 v147, vcc, 0, v133, vcc
	global_load_dwordx4 v[106:109], v[146:147], off offset:-4096
	s_movk_i32 s2, 0x5000
	v_add_co_u32_e32 v148, vcc, s2, v132
	s_waitcnt lgkmcnt(4)
	v_mfma_f32_32x32x16_f16 v[34:49], v[114:117], v[122:125], v[34:49]
	v_addc_co_u32_e32 v149, vcc, 0, v133, vcc
	ds_read_b128 v[142:145], v130 offset:9216
	s_waitcnt lgkmcnt(4)
	v_mfma_f32_32x32x16_f16 v[18:33], v[126:129], v[122:125], v[18:33]
	s_waitcnt lgkmcnt(3)
	v_mfma_f32_32x32x16_f16 v[2:17], v[134:137], v[122:125], v[2:17]
	ds_read_b128 v[126:129], v130 offset:13312
	ds_read_b128 v[122:125], v130 offset:2048
	s_waitcnt vmcnt(11) lgkmcnt(4)
	v_mfma_f32_32x32x16_f16 v[50:65], v[118:121], v[102:105], v[50:65]
	ds_read_b128 v[150:153], v130 offset:3072
	global_load_dwordx4 v[114:117], v[148:149], off offset:1024
	ds_read_b128 v[134:137], v130 offset:6144
	s_waitcnt lgkmcnt(5)
	v_mfma_f32_32x32x16_f16 v[34:49], v[138:141], v[102:105], v[34:49]
	ds_read_b128 v[138:141], v130 offset:10240
	ds_read_b128 v[154:157], v130 offset:7168
	s_waitcnt lgkmcnt(6)
	v_mfma_f32_32x32x16_f16 v[18:33], v[142:145], v[102:105], v[18:33]
	ds_read_b128 v[158:161], v130 offset:11264
	s_waitcnt lgkmcnt(6)
	v_mfma_f32_32x32x16_f16 v[2:17], v[126:129], v[102:105], v[2:17]
	ds_read_b128 v[142:145], v130 offset:14336
	ds_read_b128 v[162:165], v130 offset:15360
	s_waitcnt vmcnt(11) lgkmcnt(7)
	v_mfma_f32_32x32x16_f16 v[50:65], v[122:125], v[86:89], v[50:65]
	global_load_dwordx4 v[118:121], v[148:149], off offset:2048
	s_waitcnt lgkmcnt(5)
	v_mfma_f32_32x32x16_f16 v[34:49], v[134:137], v[86:89], v[34:49]
	s_waitcnt lgkmcnt(4)
	v_mfma_f32_32x32x16_f16 v[18:33], v[138:141], v[86:89], v[18:33]
	s_waitcnt lgkmcnt(1)
	v_mfma_f32_32x32x16_f16 v[2:17], v[142:145], v[86:89], v[2:17]
	global_load_dwordx4 v[102:105], v[148:149], off offset:3072
	s_waitcnt vmcnt(12)
	v_mfma_f32_32x32x16_f16 v[50:65], v[150:153], v[70:73], v[50:65]
	s_waitcnt lgkmcnt(0)
	s_barrier
	ds_read_b128 v[86:89], v130 offset:16384
	ds_read_b128 v[126:129], v130 offset:20480
	v_mfma_f32_32x32x16_f16 v[34:49], v[154:157], v[70:73], v[34:49]
	ds_read_b128 v[122:125], v130 offset:24576
	v_mfma_f32_32x32x16_f16 v[18:33], v[158:161], v[70:73], v[18:33]
	v_mfma_f32_32x32x16_f16 v[2:17], v[162:165], v[70:73], v[2:17]
	ds_read_b128 v[134:137], v130 offset:28672
	ds_read_b128 v[70:73], v130 offset:17408
	s_waitcnt vmcnt(11) lgkmcnt(4)
	v_mfma_f32_32x32x16_f16 v[50:65], v[86:89], v[90:93], v[50:65]
	global_load_dwordx4 v[86:89], v[146:147], off
	ds_read_b128 v[138:141], v130 offset:21504
	s_waitcnt lgkmcnt(4)
	v_mfma_f32_32x32x16_f16 v[34:49], v[126:129], v[90:93], v[34:49]
	ds_read_b128 v[126:129], v130 offset:25600
	s_waitcnt lgkmcnt(4)
	v_mfma_f32_32x32x16_f16 v[18:33], v[122:125], v[90:93], v[18:33]
	s_waitcnt lgkmcnt(3)
	v_mfma_f32_32x32x16_f16 v[2:17], v[134:137], v[90:93], v[2:17]
	ds_read_b128 v[122:125], v130 offset:29696
	ds_read_b128 v[134:137], v130 offset:18432
	s_waitcnt vmcnt(11) lgkmcnt(4)
	v_mfma_f32_32x32x16_f16 v[50:65], v[70:73], v[94:97], v[50:65]
	ds_read_b128 v[150:153], v130 offset:19456
	global_load_dwordx4 v[90:93], v[146:147], off offset:1024
	ds_read_b128 v[70:73], v130 offset:22528
	s_waitcnt lgkmcnt(5)
	v_mfma_f32_32x32x16_f16 v[34:49], v[138:141], v[94:97], v[34:49]
	ds_read_b128 v[138:141], v130 offset:26624
	ds_read_b128 v[154:157], v130 offset:23552
	s_waitcnt lgkmcnt(6)
	v_mfma_f32_32x32x16_f16 v[18:33], v[126:129], v[94:97], v[18:33]
	ds_read_b128 v[158:161], v130 offset:27648
	s_waitcnt lgkmcnt(6)
	v_mfma_f32_32x32x16_f16 v[2:17], v[122:125], v[94:97], v[2:17]
	ds_read_b128 v[126:129], v130 offset:30720
	ds_read_b128 v[162:165], v130 offset:31744
	s_waitcnt vmcnt(11) lgkmcnt(7)
	v_mfma_f32_32x32x16_f16 v[50:65], v[134:137], v[110:113], v[50:65]
	global_load_dwordx4 v[94:97], v[146:147], off offset:2048
	s_waitcnt lgkmcnt(5)
	v_mfma_f32_32x32x16_f16 v[34:49], v[70:73], v[110:113], v[34:49]
	s_waitcnt lgkmcnt(4)
	v_mfma_f32_32x32x16_f16 v[18:33], v[138:141], v[110:113], v[18:33]
	s_waitcnt lgkmcnt(1)
	v_mfma_f32_32x32x16_f16 v[2:17], v[126:129], v[110:113], v[2:17]
	global_load_dwordx4 v[70:73], v[146:147], off offset:3072
	s_waitcnt vmcnt(12)
	v_mfma_f32_32x32x16_f16 v[50:65], v[150:153], v[98:101], v[50:65]
	s_waitcnt lgkmcnt(0)
	s_barrier
	ds_read_b128 v[110:113], v130
	ds_read_b128 v[122:125], v130 offset:4096
	v_mfma_f32_32x32x16_f16 v[34:49], v[154:157], v[98:101], v[34:49]
	ds_read_b128 v[126:129], v130 offset:8192
	v_mfma_f32_32x32x16_f16 v[18:33], v[158:161], v[98:101], v[18:33]
	v_mfma_f32_32x32x16_f16 v[2:17], v[162:165], v[98:101], v[2:17]
	ds_read_b128 v[134:137], v130 offset:12288
	ds_read_b128 v[98:101], v130 offset:1024
	s_waitcnt vmcnt(11) lgkmcnt(4)
	v_mfma_f32_32x32x16_f16 v[50:65], v[110:113], v[74:77], v[50:65]
	s_mov_b32 s2, 0x8000
	v_add_co_u32_e32 v146, vcc, s2, v132
	ds_read_b128 v[138:141], v130 offset:5120
	s_nop 0
	v_addc_co_u32_e32 v147, vcc, 0, v133, vcc
	global_load_dwordx4 v[110:113], v[146:147], off offset:-4096
	s_movk_i32 s2, 0x7000
	v_add_co_u32_e32 v148, vcc, s2, v132
	s_waitcnt lgkmcnt(4)
	v_mfma_f32_32x32x16_f16 v[34:49], v[122:125], v[74:77], v[34:49]
	v_addc_co_u32_e32 v149, vcc, 0, v133, vcc
	ds_read_b128 v[142:145], v130 offset:9216
	s_waitcnt lgkmcnt(4)
	v_mfma_f32_32x32x16_f16 v[18:33], v[126:129], v[74:77], v[18:33]
	s_waitcnt lgkmcnt(3)
	v_mfma_f32_32x32x16_f16 v[2:17], v[134:137], v[74:77], v[2:17]
	ds_read_b128 v[126:129], v130 offset:13312
	ds_read_b128 v[74:77], v130 offset:2048
	s_waitcnt vmcnt(11) lgkmcnt(4)
	v_mfma_f32_32x32x16_f16 v[50:65], v[98:101], v[78:81], v[50:65]
	ds_read_b128 v[150:153], v130 offset:3072
	global_load_dwordx4 v[122:125], v[148:149], off offset:1024
	ds_read_b128 v[98:101], v130 offset:6144
	s_waitcnt lgkmcnt(5)
	v_mfma_f32_32x32x16_f16 v[34:49], v[138:141], v[78:81], v[34:49]
	ds_read_b128 v[134:137], v130 offset:10240
	ds_read_b128 v[154:157], v130 offset:7168
	s_waitcnt lgkmcnt(6)
	v_mfma_f32_32x32x16_f16 v[18:33], v[142:145], v[78:81], v[18:33]
	ds_read_b128 v[158:161], v130 offset:11264
	s_waitcnt lgkmcnt(6)
	v_mfma_f32_32x32x16_f16 v[2:17], v[126:129], v[78:81], v[2:17]
	ds_read_b128 v[138:141], v130 offset:14336
	ds_read_b128 v[162:165], v130 offset:15360
	s_waitcnt vmcnt(11) lgkmcnt(7)
	v_mfma_f32_32x32x16_f16 v[50:65], v[74:77], v[82:85], v[50:65]
	global_load_dwordx4 v[126:129], v[148:149], off offset:2048
	s_waitcnt lgkmcnt(5)
	v_mfma_f32_32x32x16_f16 v[34:49], v[98:101], v[82:85], v[34:49]
	s_waitcnt lgkmcnt(4)
	v_mfma_f32_32x32x16_f16 v[18:33], v[134:137], v[82:85], v[18:33]
	s_waitcnt lgkmcnt(1)
	v_mfma_f32_32x32x16_f16 v[2:17], v[138:141], v[82:85], v[2:17]
	global_load_dwordx4 v[98:101], v[148:149], off offset:3072
	s_waitcnt vmcnt(12)
	v_mfma_f32_32x32x16_f16 v[50:65], v[150:153], v[66:69], v[50:65]
	s_waitcnt lgkmcnt(0)
	s_barrier
	ds_read_b128 v[78:81], v130 offset:16384
	ds_read_b128 v[82:85], v130 offset:20480
	v_mfma_f32_32x32x16_f16 v[34:49], v[154:157], v[66:69], v[34:49]
	ds_read_b128 v[138:141], v130 offset:24576
	v_mfma_f32_32x32x16_f16 v[18:33], v[158:161], v[66:69], v[18:33]
	v_mfma_f32_32x32x16_f16 v[2:17], v[162:165], v[66:69], v[2:17]
	ds_read_b128 v[142:145], v130 offset:28672
	ds_read_b128 v[66:69], v130 offset:17408
	s_waitcnt vmcnt(11) lgkmcnt(4)
	v_mfma_f32_32x32x16_f16 v[50:65], v[78:81], v[106:109], v[50:65]
	global_load_dwordx4 v[74:77], v[146:147], off
	ds_read_b128 v[134:137], v130 offset:21504
	s_waitcnt lgkmcnt(4)
	v_mfma_f32_32x32x16_f16 v[34:49], v[82:85], v[106:109], v[34:49]
	ds_read_b128 v[82:85], v130 offset:25600
	s_waitcnt lgkmcnt(4)
	v_mfma_f32_32x32x16_f16 v[18:33], v[138:141], v[106:109], v[18:33]
	s_waitcnt lgkmcnt(3)
	v_mfma_f32_32x32x16_f16 v[2:17], v[142:145], v[106:109], v[2:17]
	ds_read_b128 v[138:141], v130 offset:29696
	ds_read_b128 v[106:109], v130 offset:18432
	s_waitcnt vmcnt(11) lgkmcnt(4)
	v_mfma_f32_32x32x16_f16 v[50:65], v[66:69], v[114:117], v[50:65]
	ds_read_b128 v[150:153], v130 offset:19456
	global_load_dwordx4 v[78:81], v[146:147], off offset:1024
	ds_read_b128 v[66:69], v130 offset:22528
	s_waitcnt lgkmcnt(5)
	v_mfma_f32_32x32x16_f16 v[34:49], v[134:137], v[114:117], v[34:49]
	ds_read_b128 v[134:137], v130 offset:26624
	ds_read_b128 v[154:157], v130 offset:23552
	s_waitcnt lgkmcnt(6)
	v_mfma_f32_32x32x16_f16 v[18:33], v[82:85], v[114:117], v[18:33]
	ds_read_b128 v[158:161], v130 offset:27648
	s_waitcnt lgkmcnt(6)
	v_mfma_f32_32x32x16_f16 v[2:17], v[138:141], v[114:117], v[2:17]
	ds_read_b128 v[142:145], v130 offset:30720
	ds_read_b128 v[162:165], v130 offset:31744
	s_waitcnt vmcnt(11) lgkmcnt(7)
	v_mfma_f32_32x32x16_f16 v[50:65], v[106:109], v[118:121], v[50:65]
	global_load_dwordx4 v[82:85], v[146:147], off offset:2048
	s_waitcnt lgkmcnt(5)
	v_mfma_f32_32x32x16_f16 v[34:49], v[66:69], v[118:121], v[34:49]
	s_waitcnt lgkmcnt(4)
	v_mfma_f32_32x32x16_f16 v[18:33], v[134:137], v[118:121], v[18:33]
	s_waitcnt lgkmcnt(1)
	v_mfma_f32_32x32x16_f16 v[2:17], v[142:145], v[118:121], v[2:17]
	global_load_dwordx4 v[66:69], v[146:147], off offset:3072
	s_waitcnt vmcnt(12)
	v_mfma_f32_32x32x16_f16 v[50:65], v[150:153], v[102:105], v[50:65]
	s_waitcnt lgkmcnt(0)
	s_barrier
	ds_read_b128 v[114:117], v130
	ds_read_b128 v[118:121], v130 offset:4096
	v_mfma_f32_32x32x16_f16 v[34:49], v[154:157], v[102:105], v[34:49]
	ds_read_b128 v[142:145], v130 offset:8192
	v_mfma_f32_32x32x16_f16 v[18:33], v[158:161], v[102:105], v[18:33]
	v_mfma_f32_32x32x16_f16 v[2:17], v[162:165], v[102:105], v[2:17]
	ds_read_b128 v[138:141], v130 offset:12288
	ds_read_b128 v[102:105], v130 offset:1024
	s_waitcnt vmcnt(11) lgkmcnt(4)
	v_mfma_f32_32x32x16_f16 v[50:65], v[114:117], v[86:89], v[50:65]
	s_mov_b32 s2, 0xa000
	v_add_co_u32_e32 v146, vcc, s2, v132
	s_waitcnt lgkmcnt(3)
	v_mfma_f32_32x32x16_f16 v[34:49], v[118:121], v[86:89], v[34:49]
	v_addc_co_u32_e32 v147, vcc, 0, v133, vcc
	global_load_dwordx4 v[106:109], v[146:147], off offset:-4096
	ds_read_b128 v[118:121], v130 offset:5120
	s_mov_b32 s2, 0x9000
	v_add_co_u32_e32 v148, vcc, s2, v132
	s_nop 1
	v_addc_co_u32_e32 v149, vcc, 0, v133, vcc
	ds_read_b128 v[134:137], v130 offset:9216
	s_waitcnt lgkmcnt(4)
	v_mfma_f32_32x32x16_f16 v[18:33], v[142:145], v[86:89], v[18:33]
	s_waitcnt lgkmcnt(3)
	v_mfma_f32_32x32x16_f16 v[2:17], v[138:141], v[86:89], v[2:17]
	ds_read_b128 v[142:145], v130 offset:13312
	ds_read_b128 v[86:89], v130 offset:2048
	s_waitcnt vmcnt(11) lgkmcnt(4)
	v_mfma_f32_32x32x16_f16 v[50:65], v[102:105], v[90:93], v[50:65]
	ds_read_b128 v[150:153], v130 offset:3072
	global_load_dwordx4 v[114:117], v[148:149], off offset:1024
	ds_read_b128 v[102:105], v130 offset:6144
	s_waitcnt lgkmcnt(5)
	v_mfma_f32_32x32x16_f16 v[34:49], v[118:121], v[90:93], v[34:49]
	ds_read_b128 v[138:141], v130 offset:10240
	ds_read_b128 v[154:157], v130 offset:7168
	s_waitcnt lgkmcnt(6)
	v_mfma_f32_32x32x16_f16 v[18:33], v[134:137], v[90:93], v[18:33]
	ds_read_b128 v[158:161], v130 offset:11264
	s_waitcnt lgkmcnt(6)
	v_mfma_f32_32x32x16_f16 v[2:17], v[142:145], v[90:93], v[2:17]
	ds_read_b128 v[134:137], v130 offset:14336
	ds_read_b128 v[162:165], v130 offset:15360
	s_waitcnt vmcnt(11) lgkmcnt(7)
	v_mfma_f32_32x32x16_f16 v[50:65], v[86:89], v[94:97], v[50:65]
	global_load_dwordx4 v[118:121], v[148:149], off offset:2048
	s_waitcnt lgkmcnt(5)
	v_mfma_f32_32x32x16_f16 v[34:49], v[102:105], v[94:97], v[34:49]
	s_waitcnt lgkmcnt(4)
	v_mfma_f32_32x32x16_f16 v[18:33], v[138:141], v[94:97], v[18:33]
	s_waitcnt lgkmcnt(1)
	v_mfma_f32_32x32x16_f16 v[2:17], v[134:137], v[94:97], v[2:17]
	global_load_dwordx4 v[102:105], v[148:149], off offset:3072
	s_waitcnt vmcnt(12)
	v_mfma_f32_32x32x16_f16 v[50:65], v[150:153], v[70:73], v[50:65]
	s_waitcnt lgkmcnt(0)
	s_barrier
	ds_read_b128 v[90:93], v130 offset:16384
	ds_read_b128 v[94:97], v130 offset:20480
	v_mfma_f32_32x32x16_f16 v[34:49], v[154:157], v[70:73], v[34:49]
	ds_read_b128 v[134:137], v130 offset:24576
	v_mfma_f32_32x32x16_f16 v[18:33], v[158:161], v[70:73], v[18:33]
	v_mfma_f32_32x32x16_f16 v[2:17], v[162:165], v[70:73], v[2:17]
	ds_read_b128 v[142:145], v130 offset:28672
	ds_read_b128 v[70:73], v130 offset:17408
	s_waitcnt vmcnt(11) lgkmcnt(4)
	v_mfma_f32_32x32x16_f16 v[50:65], v[90:93], v[110:113], v[50:65]
	global_load_dwordx4 v[86:89], v[146:147], off
	ds_read_b128 v[138:141], v130 offset:21504
	s_waitcnt lgkmcnt(4)
	v_mfma_f32_32x32x16_f16 v[34:49], v[94:97], v[110:113], v[34:49]
	ds_read_b128 v[94:97], v130 offset:25600
	s_waitcnt lgkmcnt(4)
	v_mfma_f32_32x32x16_f16 v[18:33], v[134:137], v[110:113], v[18:33]
	s_waitcnt lgkmcnt(3)
	v_mfma_f32_32x32x16_f16 v[2:17], v[142:145], v[110:113], v[2:17]
	ds_read_b128 v[134:137], v130 offset:29696
	ds_read_b128 v[110:113], v130 offset:18432
	s_waitcnt vmcnt(11) lgkmcnt(4)
	v_mfma_f32_32x32x16_f16 v[50:65], v[70:73], v[122:125], v[50:65]
	ds_read_b128 v[150:153], v130 offset:19456
	global_load_dwordx4 v[90:93], v[146:147], off offset:1024
	ds_read_b128 v[70:73], v130 offset:22528
	s_waitcnt lgkmcnt(5)
	v_mfma_f32_32x32x16_f16 v[34:49], v[138:141], v[122:125], v[34:49]
	ds_read_b128 v[138:141], v130 offset:26624
	ds_read_b128 v[154:157], v130 offset:23552
	s_waitcnt lgkmcnt(6)
	v_mfma_f32_32x32x16_f16 v[18:33], v[94:97], v[122:125], v[18:33]
	ds_read_b128 v[158:161], v130 offset:27648
	s_waitcnt lgkmcnt(6)
	v_mfma_f32_32x32x16_f16 v[2:17], v[134:137], v[122:125], v[2:17]
	ds_read_b128 v[142:145], v130 offset:30720
	ds_read_b128 v[162:165], v130 offset:31744
	s_waitcnt vmcnt(11) lgkmcnt(7)
	v_mfma_f32_32x32x16_f16 v[50:65], v[110:113], v[126:129], v[50:65]
	global_load_dwordx4 v[94:97], v[146:147], off offset:2048
	s_waitcnt lgkmcnt(5)
	v_mfma_f32_32x32x16_f16 v[34:49], v[70:73], v[126:129], v[34:49]
	s_waitcnt lgkmcnt(4)
	v_mfma_f32_32x32x16_f16 v[18:33], v[138:141], v[126:129], v[18:33]
	s_waitcnt lgkmcnt(1)
	v_mfma_f32_32x32x16_f16 v[2:17], v[142:145], v[126:129], v[2:17]
	global_load_dwordx4 v[70:73], v[146:147], off offset:3072
	s_waitcnt vmcnt(12)
	v_mfma_f32_32x32x16_f16 v[50:65], v[150:153], v[98:101], v[50:65]
	s_waitcnt lgkmcnt(0)
	s_barrier
	ds_read_b128 v[122:125], v130
	ds_read_b128 v[126:129], v130 offset:4096
	v_mfma_f32_32x32x16_f16 v[34:49], v[154:157], v[98:101], v[34:49]
	ds_read_b128 v[142:145], v130 offset:8192
	v_mfma_f32_32x32x16_f16 v[18:33], v[158:161], v[98:101], v[18:33]
	v_mfma_f32_32x32x16_f16 v[2:17], v[162:165], v[98:101], v[2:17]
	ds_read_b128 v[134:137], v130 offset:12288
	ds_read_b128 v[98:101], v130 offset:1024
	s_waitcnt vmcnt(11) lgkmcnt(4)
	v_mfma_f32_32x32x16_f16 v[50:65], v[122:125], v[74:77], v[50:65]
	s_mov_b32 s2, 0xc000
	v_add_co_u32_e32 v146, vcc, s2, v132
	s_waitcnt lgkmcnt(3)
	v_mfma_f32_32x32x16_f16 v[34:49], v[126:129], v[74:77], v[34:49]
	v_addc_co_u32_e32 v147, vcc, 0, v133, vcc
	global_load_dwordx4 v[110:113], v[146:147], off offset:-4096
	ds_read_b128 v[126:129], v130 offset:5120
	s_mov_b32 s2, 0xb000
	v_add_co_u32_e32 v148, vcc, s2, v132
	s_nop 1
	v_addc_co_u32_e32 v149, vcc, 0, v133, vcc
	ds_read_b128 v[138:141], v130 offset:9216
	s_waitcnt lgkmcnt(4)
	v_mfma_f32_32x32x16_f16 v[18:33], v[142:145], v[74:77], v[18:33]
	s_waitcnt lgkmcnt(3)
	v_mfma_f32_32x32x16_f16 v[2:17], v[134:137], v[74:77], v[2:17]
	ds_read_b128 v[142:145], v130 offset:13312
	ds_read_b128 v[74:77], v130 offset:2048
	s_waitcnt vmcnt(11) lgkmcnt(4)
	v_mfma_f32_32x32x16_f16 v[50:65], v[98:101], v[78:81], v[50:65]
	ds_read_b128 v[150:153], v130 offset:3072
	global_load_dwordx4 v[122:125], v[148:149], off offset:1024
	ds_read_b128 v[98:101], v130 offset:6144
	s_waitcnt lgkmcnt(5)
	v_mfma_f32_32x32x16_f16 v[34:49], v[126:129], v[78:81], v[34:49]
	ds_read_b128 v[134:137], v130 offset:10240
	ds_read_b128 v[154:157], v130 offset:7168
	s_waitcnt lgkmcnt(6)
	v_mfma_f32_32x32x16_f16 v[18:33], v[138:141], v[78:81], v[18:33]
	ds_read_b128 v[158:161], v130 offset:11264
	s_waitcnt lgkmcnt(6)
	v_mfma_f32_32x32x16_f16 v[2:17], v[142:145], v[78:81], v[2:17]
	ds_read_b128 v[138:141], v130 offset:14336
	ds_read_b128 v[162:165], v130 offset:15360
	s_waitcnt vmcnt(11) lgkmcnt(7)
	v_mfma_f32_32x32x16_f16 v[50:65], v[74:77], v[82:85], v[50:65]
	global_load_dwordx4 v[126:129], v[148:149], off offset:2048
	s_waitcnt lgkmcnt(5)
	v_mfma_f32_32x32x16_f16 v[34:49], v[98:101], v[82:85], v[34:49]
	s_waitcnt lgkmcnt(4)
	v_mfma_f32_32x32x16_f16 v[18:33], v[134:137], v[82:85], v[18:33]
	s_waitcnt lgkmcnt(1)
	v_mfma_f32_32x32x16_f16 v[2:17], v[138:141], v[82:85], v[2:17]
	global_load_dwordx4 v[74:77], v[148:149], off offset:3072
	s_waitcnt vmcnt(12)
	v_mfma_f32_32x32x16_f16 v[50:65], v[150:153], v[66:69], v[50:65]
	s_waitcnt lgkmcnt(0)
	s_barrier
	ds_read_b128 v[78:81], v130 offset:16384
	ds_read_b128 v[82:85], v130 offset:20480
	v_mfma_f32_32x32x16_f16 v[34:49], v[154:157], v[66:69], v[34:49]
	ds_read_b128 v[138:141], v130 offset:24576
	v_mfma_f32_32x32x16_f16 v[18:33], v[158:161], v[66:69], v[18:33]
	v_mfma_f32_32x32x16_f16 v[2:17], v[162:165], v[66:69], v[2:17]
	ds_read_b128 v[98:101], v130 offset:28672
	ds_read_b128 v[66:69], v130 offset:17408
	s_waitcnt vmcnt(11) lgkmcnt(4)
	v_mfma_f32_32x32x16_f16 v[50:65], v[78:81], v[106:109], v[50:65]
	global_load_dwordx4 v[78:81], v[146:147], off
	ds_read_b128 v[134:137], v130 offset:21504
	s_waitcnt lgkmcnt(4)
	v_mfma_f32_32x32x16_f16 v[34:49], v[82:85], v[106:109], v[34:49]
	ds_read_b128 v[142:145], v130 offset:25600
	s_waitcnt lgkmcnt(4)
	v_mfma_f32_32x32x16_f16 v[18:33], v[138:141], v[106:109], v[18:33]
	s_waitcnt lgkmcnt(3)
	v_mfma_f32_32x32x16_f16 v[2:17], v[98:101], v[106:109], v[2:17]
	ds_read_b128 v[138:141], v130 offset:29696
	ds_read_b128 v[98:101], v130 offset:18432
	s_waitcnt vmcnt(11) lgkmcnt(4)
	v_mfma_f32_32x32x16_f16 v[50:65], v[66:69], v[114:117], v[50:65]
	ds_read_b128 v[150:153], v130 offset:19456
	global_load_dwordx4 v[82:85], v[146:147], off offset:1024
	ds_read_b128 v[66:69], v130 offset:22528
	s_waitcnt lgkmcnt(5)
	v_mfma_f32_32x32x16_f16 v[34:49], v[134:137], v[114:117], v[34:49]
	ds_read_b128 v[106:109], v130 offset:26624
	ds_read_b128 v[154:157], v130 offset:23552
	s_waitcnt lgkmcnt(6)
	v_mfma_f32_32x32x16_f16 v[18:33], v[142:145], v[114:117], v[18:33]
	ds_read_b128 v[158:161], v130 offset:27648
	s_waitcnt lgkmcnt(6)
	v_mfma_f32_32x32x16_f16 v[2:17], v[138:141], v[114:117], v[2:17]
	ds_read_b128 v[134:137], v130 offset:30720
	ds_read_b128 v[162:165], v130 offset:31744
	s_waitcnt vmcnt(11) lgkmcnt(7)
	v_mfma_f32_32x32x16_f16 v[50:65], v[98:101], v[118:121], v[50:65]
	global_load_dwordx4 v[98:101], v[146:147], off offset:2048
	s_waitcnt lgkmcnt(5)
	v_mfma_f32_32x32x16_f16 v[34:49], v[66:69], v[118:121], v[34:49]
	s_waitcnt lgkmcnt(4)
	v_mfma_f32_32x32x16_f16 v[18:33], v[106:109], v[118:121], v[18:33]
	s_waitcnt lgkmcnt(1)
	v_mfma_f32_32x32x16_f16 v[2:17], v[134:137], v[118:121], v[2:17]
	global_load_dwordx4 v[66:69], v[146:147], off offset:3072
	s_waitcnt vmcnt(12)
	v_mfma_f32_32x32x16_f16 v[50:65], v[150:153], v[102:105], v[50:65]
	s_waitcnt lgkmcnt(0)
	s_barrier
	ds_read_b128 v[114:117], v130
	ds_read_b128 v[118:121], v130 offset:4096
	v_mfma_f32_32x32x16_f16 v[34:49], v[154:157], v[102:105], v[34:49]
	ds_read_b128 v[134:137], v130 offset:8192
	v_mfma_f32_32x32x16_f16 v[18:33], v[158:161], v[102:105], v[18:33]
	v_mfma_f32_32x32x16_f16 v[2:17], v[162:165], v[102:105], v[2:17]
	ds_read_b128 v[138:141], v130 offset:12288
	ds_read_b128 v[106:109], v130 offset:1024
	s_waitcnt vmcnt(11) lgkmcnt(4)
	v_mfma_f32_32x32x16_f16 v[50:65], v[114:117], v[86:89], v[50:65]
	s_mov_b32 s2, 0xe000
	v_add_co_u32_e32 v146, vcc, s2, v132
	ds_read_b128 v[114:117], v130 offset:5120
	s_nop 0
	v_addc_co_u32_e32 v147, vcc, 0, v133, vcc
	global_load_dwordx4 v[102:105], v[146:147], off offset:-4096
	s_mov_b32 s2, 0xd000
	v_add_co_u32_e32 v148, vcc, s2, v132
	s_waitcnt lgkmcnt(4)
	v_mfma_f32_32x32x16_f16 v[34:49], v[118:121], v[86:89], v[34:49]
	v_addc_co_u32_e32 v149, vcc, 0, v133, vcc
	ds_read_b128 v[118:121], v130 offset:9216
	s_waitcnt lgkmcnt(4)
	v_mfma_f32_32x32x16_f16 v[18:33], v[134:137], v[86:89], v[18:33]
	s_waitcnt lgkmcnt(3)
	v_mfma_f32_32x32x16_f16 v[2:17], v[138:141], v[86:89], v[2:17]
	ds_read_b128 v[134:137], v130 offset:13312
	ds_read_b128 v[86:89], v130 offset:2048
	s_waitcnt vmcnt(11) lgkmcnt(4)
	v_mfma_f32_32x32x16_f16 v[50:65], v[106:109], v[90:93], v[50:65]
	ds_read_b128 v[150:153], v130 offset:3072
	global_load_dwordx4 v[106:109], v[148:149], off offset:1024
	ds_read_b128 v[138:141], v130 offset:6144
	s_waitcnt lgkmcnt(5)
	v_mfma_f32_32x32x16_f16 v[34:49], v[114:117], v[90:93], v[34:49]
	ds_read_b128 v[114:117], v130 offset:10240
	ds_read_b128 v[154:157], v130 offset:7168
	s_waitcnt lgkmcnt(6)
	v_mfma_f32_32x32x16_f16 v[18:33], v[118:121], v[90:93], v[18:33]
	ds_read_b128 v[158:161], v130 offset:11264
	s_waitcnt lgkmcnt(6)
	v_mfma_f32_32x32x16_f16 v[2:17], v[134:137], v[90:93], v[2:17]
	ds_read_b128 v[118:121], v130 offset:14336
	ds_read_b128 v[162:165], v130 offset:15360
	s_waitcnt vmcnt(11) lgkmcnt(7)
	v_mfma_f32_32x32x16_f16 v[50:65], v[86:89], v[94:97], v[50:65]
	global_load_dwordx4 v[90:93], v[148:149], off offset:2048
	s_waitcnt lgkmcnt(5)
	v_mfma_f32_32x32x16_f16 v[34:49], v[138:141], v[94:97], v[34:49]
	s_waitcnt lgkmcnt(4)
	v_mfma_f32_32x32x16_f16 v[18:33], v[114:117], v[94:97], v[18:33]
	s_waitcnt lgkmcnt(1)
	v_mfma_f32_32x32x16_f16 v[2:17], v[118:121], v[94:97], v[2:17]
	global_load_dwordx4 v[86:89], v[148:149], off offset:3072
	s_waitcnt vmcnt(12)
	v_mfma_f32_32x32x16_f16 v[50:65], v[150:153], v[70:73], v[50:65]
	s_waitcnt lgkmcnt(0)
	s_barrier
	ds_read_b128 v[94:97], v130 offset:16384
	ds_read_b128 v[118:121], v130 offset:20480
	v_mfma_f32_32x32x16_f16 v[34:49], v[154:157], v[70:73], v[34:49]
	ds_read_b128 v[134:137], v130 offset:24576
	v_mfma_f32_32x32x16_f16 v[18:33], v[158:161], v[70:73], v[18:33]
	v_mfma_f32_32x32x16_f16 v[2:17], v[162:165], v[70:73], v[2:17]
	ds_read_b128 v[138:141], v130 offset:28672
	ds_read_b128 v[70:73], v130 offset:17408
	s_waitcnt vmcnt(11) lgkmcnt(4)
	v_mfma_f32_32x32x16_f16 v[50:65], v[94:97], v[110:113], v[50:65]
	global_load_dwordx4 v[94:97], v[146:147], off
	ds_read_b128 v[114:117], v130 offset:21504
	s_waitcnt lgkmcnt(4)
	v_mfma_f32_32x32x16_f16 v[34:49], v[118:121], v[110:113], v[34:49]
	ds_read_b128 v[118:121], v130 offset:25600
	s_waitcnt lgkmcnt(4)
	v_mfma_f32_32x32x16_f16 v[18:33], v[134:137], v[110:113], v[18:33]
	s_waitcnt lgkmcnt(3)
	v_mfma_f32_32x32x16_f16 v[2:17], v[138:141], v[110:113], v[2:17]
	ds_read_b128 v[134:137], v130 offset:29696
	ds_read_b128 v[138:141], v130 offset:18432
	s_waitcnt vmcnt(11) lgkmcnt(4)
	v_mfma_f32_32x32x16_f16 v[50:65], v[70:73], v[122:125], v[50:65]
	ds_read_b128 v[150:153], v130 offset:19456
	global_load_dwordx4 v[110:113], v[146:147], off offset:1024
	ds_read_b128 v[70:73], v130 offset:22528
	s_waitcnt lgkmcnt(5)
	v_mfma_f32_32x32x16_f16 v[34:49], v[114:117], v[122:125], v[34:49]
	ds_read_b128 v[142:145], v130 offset:26624
	ds_read_b128 v[154:157], v130 offset:23552
	s_waitcnt lgkmcnt(6)
	v_mfma_f32_32x32x16_f16 v[18:33], v[118:121], v[122:125], v[18:33]
	ds_read_b128 v[158:161], v130 offset:27648
	s_waitcnt lgkmcnt(6)
	v_mfma_f32_32x32x16_f16 v[2:17], v[134:137], v[122:125], v[2:17]
	ds_read_b128 v[118:121], v130 offset:30720
	ds_read_b128 v[162:165], v130 offset:31744
	s_waitcnt vmcnt(11) lgkmcnt(7)
	v_mfma_f32_32x32x16_f16 v[50:65], v[138:141], v[126:129], v[50:65]
	global_load_dwordx4 v[114:117], v[146:147], off offset:2048
	s_waitcnt lgkmcnt(5)
	v_mfma_f32_32x32x16_f16 v[34:49], v[70:73], v[126:129], v[34:49]
	s_waitcnt lgkmcnt(4)
	v_mfma_f32_32x32x16_f16 v[18:33], v[142:145], v[126:129], v[18:33]
	s_waitcnt lgkmcnt(1)
	v_mfma_f32_32x32x16_f16 v[2:17], v[118:121], v[126:129], v[2:17]
	global_load_dwordx4 v[70:73], v[146:147], off offset:3072
	s_waitcnt vmcnt(12)
	v_mfma_f32_32x32x16_f16 v[50:65], v[150:153], v[74:77], v[50:65]
	s_waitcnt lgkmcnt(0)
	s_barrier
	ds_read_b128 v[118:121], v130
	ds_read_b128 v[122:125], v130 offset:4096
	v_mfma_f32_32x32x16_f16 v[34:49], v[154:157], v[74:77], v[34:49]
	ds_read_b128 v[126:129], v130 offset:8192
	v_mfma_f32_32x32x16_f16 v[18:33], v[158:161], v[74:77], v[18:33]
	v_mfma_f32_32x32x16_f16 v[2:17], v[162:165], v[74:77], v[2:17]
	ds_read_b128 v[134:137], v130 offset:12288
	ds_read_b128 v[138:141], v130 offset:1024
	s_waitcnt vmcnt(11) lgkmcnt(4)
	v_mfma_f32_32x32x16_f16 v[50:65], v[118:121], v[78:81], v[50:65]
	s_mov_b32 s2, 0xf000
	v_add_co_u32_e32 v142, vcc, s2, v132
	ds_read_b128 v[118:121], v130 offset:5120
	s_nop 0
	v_addc_co_u32_e32 v143, vcc, 0, v133, vcc
	global_load_dwordx4 v[74:77], v[142:143], off
	s_waitcnt lgkmcnt(4)
	v_mfma_f32_32x32x16_f16 v[34:49], v[122:125], v[78:81], v[34:49]
	ds_read_b128 v[122:125], v130 offset:9216
	s_waitcnt lgkmcnt(4)
	v_mfma_f32_32x32x16_f16 v[18:33], v[126:129], v[78:81], v[18:33]
	s_waitcnt lgkmcnt(3)
	v_mfma_f32_32x32x16_f16 v[2:17], v[134:137], v[78:81], v[2:17]
	ds_read_b128 v[126:129], v130 offset:13312
	ds_read_b128 v[132:135], v130 offset:2048
	s_waitcnt vmcnt(11) lgkmcnt(4)
	v_mfma_f32_32x32x16_f16 v[50:65], v[138:141], v[82:85], v[50:65]
	ds_read_b128 v[150:153], v130 offset:3072
	global_load_dwordx4 v[78:81], v[142:143], off offset:1024
	ds_read_b128 v[136:139], v130 offset:6144
	s_waitcnt lgkmcnt(5)
	v_mfma_f32_32x32x16_f16 v[34:49], v[118:121], v[82:85], v[34:49]
	ds_read_b128 v[118:121], v130 offset:10240
	ds_read_b128 v[154:157], v130 offset:7168
	s_waitcnt lgkmcnt(6)
	v_mfma_f32_32x32x16_f16 v[18:33], v[122:125], v[82:85], v[18:33]
	ds_read_b128 v[158:161], v130 offset:11264
	s_waitcnt lgkmcnt(6)
	v_mfma_f32_32x32x16_f16 v[2:17], v[126:129], v[82:85], v[2:17]
	ds_read_b128 v[122:125], v130 offset:14336
	ds_read_b128 v[162:165], v130 offset:15360
	s_waitcnt vmcnt(11) lgkmcnt(7)
	v_mfma_f32_32x32x16_f16 v[50:65], v[132:135], v[98:101], v[50:65]
	global_load_dwordx4 v[82:85], v[142:143], off offset:2048
	s_waitcnt lgkmcnt(5)
	v_mfma_f32_32x32x16_f16 v[34:49], v[136:139], v[98:101], v[34:49]
	s_waitcnt lgkmcnt(4)
	v_mfma_f32_32x32x16_f16 v[18:33], v[118:121], v[98:101], v[18:33]
	s_waitcnt lgkmcnt(1)
	v_mfma_f32_32x32x16_f16 v[2:17], v[122:125], v[98:101], v[2:17]
	global_load_dwordx4 v[98:101], v[142:143], off offset:3072
	s_waitcnt vmcnt(12)
	v_mfma_f32_32x32x16_f16 v[50:65], v[150:153], v[66:69], v[50:65]
	s_waitcnt lgkmcnt(0)
	s_barrier
	ds_read_b128 v[122:125], v130 offset:16384
	ds_read_b128 v[126:129], v130 offset:20480
	v_mfma_f32_32x32x16_f16 v[34:49], v[154:157], v[66:69], v[34:49]
	ds_read_b128 v[132:135], v130 offset:24576
	v_mfma_f32_32x32x16_f16 v[18:33], v[158:161], v[66:69], v[18:33]
	v_mfma_f32_32x32x16_f16 v[2:17], v[162:165], v[66:69], v[2:17]
	ds_read_b128 v[136:139], v130 offset:28672
	ds_read_b128 v[66:69], v130 offset:17408
	s_waitcnt vmcnt(11) lgkmcnt(4)
	v_mfma_f32_32x32x16_f16 v[50:65], v[122:125], v[102:105], v[50:65]
	ds_read_b128 v[118:121], v130 offset:21504
	s_waitcnt lgkmcnt(4)
	v_mfma_f32_32x32x16_f16 v[34:49], v[126:129], v[102:105], v[34:49]
	ds_read_b128 v[122:125], v130 offset:25600
	s_waitcnt lgkmcnt(4)
	v_mfma_f32_32x32x16_f16 v[18:33], v[132:135], v[102:105], v[18:33]
	s_waitcnt lgkmcnt(3)
	v_mfma_f32_32x32x16_f16 v[2:17], v[136:139], v[102:105], v[2:17]
	ds_read_b128 v[126:129], v130 offset:29696
	s_waitcnt vmcnt(10) lgkmcnt(3)
	v_mfma_f32_32x32x16_f16 v[50:65], v[66:69], v[106:109], v[50:65]
	ds_read_b128 v[66:69], v130 offset:18432
	ds_read_b128 v[102:105], v130 offset:22528
	ds_read_b128 v[150:153], v130 offset:19456
	s_waitcnt lgkmcnt(5)
	v_mfma_f32_32x32x16_f16 v[34:49], v[118:121], v[106:109], v[34:49]
	ds_read_b128 v[118:121], v130 offset:26624
	ds_read_b128 v[154:157], v130 offset:23552
	s_waitcnt lgkmcnt(6)
	v_mfma_f32_32x32x16_f16 v[18:33], v[122:125], v[106:109], v[18:33]
	ds_read_b128 v[158:161], v130 offset:27648
	s_waitcnt lgkmcnt(6)
	v_mfma_f32_32x32x16_f16 v[2:17], v[126:129], v[106:109], v[2:17]
	ds_read_b128 v[106:109], v130 offset:30720
	ds_read_b128 v[162:165], v130 offset:31744
	s_waitcnt vmcnt(9) lgkmcnt(7)
	v_mfma_f32_32x32x16_f16 v[50:65], v[66:69], v[90:93], v[50:65]
	s_waitcnt lgkmcnt(6)
	v_mfma_f32_32x32x16_f16 v[34:49], v[102:105], v[90:93], v[34:49]
	s_waitcnt lgkmcnt(4)
	v_mfma_f32_32x32x16_f16 v[18:33], v[118:121], v[90:93], v[18:33]
	s_waitcnt lgkmcnt(1)
	v_mfma_f32_32x32x16_f16 v[2:17], v[106:109], v[90:93], v[2:17]
	s_waitcnt vmcnt(8)
	v_mfma_f32_32x32x16_f16 v[50:65], v[150:153], v[86:89], v[50:65]
	s_waitcnt lgkmcnt(0)
	s_barrier
	ds_read_b128 v[90:93], v130
	ds_read_b128 v[106:109], v130 offset:4096
	v_mfma_f32_32x32x16_f16 v[34:49], v[154:157], v[86:89], v[34:49]
	ds_read_b128 v[66:69], v130 offset:8192
	v_mfma_f32_32x32x16_f16 v[18:33], v[158:161], v[86:89], v[18:33]
	v_mfma_f32_32x32x16_f16 v[2:17], v[162:165], v[86:89], v[2:17]
	ds_read_b128 v[102:105], v130 offset:12288
	ds_read_b128 v[86:89], v130 offset:1024
	s_waitcnt vmcnt(7) lgkmcnt(4)
	v_mfma_f32_32x32x16_f16 v[50:65], v[90:93], v[94:97], v[50:65]
	ds_read_b128 v[90:93], v130 offset:5120
	s_waitcnt lgkmcnt(4)
	v_mfma_f32_32x32x16_f16 v[34:49], v[106:109], v[94:97], v[34:49]
	ds_read_b128 v[106:109], v130 offset:9216
	s_waitcnt lgkmcnt(4)
	v_mfma_f32_32x32x16_f16 v[18:33], v[66:69], v[94:97], v[18:33]
	s_waitcnt lgkmcnt(3)
	v_mfma_f32_32x32x16_f16 v[2:17], v[102:105], v[94:97], v[2:17]
	ds_read_b128 v[66:69], v130 offset:13312
	ds_read_b128 v[94:97], v130 offset:2048
	s_waitcnt vmcnt(6) lgkmcnt(4)
	v_mfma_f32_32x32x16_f16 v[50:65], v[86:89], v[110:113], v[50:65]
	ds_read_b128 v[86:89], v130 offset:6144
	ds_read_b128 v[150:153], v130 offset:3072
	s_waitcnt lgkmcnt(5)
	v_mfma_f32_32x32x16_f16 v[34:49], v[90:93], v[110:113], v[34:49]
	ds_read_b128 v[90:93], v130 offset:10240
	ds_read_b128 v[154:157], v130 offset:7168
	s_waitcnt lgkmcnt(6)
	v_mfma_f32_32x32x16_f16 v[18:33], v[106:109], v[110:113], v[18:33]
	ds_read_b128 v[158:161], v130 offset:11264
	s_waitcnt lgkmcnt(6)
	v_mfma_f32_32x32x16_f16 v[2:17], v[66:69], v[110:113], v[2:17]
	ds_read_b128 v[102:105], v130 offset:14336
	ds_read_b128 v[162:165], v130 offset:15360
	s_waitcnt vmcnt(5) lgkmcnt(7)
	v_mfma_f32_32x32x16_f16 v[50:65], v[94:97], v[114:117], v[50:65]
	s_waitcnt lgkmcnt(6)
	v_mfma_f32_32x32x16_f16 v[34:49], v[86:89], v[114:117], v[34:49]
	s_waitcnt lgkmcnt(4)
	v_mfma_f32_32x32x16_f16 v[18:33], v[90:93], v[114:117], v[18:33]
	s_waitcnt lgkmcnt(1)
	v_mfma_f32_32x32x16_f16 v[2:17], v[102:105], v[114:117], v[2:17]
	s_waitcnt vmcnt(4)
	v_mfma_f32_32x32x16_f16 v[50:65], v[150:153], v[70:73], v[50:65]
	s_waitcnt lgkmcnt(0)
	s_barrier
	ds_read_b128 v[66:69], v130 offset:16384
	ds_read_b128 v[102:105], v130 offset:20480
	v_mfma_f32_32x32x16_f16 v[34:49], v[154:157], v[70:73], v[34:49]
	ds_read_b128 v[94:97], v130 offset:24576
	v_mfma_f32_32x32x16_f16 v[18:33], v[158:161], v[70:73], v[18:33]
	v_mfma_f32_32x32x16_f16 v[2:17], v[162:165], v[70:73], v[2:17]
	ds_read_b128 v[86:89], v130 offset:28672
	ds_read_b128 v[70:73], v130 offset:17408
	s_waitcnt vmcnt(3) lgkmcnt(4)
	v_mfma_f32_32x32x16_f16 v[50:65], v[66:69], v[74:77], v[50:65]
	ds_read_b128 v[66:69], v130 offset:21504
	s_waitcnt lgkmcnt(4)
	v_mfma_f32_32x32x16_f16 v[34:49], v[102:105], v[74:77], v[34:49]
	ds_read_b128 v[90:93], v130 offset:25600
	s_waitcnt lgkmcnt(4)
	v_mfma_f32_32x32x16_f16 v[18:33], v[94:97], v[74:77], v[18:33]
	s_waitcnt lgkmcnt(3)
	v_mfma_f32_32x32x16_f16 v[2:17], v[86:89], v[74:77], v[2:17]
	ds_read_b128 v[94:97], v130 offset:29696
	ds_read_b128 v[74:77], v130 offset:18432
	s_waitcnt vmcnt(2) lgkmcnt(4)
	v_mfma_f32_32x32x16_f16 v[50:65], v[70:73], v[78:81], v[50:65]
	ds_read_b128 v[70:73], v130 offset:22528
	ds_read_b128 v[150:153], v130 offset:19456
	s_waitcnt lgkmcnt(5)
	v_mfma_f32_32x32x16_f16 v[34:49], v[66:69], v[78:81], v[34:49]
	ds_read_b128 v[66:69], v130 offset:26624
	ds_read_b128 v[154:157], v130 offset:23552
	s_waitcnt lgkmcnt(6)
	v_mfma_f32_32x32x16_f16 v[18:33], v[90:93], v[78:81], v[18:33]
	ds_read_b128 v[158:161], v130 offset:27648
	s_waitcnt lgkmcnt(6)
	v_mfma_f32_32x32x16_f16 v[2:17], v[94:97], v[78:81], v[2:17]
	ds_read_b128 v[86:89], v130 offset:30720
	ds_read_b128 v[162:165], v130 offset:31744
	s_waitcnt vmcnt(1) lgkmcnt(7)
	v_mfma_f32_32x32x16_f16 v[50:65], v[74:77], v[82:85], v[50:65]
	s_waitcnt lgkmcnt(6)
	v_mfma_f32_32x32x16_f16 v[34:49], v[70:73], v[82:85], v[34:49]
	s_waitcnt lgkmcnt(4)
	v_mfma_f32_32x32x16_f16 v[18:33], v[66:69], v[82:85], v[18:33]
	s_waitcnt lgkmcnt(1)
	v_mfma_f32_32x32x16_f16 v[2:17], v[86:89], v[82:85], v[2:17]
	s_waitcnt vmcnt(0)
	v_mfma_f32_32x32x16_f16 v[50:65], v[150:153], v[98:101], v[50:65]
	v_mfma_f32_32x32x16_f16 v[34:49], v[154:157], v[98:101], v[34:49]
	v_mfma_f32_32x32x16_f16 v[18:33], v[158:161], v[98:101], v[18:33]
	s_waitcnt lgkmcnt(0)
	v_mfma_f32_32x32x16_f16 v[2:17], v[162:165], v[98:101], v[2:17]
	v_lshrrev_b32_e32 v66, 1, v0
	v_and_b32_e32 v66, 16, v66
	ds_read_b128 v[68:71], v66 offset:32768
	ds_read_b128 v[72:75], v66 offset:32800
	ds_read_b128 v[76:79], v66 offset:32832
	s_mov_b32 s2, 0x4038aa3b
	s_waitcnt lgkmcnt(1)
	v_pk_fma_f32 v[72:73], v[54:55], s[2:3], v[72:73] op_sel_hi:[1,0,1]
	v_pk_fma_f32 v[68:69], v[50:51], s[2:3], v[68:69] op_sel_hi:[1,0,1]
	v_pk_fma_f32 v[70:71], v[52:53], s[2:3], v[70:71] op_sel_hi:[1,0,1]
	ds_read_b128 v[50:53], v66 offset:32864
	v_exp_f32_e32 v54, v68
	v_exp_f32_e32 v55, v69
	v_pk_fma_f32 v[74:75], v[56:57], s[2:3], v[74:75] op_sel_hi:[1,0,1]
	v_exp_f32_e32 v56, v70
	v_exp_f32_e32 v57, v71
	v_pk_add_f32 v[54:55], v[54:55], 1.0 op_sel_hi:[1,0]
	s_waitcnt lgkmcnt(1)
	v_pk_fma_f32 v[58:59], v[58:59], s[2:3], v[76:77] op_sel_hi:[1,0,1]
	s_waitcnt lgkmcnt(0)
	v_pk_fma_f32 v[76:77], v[62:63], s[2:3], v[50:51] op_sel_hi:[1,0,1]
	v_pk_fma_f32 v[64:65], v[64:65], s[2:3], v[52:53] op_sel_hi:[1,0,1]
	ds_read_b128 v[50:53], v66 offset:33280
	v_rcp_f32_e32 v62, v54
	v_rcp_f32_e32 v63, v55
	v_pk_add_f32 v[54:55], v[56:57], 1.0 op_sel_hi:[1,0]
	v_pk_fma_f32 v[60:61], v[60:61], s[2:3], v[78:79] op_sel_hi:[1,0,1]
	v_rcp_f32_e32 v68, v54
	v_rcp_f32_e32 v69, v55
	v_pk_fma_f32 v[70:71], v[62:63], 2.0, 1.0 op_sel_hi:[1,0,0] neg_lo:[1,0,0] neg_hi:[1,0,0]
	ds_read_b128 v[54:57], v66 offset:33312
	s_waitcnt lgkmcnt(1)
	v_pk_fma_f32 v[70:71], v[50:51], v[70:71], 0 op_sel_hi:[1,1,0]
	v_pk_fma_f32 v[78:79], v[68:69], 2.0, 1.0 op_sel_hi:[1,0,0] neg_lo:[1,0,0] neg_hi:[1,0,0]
	v_pk_fma_f32 v[62:63], v[62:63], v[62:63], v[62:63] neg_lo:[1,0,0] neg_hi:[1,0,0]
	v_pk_mul_f32 v[50:51], v[50:51], 4.0 op_sel_hi:[1,0]
	v_pk_fma_f32 v[70:71], v[52:53], v[78:79], v[70:71]
	v_pk_mul_f32 v[50:51], v[50:51], v[62:63]
	v_pk_mul_f32 v[52:53], v[52:53], 4.0 op_sel_hi:[1,0]
	v_exp_f32_e32 v62, v72
	v_exp_f32_e32 v63, v73
	v_pk_fma_f32 v[68:69], v[68:69], v[68:69], v[68:69] neg_lo:[1,0,0] neg_hi:[1,0,0]
	v_exp_f32_e32 v60, v60
	v_pk_mul_f32 v[52:53], v[52:53], v[68:69]
	v_exp_f32_e32 v68, v74
	v_exp_f32_e32 v69, v75
	v_pk_add_f32 v[62:63], v[62:63], 1.0 op_sel_hi:[1,0]
	v_cvt_pk_f16_f32 v53, v52, v53
	v_rcp_f32_e32 v62, v62
	v_rcp_f32_e32 v63, v63
	v_pk_add_f32 v[68:69], v[68:69], 1.0 op_sel_hi:[1,0]
	v_cvt_pk_f16_f32 v52, v50, v51
	v_rcp_f32_e32 v68, v68
	v_rcp_f32_e32 v69, v69
	v_pk_fma_f32 v[50:51], v[62:63], 2.0, 1.0 op_sel_hi:[1,0,0] neg_lo:[1,0,0] neg_hi:[1,0,0]
	v_pk_fma_f32 v[62:63], v[62:63], v[62:63], v[62:63] neg_lo:[1,0,0] neg_hi:[1,0,0]
	s_waitcnt lgkmcnt(0)
	v_pk_fma_f32 v[50:51], v[54:55], v[50:51], v[70:71]
	v_pk_fma_f32 v[70:71], v[68:69], 2.0, 1.0 op_sel_hi:[1,0,0] neg_lo:[1,0,0] neg_hi:[1,0,0]
	v_pk_mul_f32 v[54:55], v[54:55], 4.0 op_sel_hi:[1,0]
	v_pk_fma_f32 v[50:51], v[56:57], v[70:71], v[50:51]
	v_pk_mul_f32 v[62:63], v[54:55], v[62:63]
	v_pk_mul_f32 v[54:55], v[56:57], 4.0 op_sel_hi:[1,0]
	v_pk_fma_f32 v[56:57], v[68:69], v[68:69], v[68:69] neg_lo:[1,0,0] neg_hi:[1,0,0]
	v_exp_f32_e32 v61, v61
	v_pk_mul_f32 v[54:55], v[54:55], v[56:57]
	v_pk_add_f32 v[60:61], v[60:61], 1.0 op_sel_hi:[1,0]
	v_cvt_pk_f16_f32 v55, v54, v55
	v_cvt_pk_f16_f32 v54, v62, v63
	v_exp_f32_e32 v62, v58
	v_exp_f32_e32 v63, v59
	ds_read_b128 v[56:59], v66 offset:33344
	v_rcp_f32_e32 v70, v60
	v_rcp_f32_e32 v71, v61
	v_pk_add_f32 v[62:63], v[62:63], 1.0 op_sel_hi:[1,0]
	v_permlane32_swap_b32_e32 v52, v54
	v_rcp_f32_e32 v68, v62
	v_rcp_f32_e32 v69, v63
	ds_read_b128 v[60:63], v66 offset:33376
	v_permlane32_swap_b32_e32 v53, v55
	v_pk_fma_f32 v[72:73], v[68:69], 2.0, 1.0 op_sel_hi:[1,0,0] neg_lo:[1,0,0] neg_hi:[1,0,0]
	s_waitcnt lgkmcnt(1)
	v_pk_fma_f32 v[50:51], v[56:57], v[72:73], v[50:51]
	v_pk_fma_f32 v[72:73], v[70:71], 2.0, 1.0 op_sel_hi:[1,0,0] neg_lo:[1,0,0] neg_hi:[1,0,0]
	v_pk_mul_f32 v[56:57], v[56:57], 4.0 op_sel_hi:[1,0]
	v_pk_fma_f32 v[72:73], v[58:59], v[72:73], v[50:51]
	v_pk_fma_f32 v[50:51], v[68:69], v[68:69], v[68:69] neg_lo:[1,0,0] neg_hi:[1,0,0]
	s_nop 0
	v_pk_mul_f32 v[50:51], v[56:57], v[50:51]
	v_pk_mul_f32 v[56:57], v[58:59], 4.0 op_sel_hi:[1,0]
	v_pk_fma_f32 v[58:59], v[70:71], v[70:71], v[70:71] neg_lo:[1,0,0] neg_hi:[1,0,0]
	s_nop 0
	v_pk_mul_f32 v[56:57], v[56:57], v[58:59]
	v_exp_f32_e32 v58, v76
	v_exp_f32_e32 v59, v77
	v_cvt_pk_f16_f32 v57, v56, v57
	v_cvt_pk_f16_f32 v56, v50, v51
	v_exp_f32_e32 v50, v64
	v_exp_f32_e32 v51, v65
	v_pk_add_f32 v[58:59], v[58:59], 1.0 op_sel_hi:[1,0]
	v_pk_add_f32 v[50:51], v[50:51], 1.0 op_sel_hi:[1,0]
	v_rcp_f32_e32 v64, v58
	v_rcp_f32_e32 v65, v59
	v_rcp_f32_e32 v68, v50
	v_rcp_f32_e32 v69, v51
	s_waitcnt lgkmcnt(0)
	v_pk_mul_f32 v[50:51], v[60:61], 4.0 op_sel_hi:[1,0]
	v_pk_fma_f32 v[58:59], v[64:65], v[64:65], v[64:65] neg_lo:[1,0,0] neg_hi:[1,0,0]
	v_pk_fma_f32 v[64:65], v[64:65], 2.0, 1.0 op_sel_hi:[1,0,0] neg_lo:[1,0,0] neg_hi:[1,0,0]
	v_pk_mul_f32 v[70:71], v[50:51], v[58:59]
	v_pk_mul_f32 v[50:51], v[62:63], 4.0 op_sel_hi:[1,0]
	v_pk_fma_f32 v[58:59], v[68:69], v[68:69], v[68:69] neg_lo:[1,0,0] neg_hi:[1,0,0]
	v_pk_fma_f32 v[68:69], v[68:69], 2.0, 1.0 op_sel_hi:[1,0,0] neg_lo:[1,0,0] neg_hi:[1,0,0]
	v_pk_mul_f32 v[50:51], v[50:51], v[58:59]
	v_cvt_pk_f16_f32 v58, v70, v71
	v_cvt_pk_f16_f32 v59, v50, v51
	v_lshl_add_u64 v[50:51], s[4:5], 0, v[130:131]
	s_lshl_b32 s4, s10, 3
	s_add_i32 s4, s4, s3
	s_ashr_i32 s5, s4, 31
	s_lshl_b64 s[12:13], s[4:5], 10
	v_lshl_add_u64 v[70:71], v[50:51], 0, s[12:13]
	s_or_b32 s12, s4, 1
	s_ashr_i32 s13, s12, 31
	s_lshl_b64 s[12:13], s[12:13], 10
	global_store_dwordx4 v[70:71], v[52:55], off sc1
	v_permlane32_swap_b32_e32 v56, v58
	v_permlane32_swap_b32_e32 v57, v59
	v_lshl_add_u64 v[52:53], v[50:51], 0, s[12:13]
	global_store_dwordx4 v[52:53], v[56:59], off sc1
	ds_read_b128 v[52:55], v66 offset:32896
	s_or_b32 s12, s4, 2
	v_pk_fma_f32 v[56:57], v[60:61], v[64:65], v[72:73]
	s_ashr_i32 s13, s12, 31
	v_pk_fma_f32 v[64:65], v[62:63], v[68:69], v[56:57]
	ds_read_b128 v[56:59], v66 offset:33408
	ds_read_b128 v[60:63], v66 offset:32928
	s_waitcnt lgkmcnt(2)
	v_pk_fma_f32 v[34:35], v[34:35], s[2:3], v[52:53] op_sel_hi:[1,0,1]
	v_pk_fma_f32 v[36:37], v[36:37], s[2:3], v[54:55] op_sel_hi:[1,0,1]
	v_exp_f32_e32 v34, v34
	v_exp_f32_e32 v35, v35
	v_exp_f32_e32 v36, v36
	v_exp_f32_e32 v37, v37
	s_waitcnt lgkmcnt(0)
	v_pk_fma_f32 v[38:39], v[38:39], s[2:3], v[60:61] op_sel_hi:[1,0,1]
	v_pk_fma_f32 v[40:41], v[40:41], s[2:3], v[62:63] op_sel_hi:[1,0,1]
	v_exp_f32_e32 v38, v38
	v_exp_f32_e32 v39, v39
	v_pk_add_f32 v[34:35], v[34:35], 1.0 op_sel_hi:[1,0]
	v_exp_f32_e32 v40, v40
	v_exp_f32_e32 v41, v41
	v_rcp_f32_e32 v52, v34
	v_rcp_f32_e32 v53, v35
	v_pk_add_f32 v[34:35], v[36:37], 1.0 op_sel_hi:[1,0]
	v_pk_add_f32 v[38:39], v[38:39], 1.0 op_sel_hi:[1,0]
	v_rcp_f32_e32 v54, v34
	v_rcp_f32_e32 v55, v35
	ds_read_b128 v[34:37], v66 offset:33440
	v_rcp_f32_e32 v38, v38
	v_rcp_f32_e32 v39, v39
	v_pk_add_f32 v[40:41], v[40:41], 1.0 op_sel_hi:[1,0]
	v_pk_fma_f32 v[68:69], v[52:53], 2.0, 1.0 op_sel_hi:[1,0,0] neg_lo:[1,0,0] neg_hi:[1,0,0]
	v_rcp_f32_e32 v40, v40
	v_rcp_f32_e32 v41, v41
	v_pk_fma_f32 v[64:65], v[56:57], v[68:69], v[64:65]
	v_pk_mul_f32 v[56:57], v[56:57], 4.0 op_sel_hi:[1,0]
	v_pk_fma_f32 v[52:53], v[52:53], v[52:53], v[52:53] neg_lo:[1,0,0] neg_hi:[1,0,0]
	v_pk_fma_f32 v[68:69], v[54:55], 2.0, 1.0 op_sel_hi:[1,0,0] neg_lo:[1,0,0] neg_hi:[1,0,0]
	v_pk_mul_f32 v[56:57], v[56:57], v[52:53]
	v_pk_mul_f32 v[52:53], v[58:59], 4.0 op_sel_hi:[1,0]
	v_pk_fma_f32 v[54:55], v[54:55], v[54:55], v[54:55] neg_lo:[1,0,0] neg_hi:[1,0,0]
	v_pk_fma_f32 v[64:65], v[58:59], v[68:69], v[64:65]
	v_pk_mul_f32 v[52:53], v[52:53], v[54:55]
	v_pk_fma_f32 v[54:55], v[38:39], 2.0, 1.0 op_sel_hi:[1,0,0] neg_lo:[1,0,0] neg_hi:[1,0,0]
	v_cvt_pk_f16_f32 v53, v52, v53
	v_cvt_pk_f16_f32 v52, v56, v57
	s_waitcnt lgkmcnt(0)
	v_pk_fma_f32 v[54:55], v[34:35], v[54:55], v[64:65]
	v_pk_fma_f32 v[56:57], v[40:41], 2.0, 1.0 op_sel_hi:[1,0,0] neg_lo:[1,0,0] neg_hi:[1,0,0]
	v_pk_mul_f32 v[34:35], v[34:35], 4.0 op_sel_hi:[1,0]
	v_pk_fma_f32 v[38:39], v[38:39], v[38:39], v[38:39] neg_lo:[1,0,0] neg_hi:[1,0,0]
	v_pk_fma_f32 v[60:61], v[36:37], v[56:57], v[54:55]
	v_pk_mul_f32 v[38:39], v[34:35], v[38:39]
	v_pk_mul_f32 v[54:55], v[36:37], 4.0 op_sel_hi:[1,0]
	ds_read_b128 v[34:37], v66 offset:32960
	v_pk_fma_f32 v[40:41], v[40:41], v[40:41], v[40:41] neg_lo:[1,0,0] neg_hi:[1,0,0]
	ds_read_b128 v[56:59], v66 offset:33472
	v_pk_mul_f32 v[40:41], v[54:55], v[40:41]
	v_cvt_pk_f16_f32 v54, v38, v39
	v_cvt_pk_f16_f32 v55, v40, v41
	ds_read_b128 v[38:41], v66 offset:32992
	s_waitcnt lgkmcnt(2)
	v_pk_fma_f32 v[34:35], v[42:43], s[2:3], v[34:35] op_sel_hi:[1,0,1]
	v_pk_fma_f32 v[36:37], v[44:45], s[2:3], v[36:37] op_sel_hi:[1,0,1]
	v_exp_f32_e32 v34, v34
	v_exp_f32_e32 v35, v35
	v_exp_f32_e32 v36, v36
	v_exp_f32_e32 v37, v37
	s_waitcnt lgkmcnt(0)
	v_pk_fma_f32 v[38:39], v[46:47], s[2:3], v[38:39] op_sel_hi:[1,0,1]
	v_pk_fma_f32 v[40:41], v[48:49], s[2:3], v[40:41] op_sel_hi:[1,0,1]
	v_exp_f32_e32 v38, v38
	v_exp_f32_e32 v39, v39
	v_pk_add_f32 v[34:35], v[34:35], 1.0 op_sel_hi:[1,0]
	v_exp_f32_e32 v40, v40
	v_exp_f32_e32 v41, v41
	v_rcp_f32_e32 v42, v34
	v_rcp_f32_e32 v43, v35
	v_pk_add_f32 v[34:35], v[36:37], 1.0 op_sel_hi:[1,0]
	v_pk_add_f32 v[38:39], v[38:39], 1.0 op_sel_hi:[1,0]
	v_rcp_f32_e32 v44, v34
	v_rcp_f32_e32 v45, v35
	ds_read_b128 v[34:37], v66 offset:33504
	v_rcp_f32_e32 v46, v38
	v_rcp_f32_e32 v47, v39
	v_pk_add_f32 v[38:39], v[40:41], 1.0 op_sel_hi:[1,0]
	v_pk_fma_f32 v[62:63], v[42:43], 2.0, 1.0 op_sel_hi:[1,0,0] neg_lo:[1,0,0] neg_hi:[1,0,0]
	v_rcp_f32_e32 v40, v38
	v_rcp_f32_e32 v41, v39
	v_pk_fma_f32 v[60:61], v[56:57], v[62:63], v[60:61]
	v_pk_fma_f32 v[42:43], v[42:43], v[42:43], v[42:43] neg_lo:[1,0,0] neg_hi:[1,0,0]
	v_pk_mul_f32 v[56:57], v[56:57], 4.0 op_sel_hi:[1,0]
	v_pk_fma_f32 v[62:63], v[44:45], 2.0, 1.0 op_sel_hi:[1,0,0] neg_lo:[1,0,0] neg_hi:[1,0,0]
	v_pk_mul_f32 v[42:43], v[56:57], v[42:43]
	v_pk_mul_f32 v[56:57], v[58:59], 4.0 op_sel_hi:[1,0]
	v_pk_fma_f32 v[44:45], v[44:45], v[44:45], v[44:45] neg_lo:[1,0,0] neg_hi:[1,0,0]
	v_cvt_pk_f16_f32 v38, v42, v43
	v_pk_mul_f32 v[44:45], v[56:57], v[44:45]
	v_pk_fma_f32 v[42:43], v[46:47], 2.0, 1.0 op_sel_hi:[1,0,0] neg_lo:[1,0,0] neg_hi:[1,0,0]
	s_waitcnt lgkmcnt(0)
	v_pk_mul_f32 v[48:49], v[34:35], 4.0 op_sel_hi:[1,0]
	v_pk_fma_f32 v[46:47], v[46:47], v[46:47], v[46:47] neg_lo:[1,0,0] neg_hi:[1,0,0]
	v_cvt_pk_f16_f32 v39, v44, v45
	v_pk_fma_f32 v[44:45], v[40:41], 2.0, 1.0 op_sel_hi:[1,0,0] neg_lo:[1,0,0] neg_hi:[1,0,0]
	v_pk_mul_f32 v[46:47], v[48:49], v[46:47]
	v_pk_mul_f32 v[48:49], v[36:37], 4.0 op_sel_hi:[1,0]
	v_pk_fma_f32 v[40:41], v[40:41], v[40:41], v[40:41] neg_lo:[1,0,0] neg_hi:[1,0,0]
	s_lshl_b64 s[12:13], s[12:13], 10
	v_pk_mul_f32 v[40:41], v[48:49], v[40:41]
	v_permlane32_swap_b32_e32 v52, v54
	v_cvt_pk_f16_f32 v41, v40, v41
	v_cvt_pk_f16_f32 v40, v46, v47
	v_lshl_add_u64 v[46:47], v[50:51], 0, s[12:13]
	s_or_b32 s12, s4, 3
	s_ashr_i32 s13, s12, 31
	v_permlane32_swap_b32_e32 v53, v55
	s_lshl_b64 s[12:13], s[12:13], 10
	global_store_dwordx4 v[46:47], v[52:55], off sc1
	v_permlane32_swap_b32_e32 v38, v40
	v_permlane32_swap_b32_e32 v39, v41
	v_lshl_add_u64 v[46:47], v[50:51], 0, s[12:13]
	global_store_dwordx4 v[46:47], v[38:41], off sc1
	ds_read_b128 v[38:41], v66 offset:33024
	v_pk_fma_f32 v[60:61], v[58:59], v[62:63], v[60:61]
	s_or_b32 s12, s4, 4
	v_pk_fma_f32 v[34:35], v[34:35], v[42:43], v[60:61]
	s_ashr_i32 s13, s12, 31
	v_pk_fma_f32 v[46:47], v[36:37], v[44:45], v[34:35]
	ds_read_b128 v[34:37], v66 offset:33056
	ds_read_b128 v[42:45], v66 offset:33536
	s_waitcnt lgkmcnt(2)
	v_pk_fma_f32 v[18:19], v[18:19], s[2:3], v[38:39] op_sel_hi:[1,0,1]
	v_pk_fma_f32 v[20:21], v[20:21], s[2:3], v[40:41] op_sel_hi:[1,0,1]
	v_exp_f32_e32 v18, v18
	v_exp_f32_e32 v19, v19
	v_exp_f32_e32 v20, v20
	v_exp_f32_e32 v21, v21
	s_waitcnt lgkmcnt(1)
	v_pk_fma_f32 v[22:23], v[22:23], s[2:3], v[34:35] op_sel_hi:[1,0,1]
	v_pk_fma_f32 v[24:25], v[24:25], s[2:3], v[36:37] op_sel_hi:[1,0,1]
	v_exp_f32_e32 v22, v22
	v_exp_f32_e32 v23, v23
	v_exp_f32_e32 v24, v24
	v_exp_f32_e32 v25, v25
	v_pk_add_f32 v[18:19], v[18:19], 1.0 op_sel_hi:[1,0]
	v_pk_add_f32 v[22:23], v[22:23], 1.0 op_sel_hi:[1,0]
	v_rcp_f32_e32 v38, v18
	v_rcp_f32_e32 v39, v19
	v_pk_add_f32 v[18:19], v[20:21], 1.0 op_sel_hi:[1,0]
	v_rcp_f32_e32 v22, v22
	v_rcp_f32_e32 v40, v18
	v_rcp_f32_e32 v41, v19
	ds_read_b128 v[18:21], v66 offset:33568
	v_rcp_f32_e32 v23, v23
	v_pk_add_f32 v[24:25], v[24:25], 1.0 op_sel_hi:[1,0]
	v_pk_fma_f32 v[48:49], v[38:39], 2.0, 1.0 op_sel_hi:[1,0,0] neg_lo:[1,0,0] neg_hi:[1,0,0]
	v_rcp_f32_e32 v24, v24
	v_rcp_f32_e32 v25, v25
	s_waitcnt lgkmcnt(1)
	v_pk_fma_f32 v[46:47], v[42:43], v[48:49], v[46:47]
	v_pk_fma_f32 v[48:49], v[40:41], 2.0, 1.0 op_sel_hi:[1,0,0] neg_lo:[1,0,0] neg_hi:[1,0,0]
	v_pk_mul_f32 v[42:43], v[42:43], 4.0 op_sel_hi:[1,0]
	v_pk_fma_f32 v[38:39], v[38:39], v[38:39], v[38:39] neg_lo:[1,0,0] neg_hi:[1,0,0]
	v_pk_fma_f32 v[46:47], v[44:45], v[48:49], v[46:47]
	v_pk_mul_f32 v[42:43], v[42:43], v[38:39]
	v_pk_mul_f32 v[38:39], v[44:45], 4.0 op_sel_hi:[1,0]
	v_pk_fma_f32 v[40:41], v[40:41], v[40:41], v[40:41] neg_lo:[1,0,0] neg_hi:[1,0,0]
	v_pk_fma_f32 v[34:35], v[22:23], 2.0, 1.0 op_sel_hi:[1,0,0] neg_lo:[1,0,0] neg_hi:[1,0,0]
	v_pk_mul_f32 v[38:39], v[38:39], v[40:41]
	s_waitcnt lgkmcnt(0)
	v_pk_fma_f32 v[34:35], v[18:19], v[34:35], v[46:47]
	v_pk_fma_f32 v[36:37], v[24:25], 2.0, 1.0 op_sel_hi:[1,0,0] neg_lo:[1,0,0] neg_hi:[1,0,0]
	v_pk_mul_f32 v[18:19], v[18:19], 4.0 op_sel_hi:[1,0]
	v_pk_fma_f32 v[22:23], v[22:23], v[22:23], v[22:23] neg_lo:[1,0,0] neg_hi:[1,0,0]
	v_cvt_pk_f16_f32 v39, v38, v39
	v_cvt_pk_f16_f32 v38, v42, v43
	v_pk_fma_f32 v[42:43], v[20:21], v[36:37], v[34:35]
	v_pk_mul_f32 v[22:23], v[18:19], v[22:23]
	v_pk_mul_f32 v[18:19], v[20:21], 4.0 op_sel_hi:[1,0]
	v_pk_fma_f32 v[20:21], v[24:25], v[24:25], v[24:25] neg_lo:[1,0,0] neg_hi:[1,0,0]
	v_cvt_pk_f16_f32 v40, v22, v23
	v_pk_mul_f32 v[24:25], v[18:19], v[20:21]
	ds_read_b128 v[18:21], v66 offset:33088
	v_cvt_pk_f16_f32 v41, v24, v25
	ds_read_b128 v[22:25], v66 offset:33600
	ds_read_b128 v[34:37], v66 offset:33120
	s_lshl_b64 s[12:13], s[12:13], 10
	v_permlane32_swap_b32_e32 v38, v40
	s_waitcnt lgkmcnt(2)
	v_pk_fma_f32 v[18:19], v[26:27], s[2:3], v[18:19] op_sel_hi:[1,0,1]
	v_pk_fma_f32 v[20:21], v[28:29], s[2:3], v[20:21] op_sel_hi:[1,0,1]
	v_exp_f32_e32 v18, v18
	v_exp_f32_e32 v19, v19
	v_exp_f32_e32 v20, v20
	v_exp_f32_e32 v21, v21
	v_permlane32_swap_b32_e32 v39, v41
	v_pk_add_f32 v[18:19], v[18:19], 1.0 op_sel_hi:[1,0]
	s_nop 0
	v_rcp_f32_e32 v26, v18
	v_rcp_f32_e32 v27, v19
	v_pk_add_f32 v[18:19], v[20:21], 1.0 op_sel_hi:[1,0]
	v_pk_fma_f32 v[44:45], v[26:27], 2.0, 1.0 op_sel_hi:[1,0,0] neg_lo:[1,0,0] neg_hi:[1,0,0]
	v_rcp_f32_e32 v28, v18
	v_rcp_f32_e32 v29, v19
	s_waitcnt lgkmcnt(1)
	v_pk_fma_f32 v[42:43], v[22:23], v[44:45], v[42:43]
	v_pk_mul_f32 v[22:23], v[22:23], 4.0 op_sel_hi:[1,0]
	v_pk_fma_f32 v[26:27], v[26:27], v[26:27], v[26:27] neg_lo:[1,0,0] neg_hi:[1,0,0]
	v_pk_fma_f32 v[44:45], v[28:29], 2.0, 1.0 op_sel_hi:[1,0,0] neg_lo:[1,0,0] neg_hi:[1,0,0]
	v_pk_mul_f32 v[26:27], v[22:23], v[26:27]
	v_pk_fma_f32 v[42:43], v[24:25], v[44:45], v[42:43]
	v_pk_mul_f32 v[22:23], v[24:25], 4.0 op_sel_hi:[1,0]
	v_pk_fma_f32 v[24:25], v[28:29], v[28:29], v[28:29] neg_lo:[1,0,0] neg_hi:[1,0,0]
	s_waitcnt lgkmcnt(0)
	v_pk_fma_f32 v[28:29], v[32:33], s[2:3], v[36:37] op_sel_hi:[1,0,1]
	v_pk_mul_f32 v[22:23], v[22:23], v[24:25]
	v_pk_fma_f32 v[24:25], v[30:31], s[2:3], v[34:35] op_sel_hi:[1,0,1]
	v_exp_f32_e32 v28, v28
	v_exp_f32_e32 v24, v24
	v_exp_f32_e32 v25, v25
	v_exp_f32_e32 v29, v29
	ds_read_b128 v[18:21], v66 offset:33632
	v_cvt_pk_f16_f32 v23, v22, v23
	v_pk_add_f32 v[24:25], v[24:25], 1.0 op_sel_hi:[1,0]
	v_pk_add_f32 v[28:29], v[28:29], 1.0 op_sel_hi:[1,0]
	v_rcp_f32_e32 v24, v24
	v_rcp_f32_e32 v25, v25
	v_rcp_f32_e32 v28, v28
	v_rcp_f32_e32 v29, v29
	v_cvt_pk_f16_f32 v22, v26, v27
	v_pk_fma_f32 v[26:27], v[24:25], 2.0, 1.0 op_sel_hi:[1,0,0] neg_lo:[1,0,0] neg_hi:[1,0,0]
	s_waitcnt lgkmcnt(0)
	v_pk_mul_f32 v[32:33], v[18:19], 4.0 op_sel_hi:[1,0]
	v_pk_fma_f32 v[24:25], v[24:25], v[24:25], v[24:25] neg_lo:[1,0,0] neg_hi:[1,0,0]
	v_pk_fma_f32 v[30:31], v[28:29], 2.0, 1.0 op_sel_hi:[1,0,0] neg_lo:[1,0,0] neg_hi:[1,0,0]
	v_pk_mul_f32 v[32:33], v[32:33], v[24:25]
	v_pk_mul_f32 v[24:25], v[20:21], 4.0 op_sel_hi:[1,0]
	v_pk_fma_f32 v[28:29], v[28:29], v[28:29], v[28:29] neg_lo:[1,0,0] neg_hi:[1,0,0]
	v_pk_fma_f32 v[18:19], v[18:19], v[26:27], v[42:43]
	v_pk_mul_f32 v[24:25], v[24:25], v[28:29]
	v_lshl_add_u64 v[28:29], v[50:51], 0, s[12:13]
	s_or_b32 s12, s4, 5
	s_ashr_i32 s13, s12, 31
	v_cvt_pk_f16_f32 v25, v24, v25
	v_cvt_pk_f16_f32 v24, v32, v33
	s_lshl_b64 s[12:13], s[12:13], 10
	global_store_dwordx4 v[28:29], v[38:41], off sc1
	v_permlane32_swap_b32_e32 v22, v24
	v_permlane32_swap_b32_e32 v23, v25
	v_lshl_add_u64 v[28:29], v[50:51], 0, s[12:13]
	global_store_dwordx4 v[28:29], v[22:25], off sc1
	ds_read_b128 v[22:25], v66 offset:33152
	v_pk_fma_f32 v[30:31], v[20:21], v[30:31], v[18:19]
	ds_read_b128 v[18:21], v66 offset:33184
	ds_read_b128 v[26:29], v66 offset:33664
	s_waitcnt lgkmcnt(2)
	v_pk_fma_f32 v[2:3], v[2:3], s[2:3], v[22:23] op_sel_hi:[1,0,1]
	s_nop 0
	v_exp_f32_e32 v2, v2
	v_exp_f32_e32 v3, v3
	v_pk_fma_f32 v[4:5], v[4:5], s[2:3], v[24:25] op_sel_hi:[1,0,1]
	s_waitcnt lgkmcnt(1)
	v_pk_fma_f32 v[6:7], v[6:7], s[2:3], v[18:19] op_sel_hi:[1,0,1]
	v_exp_f32_e32 v4, v4
	v_exp_f32_e32 v5, v5
	v_exp_f32_e32 v6, v6
	v_exp_f32_e32 v7, v7
	v_pk_fma_f32 v[8:9], v[8:9], s[2:3], v[20:21] op_sel_hi:[1,0,1]
	v_pk_add_f32 v[2:3], v[2:3], 1.0 op_sel_hi:[1,0]
	v_exp_f32_e32 v8, v8
	v_exp_f32_e32 v9, v9
	v_rcp_f32_e32 v22, v2
	v_rcp_f32_e32 v23, v3
	v_pk_add_f32 v[2:3], v[4:5], 1.0 op_sel_hi:[1,0]
	v_pk_add_f32 v[6:7], v[6:7], 1.0 op_sel_hi:[1,0]
	v_rcp_f32_e32 v24, v2
	v_rcp_f32_e32 v25, v3
	ds_read_b128 v[2:5], v66 offset:33696
	v_rcp_f32_e32 v6, v6
	v_rcp_f32_e32 v7, v7
	v_pk_add_f32 v[8:9], v[8:9], 1.0 op_sel_hi:[1,0]
	v_pk_fma_f32 v[32:33], v[22:23], 2.0, 1.0 op_sel_hi:[1,0,0] neg_lo:[1,0,0] neg_hi:[1,0,0]
	v_rcp_f32_e32 v8, v8
	v_rcp_f32_e32 v9, v9
	s_waitcnt lgkmcnt(1)
	v_pk_fma_f32 v[30:31], v[26:27], v[32:33], v[30:31]
	v_pk_fma_f32 v[32:33], v[24:25], 2.0, 1.0 op_sel_hi:[1,0,0] neg_lo:[1,0,0] neg_hi:[1,0,0]
	v_pk_mul_f32 v[26:27], v[26:27], 4.0 op_sel_hi:[1,0]
	v_pk_fma_f32 v[22:23], v[22:23], v[22:23], v[22:23] neg_lo:[1,0,0] neg_hi:[1,0,0]
	v_pk_fma_f32 v[30:31], v[28:29], v[32:33], v[30:31]
	v_pk_mul_f32 v[26:27], v[26:27], v[22:23]
	v_pk_mul_f32 v[22:23], v[28:29], 4.0 op_sel_hi:[1,0]
	v_pk_fma_f32 v[24:25], v[24:25], v[24:25], v[24:25] neg_lo:[1,0,0] neg_hi:[1,0,0]
	v_pk_fma_f32 v[18:19], v[6:7], 2.0, 1.0 op_sel_hi:[1,0,0] neg_lo:[1,0,0] neg_hi:[1,0,0]
	v_pk_mul_f32 v[22:23], v[22:23], v[24:25]
	s_waitcnt lgkmcnt(0)
	v_pk_fma_f32 v[18:19], v[2:3], v[18:19], v[30:31]
	v_pk_fma_f32 v[20:21], v[8:9], 2.0, 1.0 op_sel_hi:[1,0,0] neg_lo:[1,0,0] neg_hi:[1,0,0]
	v_pk_mul_f32 v[2:3], v[2:3], 4.0 op_sel_hi:[1,0]
	v_pk_fma_f32 v[6:7], v[6:7], v[6:7], v[6:7] neg_lo:[1,0,0] neg_hi:[1,0,0]
	v_cvt_pk_f16_f32 v23, v22, v23
	v_cvt_pk_f16_f32 v22, v26, v27
	v_pk_fma_f32 v[26:27], v[4:5], v[20:21], v[18:19]
	v_pk_mul_f32 v[6:7], v[2:3], v[6:7]
	v_pk_mul_f32 v[2:3], v[4:5], 4.0 op_sel_hi:[1,0]
	v_pk_fma_f32 v[4:5], v[8:9], v[8:9], v[8:9] neg_lo:[1,0,0] neg_hi:[1,0,0]
	v_cvt_pk_f16_f32 v24, v6, v7
	v_pk_mul_f32 v[8:9], v[2:3], v[4:5]
	ds_read_b128 v[2:5], v66 offset:33216
	v_cvt_pk_f16_f32 v25, v8, v9
	ds_read_b128 v[6:9], v66 offset:33728
	ds_read_b128 v[18:21], v66 offset:33248
	v_permlane32_swap_b32_e32 v22, v24
	s_waitcnt lgkmcnt(2)
	v_pk_fma_f32 v[2:3], v[10:11], s[2:3], v[2:3] op_sel_hi:[1,0,1]
	v_pk_fma_f32 v[4:5], v[12:13], s[2:3], v[4:5] op_sel_hi:[1,0,1]
	v_exp_f32_e32 v2, v2
	v_exp_f32_e32 v3, v3
	v_exp_f32_e32 v4, v4
	v_exp_f32_e32 v5, v5
	v_permlane32_swap_b32_e32 v23, v25
	v_pk_add_f32 v[2:3], v[2:3], 1.0 op_sel_hi:[1,0]
	s_nop 0
	v_rcp_f32_e32 v10, v2
	v_rcp_f32_e32 v11, v3
	v_pk_add_f32 v[2:3], v[4:5], 1.0 op_sel_hi:[1,0]
	v_pk_fma_f32 v[28:29], v[10:11], 2.0, 1.0 op_sel_hi:[1,0,0] neg_lo:[1,0,0] neg_hi:[1,0,0]
	v_rcp_f32_e32 v12, v2
	v_rcp_f32_e32 v13, v3
	s_waitcnt lgkmcnt(1)
	v_pk_fma_f32 v[26:27], v[6:7], v[28:29], v[26:27]
	v_pk_mul_f32 v[6:7], v[6:7], 4.0 op_sel_hi:[1,0]
	v_pk_fma_f32 v[10:11], v[10:11], v[10:11], v[10:11] neg_lo:[1,0,0] neg_hi:[1,0,0]
	v_pk_fma_f32 v[28:29], v[12:13], 2.0, 1.0 op_sel_hi:[1,0,0] neg_lo:[1,0,0] neg_hi:[1,0,0]
	v_pk_mul_f32 v[10:11], v[6:7], v[10:11]
	v_pk_fma_f32 v[26:27], v[8:9], v[28:29], v[26:27]
	v_pk_mul_f32 v[6:7], v[8:9], 4.0 op_sel_hi:[1,0]
	v_pk_fma_f32 v[8:9], v[12:13], v[12:13], v[12:13] neg_lo:[1,0,0] neg_hi:[1,0,0]
	s_waitcnt lgkmcnt(0)
	v_pk_fma_f32 v[12:13], v[16:17], s[2:3], v[20:21] op_sel_hi:[1,0,1]
	v_pk_mul_f32 v[6:7], v[6:7], v[8:9]
	v_pk_fma_f32 v[8:9], v[14:15], s[2:3], v[18:19] op_sel_hi:[1,0,1]
	v_exp_f32_e32 v12, v12
	v_exp_f32_e32 v8, v8
	v_exp_f32_e32 v9, v9
	v_exp_f32_e32 v13, v13
	ds_read_b128 v[2:5], v66 offset:33760
	v_cvt_pk_f16_f32 v7, v6, v7
	v_pk_add_f32 v[8:9], v[8:9], 1.0 op_sel_hi:[1,0]
	v_pk_add_f32 v[12:13], v[12:13], 1.0 op_sel_hi:[1,0]
	v_rcp_f32_e32 v8, v8
	v_rcp_f32_e32 v9, v9
	v_rcp_f32_e32 v12, v12
	v_rcp_f32_e32 v13, v13
	v_cvt_pk_f16_f32 v6, v10, v11
	v_pk_fma_f32 v[10:11], v[8:9], 2.0, 1.0 op_sel_hi:[1,0,0] neg_lo:[1,0,0] neg_hi:[1,0,0]
	s_waitcnt lgkmcnt(0)
	v_pk_mul_f32 v[16:17], v[2:3], 4.0 op_sel_hi:[1,0]
	v_pk_fma_f32 v[14:15], v[12:13], 2.0, 1.0 op_sel_hi:[1,0,0] neg_lo:[1,0,0] neg_hi:[1,0,0]
	v_pk_fma_f32 v[2:3], v[2:3], v[10:11], v[26:27]
	v_pk_fma_f32 v[8:9], v[8:9], v[8:9], v[8:9] neg_lo:[1,0,0] neg_hi:[1,0,0]
	v_pk_fma_f32 v[2:3], v[4:5], v[14:15], v[2:3]
	v_pk_mul_f32 v[16:17], v[16:17], v[8:9]
	v_add_f32_e32 v2, v2, v3
	v_mbcnt_lo_u32_b32 v3, -1, 0
	v_mbcnt_hi_u32_b32 v3, -1, v3
	v_pk_mul_f32 v[8:9], v[4:5], 4.0 op_sel_hi:[1,0]
	v_and_b32_e32 v5, 64, v3
	v_xor_b32_e32 v4, 32, v3
	v_add_u32_e32 v5, 64, v5
	v_cmp_lt_i32_e32 vcc, v4, v5
	s_or_b32 s2, s4, 6
	s_ashr_i32 s3, s2, 31
	v_cndmask_b32_e32 v3, v3, v4, vcc
	v_lshlrev_b32_e32 v3, 2, v3
	v_pk_fma_f32 v[12:13], v[12:13], v[12:13], v[12:13] neg_lo:[1,0,0] neg_hi:[1,0,0]
	s_lshl_b64 s[2:3], s[2:3], 10
	ds_bpermute_b32 v3, v3, v2
	v_pk_mul_f32 v[8:9], v[8:9], v[12:13]
	v_lshl_add_u64 v[12:13], v[50:51], 0, s[2:3]
	s_or_b32 s2, s4, 7
	s_ashr_i32 s3, s2, 31
	v_cvt_pk_f16_f32 v9, v8, v9
	v_cvt_pk_f16_f32 v8, v16, v17
	s_lshl_b64 s[2:3], s[2:3], 10
	s_nop 0
	v_permlane32_swap_b32_e32 v6, v8
	v_permlane32_swap_b32_e32 v7, v9
	v_lshl_add_u64 v[4:5], v[50:51], 0, s[2:3]
	v_cmp_gt_u32_e32 vcc, 32, v1
	global_store_dwordx4 v[12:13], v[22:25], off sc1
	global_store_dwordx4 v[4:5], v[6:9], off sc1
	s_and_saveexec_b64 s[2:3], vcc
	s_cbranch_execz .LBB2_5
	s_load_dwordx2 s[4:5], s[0:1], 0x30
	s_lshl_b32 s7, s10, 12
	s_lshl_b32 s6, s6, 7
	s_or_b32 s6, s6, s7
	s_lshl_b32 s7, s8, 5
	s_or_b32 s6, s7, s6
	s_waitcnt lgkmcnt(0)
	v_add_f32_e32 v4, v2, v3
	v_or_b32_e32 v2, s6, v1
	v_ashrrev_i32_e32 v3, 31, v2
	v_lshl_add_u64 v[2:3], v[2:3], 2, s[4:5]
	global_store_dword v[2:3], v4, off sc1

.LBB2_6:
	s_load_dwordx2 s[2:3], s[0:1], 0x0
	s_load_dwordx4 s[4:7], s[0:1], 0x10
	s_lshl_b32 s0, s10, 8
	s_lshl_b32 s1, s9, 7
	s_add_i32 s0, s1, s0
	s_ashr_i32 s1, s0, 31
	s_lshl_b64 s[0:1], s[0:1], 10
	s_waitcnt lgkmcnt(0)
	s_add_u32 s0, s2, s0
	s_addc_u32 s1, s3, s1
	v_mov_b32_e32 v131, 0
	v_lshl_add_u64 v[2:3], s[0:1], 0, v[130:131]
	global_load_dwordx4 v[4:7], v130, s[0:1]
	global_load_dwordx4 v[8:11], v130, s[0:1] offset:1024
	global_load_dwordx4 v[12:15], v130, s[0:1] offset:2048
	global_load_dwordx4 v[16:19], v130, s[0:1] offset:3072
	s_mov_b32 s0, 0x10000
	v_add_co_u32_e32 v36, vcc, s0, v2
	s_mov_b32 s0, 0x11000
	s_nop 0
	v_addc_co_u32_e32 v37, vcc, 0, v3, vcc
	v_add_co_u32_e32 v80, vcc, s0, v2
	s_lshl_b32 s0, s10, 7
	s_ashr_i32 s1, s0, 31
	v_mov_b32_e32 v1, v131
	v_lshl_add_u64 v[32:33], s[0:1], 0, v[0:1]
	v_lshlrev_b64 v[32:33], 2, v[32:33]
	v_addc_co_u32_e32 v81, vcc, 0, v3, vcc
	v_lshl_add_u64 v[34:35], s[4:5], 0, v[32:33]
	global_load_dwordx4 v[20:23], v[80:81], off offset:-4096
	global_load_dwordx4 v[24:27], v[36:37], off offset:1024
	global_load_dwordx4 v[28:31], v[36:37], off offset:2048
	global_load_dword v1, v[34:35], off offset:-1024
	v_lshl_add_u64 v[38:39], s[6:7], 0, v[32:33]
	global_load_dword v102, v[38:39], off offset:-1024
	global_load_dwordx4 v[32:35], v[36:37], off offset:3072
	s_movk_i32 s1, 0x2000
	v_add_co_u32_e32 v82, vcc, s1, v2
	s_movk_i32 s0, 0x1000
	s_nop 0
	v_addc_co_u32_e32 v83, vcc, 0, v3, vcc
	global_load_dwordx4 v[36:39], v[82:83], off offset:-4096
	v_add_co_u32_e32 v84, vcc, s0, v2
	s_mov_b32 s1, 0x13000
	s_nop 0
	v_addc_co_u32_e32 v85, vcc, 0, v3, vcc
	global_load_dwordx4 v[40:43], v[84:85], off offset:1024
	global_load_dwordx4 v[44:47], v[84:85], off offset:2048
	global_load_dwordx4 v[48:51], v[84:85], off offset:3072
	global_load_dwordx4 v[52:55], v[80:81], off
	global_load_dwordx4 v[56:59], v[80:81], off offset:1024
	global_load_dwordx4 v[60:63], v[80:81], off offset:2048
	global_load_dwordx4 v[64:67], v[80:81], off offset:3072
	global_load_dwordx4 v[68:71], v[82:83], off
	global_load_dwordx4 v[72:75], v[82:83], off offset:1024
	global_load_dwordx4 v[76:79], v[82:83], off offset:2048
	v_add_co_u32_e32 v100, vcc, s1, v2
	s_mov_b32 s0, 0x12000
	global_load_dwordx4 v[80:83], v[82:83], off offset:3072
	v_addc_co_u32_e32 v101, vcc, 0, v3, vcc
	global_load_dwordx4 v[84:87], v[100:101], off offset:-4096
	v_add_co_u32_e32 v96, vcc, s0, v2
	v_lshlrev_b32_e32 v0, 2, v0
	s_nop 0
	v_addc_co_u32_e32 v97, vcc, 0, v3, vcc
	global_load_dwordx4 v[88:91], v[96:97], off offset:1024
	global_load_dwordx4 v[92:95], v[96:97], off offset:2048
	v_lshl_or_b32 v103, s9, 13, v130
	global_load_dwordx4 v[96:99], v[96:97], off offset:3072
	s_movk_i32 s1, 0x4000
	s_movk_i32 s0, 0x3000
	s_mov_b32 s2, 0x15000
	s_waitcnt vmcnt(25)
	ds_write_b128 v103, v[4:7]
	s_waitcnt vmcnt(24)
	ds_write_b128 v103, v[8:11] offset:1024
	s_waitcnt vmcnt(23)
	ds_write_b128 v103, v[12:15] offset:2048
	s_waitcnt vmcnt(22)
	ds_write_b128 v103, v[16:19] offset:3072
	s_waitcnt vmcnt(21)
	ds_write_b128 v103, v[20:23] offset:4096
	s_waitcnt vmcnt(20)
	ds_write_b128 v103, v[24:27] offset:5120
	s_waitcnt vmcnt(19)
	ds_write_b128 v103, v[28:31] offset:6144
	s_waitcnt vmcnt(18)
	v_mul_f32_e32 v1, 0x4038aa3b, v1
	s_waitcnt vmcnt(17)
	ds_write2st64_b32 v0, v1, v102 offset0:124 offset1:126
	s_waitcnt vmcnt(16)
	ds_write_b128 v103, v[32:35] offset:7168
	v_add_co_u32_e32 v102, vcc, s1, v2
	s_waitcnt lgkmcnt(0)
	s_nop 0
	v_addc_co_u32_e32 v103, vcc, 0, v3, vcc
	v_add_co_u32_e32 v0, vcc, s0, v2
	s_barrier
	s_nop 0
	v_addc_co_u32_e32 v1, vcc, 0, v3, vcc
	global_load_dwordx4 v[4:7], v[102:103], off offset:-4096
	global_load_dwordx4 v[8:11], v[0:1], off offset:1024
	global_load_dwordx4 v[12:15], v[0:1], off offset:2048
	global_load_dwordx4 v[16:19], v[0:1], off offset:3072
	global_load_dwordx4 v[20:23], v[100:101], off
	global_load_dwordx4 v[24:27], v[100:101], off offset:1024
	global_load_dwordx4 v[28:31], v[100:101], off offset:2048
	global_load_dwordx4 v[32:35], v[100:101], off offset:3072
	s_lshl_b32 s0, s8, 13
	s_and_b32 s0, s0, 0x6000
	v_or_b32_e32 v0, s0, v130
	s_mov_b32 s1, 0x14000
	s_waitcnt vmcnt(23)
	ds_write_b128 v0, v[36:39] offset:16384
	s_waitcnt vmcnt(22)
	ds_write_b128 v0, v[40:43] offset:17408
	s_waitcnt vmcnt(21)
	ds_write_b128 v0, v[44:47] offset:18432
	s_waitcnt vmcnt(20)
	ds_write_b128 v0, v[48:51] offset:19456
	s_waitcnt vmcnt(19)
	ds_write_b128 v0, v[52:55] offset:20480
	s_waitcnt vmcnt(18)
	ds_write_b128 v0, v[56:59] offset:21504
	s_waitcnt vmcnt(17)
	ds_write_b128 v0, v[60:63] offset:22528
	s_waitcnt vmcnt(16)
	ds_write_b128 v0, v[64:67] offset:23552
	s_waitcnt lgkmcnt(0)
	s_barrier
	s_waitcnt vmcnt(15)
	ds_write_b128 v0, v[68:71]
	v_add_co_u32_e32 v68, vcc, s1, v2
	s_waitcnt vmcnt(14)
	ds_write_b128 v0, v[72:75] offset:1024
	v_addc_co_u32_e32 v69, vcc, 0, v3, vcc
	v_add_co_u32_e32 v100, vcc, s2, v2
	s_movk_i32 s0, 0x6000
	global_load_dwordx4 v[36:39], v[102:103], off
	global_load_dwordx4 v[40:43], v[102:103], off offset:1024
	global_load_dwordx4 v[44:47], v[102:103], off offset:2048
	s_waitcnt vmcnt(16)
	ds_write_b128 v0, v[76:79] offset:2048
	v_addc_co_u32_e32 v101, vcc, 0, v3, vcc
	s_waitcnt vmcnt(15)
	ds_write_b128 v0, v[80:83] offset:3072
	global_load_dwordx4 v[48:51], v[102:103], off offset:3072
	global_load_dwordx4 v[52:55], v[100:101], off offset:-4096
	s_waitcnt vmcnt(16)
	ds_write_b128 v0, v[84:87] offset:4096
	v_add_co_u32_e32 v102, vcc, s0, v2
	global_load_dwordx4 v[56:59], v[68:69], off offset:1024
	global_load_dwordx4 v[60:63], v[68:69], off offset:2048
	global_load_dwordx4 v[64:67], v[68:69], off offset:3072
	v_addc_co_u32_e32 v103, vcc, 0, v3, vcc
	s_waitcnt vmcnt(18)
	ds_write_b128 v0, v[88:91] offset:5120
	s_waitcnt vmcnt(17)
	ds_write_b128 v0, v[92:95] offset:6144
	s_waitcnt vmcnt(16)
	ds_write_b128 v0, v[96:99] offset:7168
	s_waitcnt lgkmcnt(0)
	s_barrier
	global_load_dwordx4 v[68:71], v[102:103], off offset:-4096
	s_movk_i32 s1, 0x5000
	v_add_co_u32_e32 v104, vcc, s1, v2
	s_mov_b32 s1, 0x17000
	s_nop 0
	v_addc_co_u32_e32 v105, vcc, 0, v3, vcc
	global_load_dwordx4 v[72:75], v[104:105], off offset:1024
	global_load_dwordx4 v[76:79], v[104:105], off offset:2048
	global_load_dwordx4 v[80:83], v[104:105], off offset:3072
	global_load_dwordx4 v[84:87], v[100:101], off
	global_load_dwordx4 v[88:91], v[100:101], off offset:1024
	global_load_dwordx4 v[92:95], v[100:101], off offset:2048
	global_load_dwordx4 v[96:99], v[100:101], off offset:3072
	v_add_co_u32_e32 v100, vcc, s1, v2
	s_mov_b32 s0, 0x16000
	s_nop 0
	v_addc_co_u32_e32 v101, vcc, 0, v3, vcc
	s_mov_b32 s1, 0x8000
	s_mov_b32 s2, 0xb000
	s_waitcnt vmcnt(23)
	ds_write_b128 v0, v[4:7] offset:16384
	s_waitcnt vmcnt(22)
	ds_write_b128 v0, v[8:11] offset:17408
	s_waitcnt vmcnt(21)
	ds_write_b128 v0, v[12:15] offset:18432
	s_waitcnt vmcnt(20)
	ds_write_b128 v0, v[16:19] offset:19456
	s_waitcnt vmcnt(19)
	ds_write_b128 v0, v[20:23] offset:20480
	s_waitcnt vmcnt(18)
	ds_write_b128 v0, v[24:27] offset:21504
	s_waitcnt vmcnt(17)
	ds_write_b128 v0, v[28:31] offset:22528
	s_waitcnt vmcnt(16)
	ds_write_b128 v0, v[32:35] offset:23552
	s_waitcnt lgkmcnt(0)
	s_barrier
	global_load_dwordx4 v[4:7], v[102:103], off
	global_load_dwordx4 v[8:11], v[102:103], off offset:1024
	global_load_dwordx4 v[12:15], v[102:103], off offset:2048
	global_load_dwordx4 v[16:19], v[102:103], off offset:3072
	global_load_dwordx4 v[20:23], v[100:101], off offset:-4096
	v_add_co_u32_e32 v102, vcc, s0, v2
	s_movk_i32 s0, 0x7000
	s_nop 0
	v_addc_co_u32_e32 v103, vcc, 0, v3, vcc
	global_load_dwordx4 v[24:27], v[102:103], off offset:1024
	global_load_dwordx4 v[28:31], v[102:103], off offset:2048
	global_load_dwordx4 v[32:35], v[102:103], off offset:3072
	v_add_co_u32_e32 v102, vcc, s1, v2
	s_waitcnt vmcnt(23)
	ds_write_b128 v0, v[36:39]
	s_waitcnt vmcnt(22)
	ds_write_b128 v0, v[40:43] offset:1024
	s_waitcnt vmcnt(21)
	ds_write_b128 v0, v[44:47] offset:2048
	s_waitcnt vmcnt(20)
	ds_write_b128 v0, v[48:51] offset:3072
	s_waitcnt vmcnt(19)
	ds_write_b128 v0, v[52:55] offset:4096
	s_waitcnt vmcnt(18)
	ds_write_b128 v0, v[56:59] offset:5120
	s_waitcnt vmcnt(17)
	ds_write_b128 v0, v[60:63] offset:6144
	s_waitcnt vmcnt(16)
	ds_write_b128 v0, v[64:67] offset:7168
	v_addc_co_u32_e32 v103, vcc, 0, v3, vcc
	v_add_co_u32_e32 v56, vcc, s0, v2
	s_waitcnt lgkmcnt(0)
	s_barrier
	global_load_dwordx4 v[36:39], v[102:103], off offset:-4096
	s_waitcnt vmcnt(16)
	ds_write_b128 v0, v[68:71] offset:16384
	v_addc_co_u32_e32 v57, vcc, 0, v3, vcc
	s_waitcnt vmcnt(15)
	ds_write_b128 v0, v[72:75] offset:17408
	s_waitcnt vmcnt(14)
	ds_write_b128 v0, v[76:79] offset:18432
	global_load_dwordx4 v[40:43], v[56:57], off offset:1024
	global_load_dwordx4 v[44:47], v[56:57], off offset:2048
	s_waitcnt vmcnt(15)
	ds_write_b128 v0, v[80:83] offset:19456
	global_load_dwordx4 v[48:51], v[56:57], off offset:3072
	global_load_dwordx4 v[52:55], v[100:101], off
	s_waitcnt vmcnt(16)
	ds_write_b128 v0, v[84:87] offset:20480
	s_waitcnt vmcnt(15)
	ds_write_b128 v0, v[88:91] offset:21504
	global_load_dwordx4 v[56:59], v[100:101], off offset:1024
	global_load_dwordx4 v[60:63], v[100:101], off offset:2048
	s_mov_b32 s0, 0x18000
	v_add_co_u32_e32 v84, vcc, s0, v2
	s_waitcnt vmcnt(16)
	ds_write_b128 v0, v[92:95] offset:22528
	global_load_dwordx4 v[64:67], v[100:101], off offset:3072
	s_waitcnt vmcnt(16)
	ds_write_b128 v0, v[96:99] offset:23552
	s_waitcnt lgkmcnt(0)
	s_barrier
	global_load_dwordx4 v[68:71], v[102:103], off
	global_load_dwordx4 v[72:75], v[102:103], off offset:1024
	s_mov_b32 s1, 0x19000
	v_addc_co_u32_e32 v85, vcc, 0, v3, vcc
	global_load_dwordx4 v[76:79], v[102:103], off offset:2048
	global_load_dwordx4 v[80:83], v[102:103], off offset:3072
	v_add_co_u32_e32 v100, vcc, s1, v2
	s_waitcnt vmcnt(19)
	ds_write_b128 v0, v[4:7]
	s_waitcnt vmcnt(18)
	ds_write_b128 v0, v[8:11] offset:1024
	v_addc_co_u32_e32 v101, vcc, 0, v3, vcc
	s_mov_b32 s1, 0xa000
	global_load_dwordx4 v[4:7], v[100:101], off offset:-4096
	global_load_dwordx4 v[8:11], v[84:85], off offset:1024
	s_waitcnt vmcnt(19)
	ds_write_b128 v0, v[12:15] offset:2048
	s_waitcnt vmcnt(18)
	ds_write_b128 v0, v[16:19] offset:3072
	s_waitcnt vmcnt(17)
	ds_write_b128 v0, v[20:23] offset:4096
	v_add_co_u32_e32 v102, vcc, s1, v2
	global_load_dwordx4 v[12:15], v[84:85], off offset:2048
	s_waitcnt vmcnt(17)
	ds_write_b128 v0, v[24:27] offset:5120
	s_waitcnt vmcnt(16)
	ds_write_b128 v0, v[28:31] offset:6144
	v_addc_co_u32_e32 v103, vcc, 0, v3, vcc
	global_load_dwordx4 v[16:19], v[84:85], off offset:3072
	s_waitcnt vmcnt(16)
	ds_write_b128 v0, v[32:35] offset:7168
	s_waitcnt lgkmcnt(0)
	s_barrier
	global_load_dwordx4 v[20:23], v[102:103], off offset:-4096
	s_mov_b32 s0, 0x9000
	v_add_co_u32_e32 v104, vcc, s0, v2
	s_mov_b32 s0, 0x1a000
	s_nop 0
	v_addc_co_u32_e32 v105, vcc, 0, v3, vcc
	global_load_dwordx4 v[24:27], v[104:105], off offset:1024
	global_load_dwordx4 v[28:31], v[104:105], off offset:2048
	global_load_dwordx4 v[32:35], v[104:105], off offset:3072
	global_load_dwordx4 v[84:87], v[100:101], off
	global_load_dwordx4 v[88:91], v[100:101], off offset:1024
	global_load_dwordx4 v[92:95], v[100:101], off offset:2048
	global_load_dwordx4 v[96:99], v[100:101], off offset:3072
	s_waitcnt vmcnt(23)
	ds_write_b128 v0, v[36:39] offset:16384
	s_waitcnt vmcnt(22)
	ds_write_b128 v0, v[40:43] offset:17408
	s_waitcnt vmcnt(21)
	ds_write_b128 v0, v[44:47] offset:18432
	s_waitcnt vmcnt(20)
	ds_write_b128 v0, v[48:51] offset:19456
	s_waitcnt vmcnt(19)
	ds_write_b128 v0, v[52:55] offset:20480
	s_waitcnt vmcnt(18)
	ds_write_b128 v0, v[56:59] offset:21504
	s_waitcnt vmcnt(17)
	ds_write_b128 v0, v[60:63] offset:22528
	s_waitcnt vmcnt(16)
	ds_write_b128 v0, v[64:67] offset:23552
	v_add_co_u32_e32 v56, vcc, s0, v2
	s_mov_b32 s1, 0x1b000
	s_nop 0
	v_addc_co_u32_e32 v57, vcc, 0, v3, vcc
	v_add_co_u32_e32 v64, vcc, s1, v2
	s_waitcnt lgkmcnt(0)
	s_barrier
	s_waitcnt vmcnt(15)
	ds_write_b128 v0, v[68:71]
	s_waitcnt vmcnt(14)
	ds_write_b128 v0, v[72:75] offset:1024
	v_addc_co_u32_e32 v65, vcc, 0, v3, vcc
	s_mov_b32 s0, 0xc000
	global_load_dwordx4 v[36:39], v[102:103], off offset:1024
	global_load_dwordx4 v[40:43], v[102:103], off offset:2048
	s_waitcnt vmcnt(14)
	ds_write_b128 v0, v[80:83] offset:3072
	v_add_co_u32_e32 v80, vcc, s0, v2
	ds_write_b128 v0, v[76:79] offset:2048
	s_nop 0
	v_addc_co_u32_e32 v81, vcc, 0, v3, vcc
	global_load_dwordx4 v[44:47], v[102:103], off offset:3072
	global_load_dwordx4 v[48:51], v[64:65], off offset:-4096
	v_add_co_u32_e32 v66, vcc, s2, v2
	s_mov_b32 s0, 0x1c000
	s_nop 0
	v_addc_co_u32_e32 v67, vcc, 0, v3, vcc
	v_add_co_u32_e32 v100, vcc, s0, v2
	s_mov_b32 s0, 0x1d000
	s_nop 0
	v_addc_co_u32_e32 v101, vcc, 0, v3, vcc
	s_mov_b32 s1, 0xe000
	s_waitcnt vmcnt(15)
	ds_write_b128 v0, v[4:7] offset:4096
	s_waitcnt vmcnt(14)
	ds_write_b128 v0, v[8:11] offset:5120
	global_load_dwordx4 v[4:7], v[56:57], off offset:1024
	global_load_dwordx4 v[8:11], v[56:57], off offset:2048
	s_waitcnt vmcnt(15)
	ds_write_b128 v0, v[12:15] offset:6144
	global_load_dwordx4 v[12:15], v[102:103], off
	global_load_dwordx4 v[52:55], v[56:57], off offset:3072
	v_add_co_u32_e32 v102, vcc, s0, v2
	s_waitcnt vmcnt(16)
	ds_write_b128 v0, v[16:19] offset:7168
	s_waitcnt lgkmcnt(0)
	s_barrier
	global_load_dwordx4 v[16:19], v[80:81], off offset:-4096
	global_load_dwordx4 v[56:59], v[66:67], off offset:1024
	global_load_dwordx4 v[60:63], v[66:67], off offset:2048
	s_waitcnt vmcnt(18)
	ds_write_b128 v0, v[20:23] offset:16384
	s_waitcnt vmcnt(17)
	ds_write_b128 v0, v[24:27] offset:17408
	global_load_dwordx4 v[20:23], v[66:67], off offset:3072
	s_waitcnt vmcnt(17)
	ds_write_b128 v0, v[28:31] offset:18432
	s_waitcnt vmcnt(16)
	ds_write_b128 v0, v[32:35] offset:19456
	global_load_dwordx4 v[24:27], v[64:65], off
	global_load_dwordx4 v[28:31], v[64:65], off offset:1024
	s_waitcnt vmcnt(17)
	ds_write_b128 v0, v[84:87] offset:20480
	s_waitcnt vmcnt(16)
	ds_write_b128 v0, v[88:91] offset:21504
	global_load_dwordx4 v[32:35], v[64:65], off offset:2048
	s_waitcnt vmcnt(16)
	ds_write_b128 v0, v[92:95] offset:22528
	global_load_dwordx4 v[64:67], v[64:65], off offset:3072
	s_waitcnt vmcnt(16)
	ds_write_b128 v0, v[96:99] offset:23552
	s_waitcnt lgkmcnt(0)
	s_barrier
	global_load_dwordx4 v[68:71], v[80:81], off
	global_load_dwordx4 v[72:75], v[80:81], off offset:1024
	global_load_dwordx4 v[76:79], v[80:81], off offset:2048
	v_addc_co_u32_e32 v103, vcc, 0, v3, vcc
	global_load_dwordx4 v[80:83], v[80:81], off offset:3072
	s_nop 0
	global_load_dwordx4 v[84:87], v[102:103], off offset:-4096
	global_load_dwordx4 v[88:91], v[100:101], off offset:1024
	global_load_dwordx4 v[92:95], v[100:101], off offset:2048
	global_load_dwordx4 v[96:99], v[100:101], off offset:3072
	v_add_co_u32_e32 v100, vcc, s1, v2
	s_mov_b32 s0, 0xd000
	s_nop 0
	v_addc_co_u32_e32 v101, vcc, 0, v3, vcc
	v_add_co_u32_e32 v104, vcc, s0, v2
	s_mov_b32 s0, 0x1e000
	s_nop 0
	v_addc_co_u32_e32 v105, vcc, 0, v3, vcc
	s_waitcnt vmcnt(17)
	ds_write_b128 v0, v[12:15]
	ds_write_b128 v0, v[36:39] offset:1024
	ds_write_b128 v0, v[40:43] offset:2048
	ds_write_b128 v0, v[44:47] offset:3072
	ds_write_b128 v0, v[48:51] offset:4096
	ds_write_b128 v0, v[4:7] offset:5120
	ds_write_b128 v0, v[8:11] offset:6144
	s_waitcnt vmcnt(16)
	ds_write_b128 v0, v[52:55] offset:7168
	s_waitcnt lgkmcnt(0)
	s_barrier
	s_waitcnt vmcnt(15)
	ds_write_b128 v0, v[16:19] offset:16384
	s_waitcnt vmcnt(14)
	ds_write_b128 v0, v[56:59] offset:17408
	s_waitcnt vmcnt(13)
	ds_write_b128 v0, v[60:63] offset:18432
	global_load_dwordx4 v[4:7], v[104:105], off offset:1024
	global_load_dwordx4 v[8:11], v[104:105], off offset:2048
	s_waitcnt vmcnt(14)
	ds_write_b128 v0, v[20:23] offset:19456
	global_load_dwordx4 v[12:15], v[104:105], off offset:3072
	global_load_dwordx4 v[16:19], v[102:103], off
	s_waitcnt vmcnt(15)
	ds_write_b128 v0, v[24:27] offset:20480
	s_waitcnt vmcnt(14)
	ds_write_b128 v0, v[28:31] offset:21504
	global_load_dwordx4 v[20:23], v[102:103], off offset:1024
	global_load_dwordx4 v[24:27], v[102:103], off offset:2048
	s_waitcnt vmcnt(15)
	ds_write_b128 v0, v[32:35] offset:22528
	global_load_dwordx4 v[28:31], v[100:101], off offset:-4096
	global_load_dwordx4 v[32:35], v[102:103], off offset:3072
	s_waitcnt vmcnt(16)
	ds_write_b128 v0, v[64:67] offset:23552
	s_waitcnt lgkmcnt(0)
	s_barrier
	s_waitcnt vmcnt(15)
	ds_write_b128 v0, v[68:71]
	v_add_co_u32_e32 v68, vcc, s0, v2
	s_mov_b32 s0, 0x1f000
	s_nop 0
	v_addc_co_u32_e32 v69, vcc, 0, v3, vcc
	v_add_co_u32_e32 v102, vcc, s0, v2
	global_load_dwordx4 v[36:39], v[100:101], off offset:1024
	global_load_dwordx4 v[40:43], v[100:101], off offset:2048
	s_waitcnt vmcnt(16)
	ds_write_b128 v0, v[72:75] offset:1024
	v_addc_co_u32_e32 v103, vcc, 0, v3, vcc
	s_waitcnt vmcnt(15)
	ds_write_b128 v0, v[76:79] offset:2048
	s_waitcnt vmcnt(14)
	ds_write_b128 v0, v[80:83] offset:3072
	s_mov_b32 s0, 0xf000
	global_load_dwordx4 v[44:47], v[100:101], off offset:3072
	global_load_dwordx4 v[48:51], v[102:103], off offset:-4096
	s_waitcnt vmcnt(15)
	ds_write_b128 v0, v[84:87] offset:4096
	s_waitcnt vmcnt(14)
	ds_write_b128 v0, v[88:91] offset:5120
	v_add_co_u32_e32 v2, vcc, s0, v2
	global_load_dwordx4 v[52:55], v[68:69], off offset:1024
	global_load_dwordx4 v[56:59], v[68:69], off offset:2048
	s_waitcnt vmcnt(15)
	ds_write_b128 v0, v[92:95] offset:6144
	v_addc_co_u32_e32 v3, vcc, 0, v3, vcc
	global_load_dwordx4 v[60:63], v[100:101], off
	global_load_dwordx4 v[64:67], v[68:69], off offset:3072
	s_waitcnt vmcnt(16)
	ds_write_b128 v0, v[96:99] offset:7168
	s_waitcnt lgkmcnt(0)
	s_barrier
	global_load_dwordx4 v[68:71], v[2:3], off
	global_load_dwordx4 v[72:75], v[2:3], off offset:1024
	global_load_dwordx4 v[76:79], v[2:3], off offset:2048
	global_load_dwordx4 v[80:83], v[2:3], off offset:3072
	global_load_dwordx4 v[84:87], v[102:103], off
	global_load_dwordx4 v[88:91], v[102:103], off offset:1024
	global_load_dwordx4 v[92:95], v[102:103], off offset:2048
	global_load_dwordx4 v[96:99], v[102:103], off offset:3072
	s_waitcnt vmcnt(17)
	ds_write_b128 v0, v[28:31] offset:16384
	ds_write_b128 v0, v[4:7] offset:17408
	ds_write_b128 v0, v[8:11] offset:18432
	ds_write_b128 v0, v[12:15] offset:19456
	ds_write_b128 v0, v[16:19] offset:20480
	ds_write_b128 v0, v[20:23] offset:21504
	ds_write_b128 v0, v[24:27] offset:22528
	s_waitcnt vmcnt(16)
	ds_write_b128 v0, v[32:35] offset:23552
	s_waitcnt lgkmcnt(0)
	s_barrier
	s_waitcnt vmcnt(9)
	ds_write_b128 v0, v[60:63]
	ds_write_b128 v0, v[36:39] offset:1024
	ds_write_b128 v0, v[40:43] offset:2048
	ds_write_b128 v0, v[44:47] offset:3072
	ds_write_b128 v0, v[48:51] offset:4096
	ds_write_b128 v0, v[52:55] offset:5120
	ds_write_b128 v0, v[56:59] offset:6144
	s_waitcnt vmcnt(8)
	ds_write_b128 v0, v[64:67] offset:7168
	s_waitcnt lgkmcnt(0)
	s_barrier
	s_waitcnt vmcnt(7)
	ds_write_b128 v0, v[68:71] offset:16384
	s_waitcnt vmcnt(6)
	ds_write_b128 v0, v[72:75] offset:17408
	s_waitcnt vmcnt(5)
	ds_write_b128 v0, v[76:79] offset:18432
	s_waitcnt vmcnt(4)
	ds_write_b128 v0, v[80:83] offset:19456
	s_waitcnt vmcnt(3)
	ds_write_b128 v0, v[84:87] offset:20480
	s_waitcnt vmcnt(2)
	ds_write_b128 v0, v[88:91] offset:21504
	s_waitcnt vmcnt(1)
	ds_write_b128 v0, v[92:95] offset:22528
	s_waitcnt vmcnt(0)
	ds_write_b128 v0, v[96:99] offset:23552
	s_waitcnt lgkmcnt(0)
	s_barrier
	s_endpgm
	s_nop 0
	s_nop 0
	s_nop 0
	s_nop 0
	s_nop 0
	s_nop 0
	s_nop 0
	s_nop 0
	s_nop 0
	s_nop 0
	s_nop 0
	s_nop 0
	s_nop 0
	s_nop 0
	s_nop 0
	s_nop 0
	s_nop 0
	s_nop 0
	s_nop 0
	s_nop 0
	s_nop 0
	s_nop 0
	s_nop 0
	s_nop 0
	s_nop 0
	s_nop 0
	s_nop 0
	s_nop 0
	s_nop 0
	s_nop 0
	s_nop 0
	s_endpgm

	.amdhsa_kernel _Z6k_gemmILi0EEvPKDF16_S1_PKfS3_S1_PDF16_PfS1_S5_
		.amdhsa_group_segment_fixed_size 33808
		.amdhsa_private_segment_fixed_size 0
		.amdhsa_kernarg_size 72
		.amdhsa_user_sgpr_count 2
		.amdhsa_user_sgpr_dispatch_ptr 0
		.amdhsa_user_sgpr_queue_ptr 0
		.amdhsa_user_sgpr_kernarg_segment_ptr 1
		.amdhsa_user_sgpr_dispatch_id 0
		.amdhsa_user_sgpr_kernarg_preload_length 0
		.amdhsa_user_sgpr_kernarg_preload_offset 0
		.amdhsa_user_sgpr_private_segment_size 0
		.amdhsa_uses_dynamic_stack 0
		.amdhsa_enable_private_segment 0
		.amdhsa_system_sgpr_workgroup_id_x 1
		.amdhsa_system_sgpr_workgroup_id_y 0
		.amdhsa_system_sgpr_workgroup_id_z 0
		.amdhsa_system_sgpr_workgroup_info 0
		.amdhsa_system_vgpr_workitem_id 0
		.amdhsa_next_free_vgpr 166
		.amdhsa_next_free_sgpr 91
		.amdhsa_accum_offset 168
		.amdhsa_reserve_vcc 1
		.amdhsa_float_round_mode_32 0
		.amdhsa_float_round_mode_16_64 0
		.amdhsa_float_denorm_mode_32 3
		.amdhsa_float_denorm_mode_16_64 3
		.amdhsa_dx10_clamp 1
		.amdhsa_ieee_mode 1
		.amdhsa_fp16_overflow 0
		.amdhsa_tg_split 0
		.amdhsa_exception_fp_ieee_invalid_op 0
		.amdhsa_exception_fp_denorm_src 0
		.amdhsa_exception_fp_ieee_div_zero 0
		.amdhsa_exception_fp_ieee_overflow 0
		.amdhsa_exception_fp_ieee_underflow 0
		.amdhsa_exception_fp_ieee_inexact 0
		.amdhsa_exception_int_div_zero 0
	.end_amdhsa_kernel

.LBB3_3:
	s_lshl_b32 s3, s2, 2
	s_and_b32 s3, s3, 28
	s_bfe_u32 s2, s2, 0x20003
	s_load_dwordx2 s[10:11], s[0:1], 0x8
	s_load_dwordx2 s[12:13], s[0:1], 0x20
	s_or_b32 s2, s3, s2
	s_lshl_b32 s2, s2, 2
	s_or_b32 s6, s5, s2
	s_lshl_b32 s2, s6, 16
	s_waitcnt lgkmcnt(0)
	s_add_u32 s2, s10, s2
	s_addc_u32 s3, s11, 0
	v_lshl_add_u64 v[168:169], s[2:3], 0, v[134:135]
	s_movk_i32 s7, 0x1000
	v_add_co_u32_e32 v6, vcc, s7, v168
	s_movk_i32 s7, 0x2000
	s_nop 0
	v_addc_co_u32_e32 v7, vcc, 0, v169, vcc
	v_add_co_u32_e32 v8, vcc, s7, v168
	global_load_dwordx4 v[90:93], v134, s[2:3] offset:1024
	global_load_dwordx4 v[102:105], v134, s[2:3] offset:2048
	v_addc_co_u32_e32 v9, vcc, 0, v169, vcc
	global_load_dwordx4 v[106:109], v134, s[2:3] offset:3072
	global_load_dwordx4 v[94:97], v[8:9], off offset:-4096
	global_load_dwordx4 v[98:101], v[6:7], off offset:1024
	global_load_dwordx4 v[86:89], v[6:7], off offset:2048
	global_load_dwordx4 v[2:5], v134, s[2:3]
	global_load_dwordx4 v[82:85], v[6:7], off offset:3072
	global_load_dwordx4 v[78:81], v[8:9], off
	global_load_dwordx4 v[74:77], v[8:9], off offset:1024
	global_load_dwordx4 v[70:73], v[8:9], off offset:2048
	global_load_dwordx4 v[66:69], v[8:9], off offset:3072
	s_barrier
	ds_read_b128 v[6:9], v134
	ds_read_b128 v[10:13], v134 offset:4096
	ds_read_b128 v[14:17], v134 offset:8192
	ds_read_b128 v[110:113], v134 offset:12288
	s_load_dwordx2 s[2:3], s[0:1], 0x40
	s_lshl_b32 s7, s6, 6
	v_and_b32_e32 v1, 31, v0
	s_lshl_b32 s9, s4, 3
	v_lshrrev_b32_e32 v18, 2, v0
	s_add_i32 s10, s9, s7
	v_and_b32_e32 v18, 8, v18
	v_mov_b32_e32 v19, v135
	s_ashr_i32 s11, s10, 31
	v_lshl_add_u64 v[18:19], s[12:13], 0, v[18:19]
	s_lshl_b64 s[12:13], s[10:11], 10
	v_lshlrev_b32_e32 v1, 4, v1
	v_or_b32_e32 v20, s12, v1
	s_or_b32 s12, s10, 1
	v_mov_b32_e32 v21, s13
	s_ashr_i32 s13, s12, 31
	s_lshl_b64 s[12:13], s[12:13], 10
	v_or_b32_e32 v22, s12, v1
	s_or_b32 s12, s10, 2
	v_mov_b32_e32 v23, s13
	s_ashr_i32 s13, s12, 31
	v_lshl_add_u64 v[20:21], v[18:19], 0, v[20:21]
	s_lshl_b64 s[12:13], s[12:13], 10
	v_lshl_add_u64 v[22:23], v[18:19], 0, v[22:23]
	global_load_dwordx2 v[166:167], v[20:21], off
	global_load_dwordx2 v[164:165], v[20:21], off offset:512
	global_load_dwordx2 v[162:163], v[22:23], off
	global_load_dwordx2 v[160:161], v[22:23], off offset:512
	v_or_b32_e32 v20, s12, v1
	s_or_b32 s12, s10, 3
	v_mov_b32_e32 v21, s13
	s_ashr_i32 s13, s12, 31
	s_lshl_b64 s[12:13], s[12:13], 10
	v_or_b32_e32 v22, s12, v1
	s_or_b32 s12, s10, 4
	v_mov_b32_e32 v23, s13
	s_ashr_i32 s13, s12, 31
	v_lshl_add_u64 v[20:21], v[18:19], 0, v[20:21]
	s_lshl_b64 s[12:13], s[12:13], 10
	v_lshl_add_u64 v[22:23], v[18:19], 0, v[22:23]
	global_load_dwordx2 v[158:159], v[20:21], off
	global_load_dwordx2 v[156:157], v[20:21], off offset:512
	global_load_dwordx2 v[154:155], v[22:23], off
	global_load_dwordx2 v[152:153], v[22:23], off offset:512
	v_or_b32_e32 v20, s12, v1
	s_or_b32 s12, s10, 5
	v_mov_b32_e32 v21, s13
	s_ashr_i32 s13, s12, 31
	s_lshl_b64 s[12:13], s[12:13], 10
	v_or_b32_e32 v22, s12, v1
	s_or_b32 s12, s10, 6
	v_mov_b32_e32 v23, s13
	s_ashr_i32 s13, s12, 31
	s_or_b32 s10, s10, 7
	v_lshl_add_u64 v[20:21], v[18:19], 0, v[20:21]
	s_lshl_b64 s[12:13], s[12:13], 10
	s_ashr_i32 s11, s10, 31
	v_lshl_add_u64 v[22:23], v[18:19], 0, v[22:23]
	global_load_dwordx2 v[150:151], v[20:21], off
	global_load_dwordx2 v[148:149], v[20:21], off offset:512
	global_load_dwordx2 v[146:147], v[22:23], off
	global_load_dwordx2 v[144:145], v[22:23], off offset:512
	v_or_b32_e32 v20, s12, v1
	v_mov_b32_e32 v21, s13
	s_lshl_b64 s[10:11], s[10:11], 10
	v_lshl_add_u64 v[20:21], v[18:19], 0, v[20:21]
	v_or_b32_e32 v22, s10, v1
	v_mov_b32_e32 v23, s11
	v_lshl_add_u64 v[18:19], v[18:19], 0, v[22:23]
	global_load_dwordx2 v[142:143], v[20:21], off
	global_load_dwordx2 v[140:141], v[20:21], off offset:512
	global_load_dwordx2 v[138:139], v[18:19], off
	global_load_dwordx2 v[136:137], v[18:19], off offset:512
	s_lshl_b32 s7, s4, 7
	ds_read_b128 v[118:121], v134 offset:1024
	s_waitcnt vmcnt(21) lgkmcnt(0)
	v_mfma_f32_32x32x16_f16 v[50:65], v[6:9], v[2:5], 0
	s_movk_i32 s9, 0x4000
	v_add_co_u32_e32 v178, vcc, s9, v168
	ds_read_b128 v[122:125], v134 offset:5120
	s_nop 0
	v_addc_co_u32_e32 v179, vcc, 0, v169, vcc
	global_load_dwordx4 v[114:117], v[178:179], off offset:-4096
	s_movk_i32 s9, 0x3000
	v_add_co_u32_e32 v180, vcc, s9, v168
	v_mfma_f32_32x32x16_f16 v[34:49], v[10:13], v[2:5], 0
	s_nop 0
	v_addc_co_u32_e32 v181, vcc, 0, v169, vcc
	ds_read_b128 v[126:129], v134 offset:9216
	v_mfma_f32_32x32x16_f16 v[18:33], v[14:17], v[2:5], 0
	ds_read_b128 v[130:133], v134 offset:13312
	v_mfma_f32_32x32x16_f16 v[2:17], v[110:113], v[2:5], 0
	ds_read_b128 v[110:113], v134 offset:2048
	v_mfma_f32_32x32x16_f16 v[50:65], v[118:121], v[90:93], v[50:65]
	ds_read_b128 v[182:185], v134 offset:3072
	global_load_dwordx4 v[118:121], v[180:181], off offset:1024
	ds_read_b128 v[170:173], v134 offset:6144
	s_waitcnt lgkmcnt(5)
	v_mfma_f32_32x32x16_f16 v[34:49], v[122:125], v[90:93], v[34:49]
	ds_read_b128 v[174:177], v134 offset:10240
	ds_read_b128 v[186:189], v134 offset:7168
	s_waitcnt lgkmcnt(6)
	v_mfma_f32_32x32x16_f16 v[18:33], v[126:129], v[90:93], v[18:33]
	ds_read_b128 v[126:129], v134 offset:14336
	ds_read_b128 v[190:193], v134 offset:11264
	s_waitcnt lgkmcnt(7)
	v_mfma_f32_32x32x16_f16 v[2:17], v[130:133], v[90:93], v[2:17]
	ds_read_b128 v[194:197], v134 offset:15360
	s_waitcnt lgkmcnt(7)
	v_mfma_f32_32x32x16_f16 v[50:65], v[110:113], v[102:105], v[50:65]
	global_load_dwordx4 v[122:125], v[180:181], off offset:2048
	s_waitcnt lgkmcnt(5)
	v_mfma_f32_32x32x16_f16 v[34:49], v[170:173], v[102:105], v[34:49]
	s_waitcnt lgkmcnt(4)
	v_mfma_f32_32x32x16_f16 v[18:33], v[174:177], v[102:105], v[18:33]
	s_waitcnt lgkmcnt(2)
	v_mfma_f32_32x32x16_f16 v[2:17], v[126:129], v[102:105], v[2:17]
	global_load_dwordx4 v[102:105], v[180:181], off offset:3072
	v_mfma_f32_32x32x16_f16 v[50:65], v[182:185], v[106:109], v[50:65]
	s_waitcnt lgkmcnt(0)
	s_barrier
	ds_read_b128 v[90:93], v134 offset:16384
	ds_read_b128 v[126:129], v134 offset:20480
	v_mfma_f32_32x32x16_f16 v[34:49], v[186:189], v[106:109], v[34:49]
	ds_read_b128 v[110:113], v134 offset:24576
	v_mfma_f32_32x32x16_f16 v[18:33], v[190:193], v[106:109], v[18:33]
	ds_read_b128 v[130:133], v134 offset:28672
	v_mfma_f32_32x32x16_f16 v[2:17], v[194:197], v[106:109], v[2:17]
	ds_read_b128 v[106:109], v134 offset:17408
	s_waitcnt lgkmcnt(4)
	v_mfma_f32_32x32x16_f16 v[50:65], v[90:93], v[94:97], v[50:65]
	global_load_dwordx4 v[90:93], v[178:179], off
	ds_read_b128 v[170:173], v134 offset:21504
	s_waitcnt lgkmcnt(4)
	v_mfma_f32_32x32x16_f16 v[34:49], v[126:129], v[94:97], v[34:49]
	ds_read_b128 v[126:129], v134 offset:25600
	s_waitcnt lgkmcnt(4)
	v_mfma_f32_32x32x16_f16 v[18:33], v[110:113], v[94:97], v[18:33]
	ds_read_b128 v[110:113], v134 offset:29696
	s_waitcnt lgkmcnt(4)
	v_mfma_f32_32x32x16_f16 v[2:17], v[130:133], v[94:97], v[2:17]
	ds_read_b128 v[130:133], v134 offset:18432
	s_waitcnt lgkmcnt(4)
	v_mfma_f32_32x32x16_f16 v[50:65], v[106:109], v[98:101], v[50:65]
	ds_read_b128 v[182:185], v134 offset:19456
	global_load_dwordx4 v[94:97], v[178:179], off offset:1024
	ds_read_b128 v[106:109], v134 offset:22528
	s_waitcnt lgkmcnt(5)
	v_mfma_f32_32x32x16_f16 v[34:49], v[170:173], v[98:101], v[34:49]
	ds_read_b128 v[170:173], v134 offset:26624
	ds_read_b128 v[186:189], v134 offset:23552
	s_waitcnt lgkmcnt(6)
	v_mfma_f32_32x32x16_f16 v[18:33], v[126:129], v[98:101], v[18:33]
	ds_read_b128 v[126:129], v134 offset:30720
	ds_read_b128 v[190:193], v134 offset:27648
	s_waitcnt lgkmcnt(7)
	v_mfma_f32_32x32x16_f16 v[2:17], v[110:113], v[98:101], v[2:17]
	ds_read_b128 v[194:197], v134 offset:31744
	s_waitcnt lgkmcnt(7)
	v_mfma_f32_32x32x16_f16 v[50:65], v[130:133], v[86:89], v[50:65]
	global_load_dwordx4 v[98:101], v[178:179], off offset:2048
	s_waitcnt lgkmcnt(5)
	v_mfma_f32_32x32x16_f16 v[34:49], v[106:109], v[86:89], v[34:49]
	s_waitcnt lgkmcnt(4)
	v_mfma_f32_32x32x16_f16 v[18:33], v[170:173], v[86:89], v[18:33]
	s_waitcnt lgkmcnt(2)
	v_mfma_f32_32x32x16_f16 v[2:17], v[126:129], v[86:89], v[2:17]
	global_load_dwordx4 v[86:89], v[178:179], off offset:3072
	s_waitcnt vmcnt(28)
	v_mfma_f32_32x32x16_f16 v[50:65], v[182:185], v[82:85], v[50:65]
	s_waitcnt lgkmcnt(0)
	s_barrier
	ds_read_b128 v[110:113], v134
	ds_read_b128 v[126:129], v134 offset:4096
	v_mfma_f32_32x32x16_f16 v[34:49], v[186:189], v[82:85], v[34:49]
	ds_read_b128 v[130:133], v134 offset:8192
	v_mfma_f32_32x32x16_f16 v[18:33], v[190:193], v[82:85], v[18:33]
	ds_read_b128 v[106:109], v134 offset:12288
	v_mfma_f32_32x32x16_f16 v[2:17], v[194:197], v[82:85], v[2:17]
	ds_read_b128 v[82:85], v134 offset:1024
	s_waitcnt vmcnt(27) lgkmcnt(4)
	v_mfma_f32_32x32x16_f16 v[50:65], v[110:113], v[78:81], v[50:65]
	s_movk_i32 s9, 0x6000
	v_add_co_u32_e32 v178, vcc, s9, v168
	ds_read_b128 v[170:173], v134 offset:5120
	s_nop 0
	v_addc_co_u32_e32 v179, vcc, 0, v169, vcc
	global_load_dwordx4 v[110:113], v[178:179], off offset:-4096
	s_movk_i32 s9, 0x5000
	v_add_co_u32_e32 v180, vcc, s9, v168
	s_waitcnt lgkmcnt(4)
	v_mfma_f32_32x32x16_f16 v[34:49], v[126:129], v[78:81], v[34:49]
	v_addc_co_u32_e32 v181, vcc, 0, v169, vcc
	ds_read_b128 v[174:177], v134 offset:9216
	s_waitcnt lgkmcnt(4)
	v_mfma_f32_32x32x16_f16 v[18:33], v[130:133], v[78:81], v[18:33]
	ds_read_b128 v[130:133], v134 offset:13312
	s_waitcnt lgkmcnt(4)
	v_mfma_f32_32x32x16_f16 v[2:17], v[106:109], v[78:81], v[2:17]
	ds_read_b128 v[78:81], v134 offset:2048
	s_waitcnt vmcnt(27) lgkmcnt(4)
	v_mfma_f32_32x32x16_f16 v[50:65], v[82:85], v[74:77], v[50:65]
	ds_read_b128 v[182:185], v134 offset:3072
	global_load_dwordx4 v[126:129], v[180:181], off offset:1024
	ds_read_b128 v[82:85], v134 offset:6144
	s_waitcnt lgkmcnt(5)
	v_mfma_f32_32x32x16_f16 v[34:49], v[170:173], v[74:77], v[34:49]
	ds_read_b128 v[106:109], v134 offset:10240
	ds_read_b128 v[186:189], v134 offset:7168
	s_waitcnt lgkmcnt(6)
	v_mfma_f32_32x32x16_f16 v[18:33], v[174:177], v[74:77], v[18:33]
	ds_read_b128 v[170:173], v134 offset:14336
	ds_read_b128 v[190:193], v134 offset:11264
	s_waitcnt lgkmcnt(7)
	v_mfma_f32_32x32x16_f16 v[2:17], v[130:133], v[74:77], v[2:17]
	ds_read_b128 v[194:197], v134 offset:15360
	s_waitcnt vmcnt(27) lgkmcnt(7)
	v_mfma_f32_32x32x16_f16 v[50:65], v[78:81], v[70:73], v[50:65]
	global_load_dwordx4 v[130:133], v[180:181], off offset:2048
	s_waitcnt lgkmcnt(5)
	v_mfma_f32_32x32x16_f16 v[34:49], v[82:85], v[70:73], v[34:49]
	s_waitcnt lgkmcnt(4)
	v_mfma_f32_32x32x16_f16 v[18:33], v[106:109], v[70:73], v[18:33]
	s_waitcnt lgkmcnt(2)
	v_mfma_f32_32x32x16_f16 v[2:17], v[170:173], v[70:73], v[2:17]
	global_load_dwordx4 v[106:109], v[180:181], off offset:3072
	s_waitcnt vmcnt(28)
	v_mfma_f32_32x32x16_f16 v[50:65], v[182:185], v[66:69], v[50:65]
	s_waitcnt lgkmcnt(0)
	s_barrier
	ds_read_b128 v[70:73], v134 offset:16384
	ds_read_b128 v[170:173], v134 offset:20480
	v_mfma_f32_32x32x16_f16 v[34:49], v[186:189], v[66:69], v[34:49]
	ds_read_b128 v[78:81], v134 offset:24576
	v_mfma_f32_32x32x16_f16 v[18:33], v[190:193], v[66:69], v[18:33]
	ds_read_b128 v[82:85], v134 offset:28672
	v_mfma_f32_32x32x16_f16 v[2:17], v[194:197], v[66:69], v[2:17]
	ds_read_b128 v[66:69], v134 offset:17408
	s_waitcnt vmcnt(11) lgkmcnt(4)
	v_mfma_f32_32x32x16_f16 v[50:65], v[70:73], v[114:117], v[50:65]
	global_load_dwordx4 v[74:77], v[178:179], off
	ds_read_b128 v[70:73], v134 offset:21504
	s_waitcnt lgkmcnt(4)
	v_mfma_f32_32x32x16_f16 v[34:49], v[170:173], v[114:117], v[34:49]
	ds_read_b128 v[170:173], v134 offset:25600
	s_waitcnt lgkmcnt(4)
	v_mfma_f32_32x32x16_f16 v[18:33], v[78:81], v[114:117], v[18:33]
	ds_read_b128 v[174:177], v134 offset:29696
	s_waitcnt lgkmcnt(4)
	v_mfma_f32_32x32x16_f16 v[2:17], v[82:85], v[114:117], v[2:17]
	ds_read_b128 v[82:85], v134 offset:18432
	s_waitcnt vmcnt(11) lgkmcnt(4)
	v_mfma_f32_32x32x16_f16 v[50:65], v[66:69], v[118:121], v[50:65]
	ds_read_b128 v[182:185], v134 offset:19456
	global_load_dwordx4 v[78:81], v[178:179], off offset:1024
	ds_read_b128 v[66:69], v134 offset:22528
	s_waitcnt lgkmcnt(5)
	v_mfma_f32_32x32x16_f16 v[34:49], v[70:73], v[118:121], v[34:49]
	ds_read_b128 v[70:73], v134 offset:26624
	ds_read_b128 v[186:189], v134 offset:23552
	s_waitcnt lgkmcnt(6)
	v_mfma_f32_32x32x16_f16 v[18:33], v[170:173], v[118:121], v[18:33]
	ds_read_b128 v[114:117], v134 offset:30720
	ds_read_b128 v[190:193], v134 offset:27648
	s_waitcnt lgkmcnt(7)
	v_mfma_f32_32x32x16_f16 v[2:17], v[174:177], v[118:121], v[2:17]
	ds_read_b128 v[194:197], v134 offset:31744
	s_waitcnt vmcnt(11) lgkmcnt(7)
	v_mfma_f32_32x32x16_f16 v[50:65], v[82:85], v[122:125], v[50:65]
	global_load_dwordx4 v[82:85], v[178:179], off offset:2048
	s_waitcnt lgkmcnt(5)
	v_mfma_f32_32x32x16_f16 v[34:49], v[66:69], v[122:125], v[34:49]
	s_waitcnt lgkmcnt(4)
	v_mfma_f32_32x32x16_f16 v[18:33], v[70:73], v[122:125], v[18:33]
	s_waitcnt lgkmcnt(2)
	v_mfma_f32_32x32x16_f16 v[2:17], v[114:117], v[122:125], v[2:17]
	global_load_dwordx4 v[66:69], v[178:179], off offset:3072
	s_waitcnt vmcnt(12)
	v_mfma_f32_32x32x16_f16 v[50:65], v[182:185], v[102:105], v[50:65]
	s_waitcnt lgkmcnt(0)
	s_barrier
	ds_read_b128 v[114:117], v134
	ds_read_b128 v[118:121], v134 offset:4096
	v_mfma_f32_32x32x16_f16 v[34:49], v[186:189], v[102:105], v[34:49]
	ds_read_b128 v[122:125], v134 offset:8192
	v_mfma_f32_32x32x16_f16 v[18:33], v[190:193], v[102:105], v[18:33]
	ds_read_b128 v[170:173], v134 offset:12288
	v_mfma_f32_32x32x16_f16 v[2:17], v[194:197], v[102:105], v[2:17]
	ds_read_b128 v[70:73], v134 offset:1024
	s_waitcnt vmcnt(11) lgkmcnt(4)
	v_mfma_f32_32x32x16_f16 v[50:65], v[114:117], v[90:93], v[50:65]
	s_mov_b32 s9, 0x8000
	v_add_co_u32_e32 v178, vcc, s9, v168
	ds_read_b128 v[102:105], v134 offset:5120
	s_nop 0
	v_addc_co_u32_e32 v179, vcc, 0, v169, vcc
	global_load_dwordx4 v[114:117], v[178:179], off offset:-4096
	s_movk_i32 s9, 0x7000
	v_add_co_u32_e32 v180, vcc, s9, v168
	s_waitcnt lgkmcnt(4)
	v_mfma_f32_32x32x16_f16 v[34:49], v[118:121], v[90:93], v[34:49]
	v_addc_co_u32_e32 v181, vcc, 0, v169, vcc
	ds_read_b128 v[174:177], v134 offset:9216
	s_waitcnt lgkmcnt(4)
	v_mfma_f32_32x32x16_f16 v[18:33], v[122:125], v[90:93], v[18:33]
	ds_read_b128 v[122:125], v134 offset:13312
	s_waitcnt lgkmcnt(4)
	v_mfma_f32_32x32x16_f16 v[2:17], v[170:173], v[90:93], v[2:17]
	ds_read_b128 v[90:93], v134 offset:2048
	s_waitcnt vmcnt(11) lgkmcnt(4)
	v_mfma_f32_32x32x16_f16 v[50:65], v[70:73], v[94:97], v[50:65]
	ds_read_b128 v[182:185], v134 offset:3072
	global_load_dwordx4 v[118:121], v[180:181], off offset:1024
	ds_read_b128 v[70:73], v134 offset:6144
	s_waitcnt lgkmcnt(5)
	v_mfma_f32_32x32x16_f16 v[34:49], v[102:105], v[94:97], v[34:49]
	ds_read_b128 v[102:105], v134 offset:10240
	ds_read_b128 v[186:189], v134 offset:7168
	s_waitcnt lgkmcnt(6)
	v_mfma_f32_32x32x16_f16 v[18:33], v[174:177], v[94:97], v[18:33]
	ds_read_b128 v[170:173], v134 offset:14336
	ds_read_b128 v[190:193], v134 offset:11264
	s_waitcnt lgkmcnt(7)
	v_mfma_f32_32x32x16_f16 v[2:17], v[122:125], v[94:97], v[2:17]
	ds_read_b128 v[194:197], v134 offset:15360
	s_waitcnt vmcnt(11) lgkmcnt(7)
	v_mfma_f32_32x32x16_f16 v[50:65], v[90:93], v[98:101], v[50:65]
	global_load_dwordx4 v[122:125], v[180:181], off offset:2048
	s_waitcnt lgkmcnt(5)
	v_mfma_f32_32x32x16_f16 v[34:49], v[70:73], v[98:101], v[34:49]
	s_waitcnt lgkmcnt(4)
	v_mfma_f32_32x32x16_f16 v[18:33], v[102:105], v[98:101], v[18:33]
	s_waitcnt lgkmcnt(2)
	v_mfma_f32_32x32x16_f16 v[2:17], v[170:173], v[98:101], v[2:17]
	global_load_dwordx4 v[102:105], v[180:181], off offset:3072
	s_waitcnt vmcnt(12)
	v_mfma_f32_32x32x16_f16 v[50:65], v[182:185], v[86:89], v[50:65]
	s_waitcnt lgkmcnt(0)
	s_barrier
	ds_read_b128 v[94:97], v134 offset:16384
	ds_read_b128 v[98:101], v134 offset:20480
	v_mfma_f32_32x32x16_f16 v[34:49], v[186:189], v[86:89], v[34:49]
	ds_read_b128 v[90:93], v134 offset:24576
	v_mfma_f32_32x32x16_f16 v[18:33], v[190:193], v[86:89], v[18:33]
	ds_read_b128 v[70:73], v134 offset:28672
	v_mfma_f32_32x32x16_f16 v[2:17], v[194:197], v[86:89], v[2:17]
	ds_read_b128 v[170:173], v134 offset:17408
	s_waitcnt vmcnt(11) lgkmcnt(4)
	v_mfma_f32_32x32x16_f16 v[50:65], v[94:97], v[110:113], v[50:65]
	global_load_dwordx4 v[86:89], v[178:179], off
	ds_read_b128 v[94:97], v134 offset:21504
	s_waitcnt lgkmcnt(4)
	v_mfma_f32_32x32x16_f16 v[34:49], v[98:101], v[110:113], v[34:49]
	ds_read_b128 v[98:101], v134 offset:25600
	s_waitcnt lgkmcnt(4)
	v_mfma_f32_32x32x16_f16 v[18:33], v[90:93], v[110:113], v[18:33]
	ds_read_b128 v[174:177], v134 offset:29696
	s_waitcnt lgkmcnt(4)
	v_mfma_f32_32x32x16_f16 v[2:17], v[70:73], v[110:113], v[2:17]
	ds_read_b128 v[70:73], v134 offset:18432
	s_waitcnt vmcnt(11) lgkmcnt(4)
	v_mfma_f32_32x32x16_f16 v[50:65], v[170:173], v[126:129], v[50:65]
	ds_read_b128 v[182:185], v134 offset:19456
	global_load_dwordx4 v[90:93], v[178:179], off offset:1024
	ds_read_b128 v[110:113], v134 offset:22528
	s_waitcnt lgkmcnt(5)
	v_mfma_f32_32x32x16_f16 v[34:49], v[94:97], v[126:129], v[34:49]
	ds_read_b128 v[170:173], v134 offset:26624
	ds_read_b128 v[186:189], v134 offset:23552
	s_waitcnt lgkmcnt(6)
	v_mfma_f32_32x32x16_f16 v[18:33], v[98:101], v[126:129], v[18:33]
	ds_read_b128 v[98:101], v134 offset:30720
	ds_read_b128 v[190:193], v134 offset:27648
	s_waitcnt lgkmcnt(7)
	v_mfma_f32_32x32x16_f16 v[2:17], v[174:177], v[126:129], v[2:17]
	ds_read_b128 v[194:197], v134 offset:31744
	s_waitcnt vmcnt(11) lgkmcnt(7)
	v_mfma_f32_32x32x16_f16 v[50:65], v[70:73], v[130:133], v[50:65]
	global_load_dwordx4 v[94:97], v[178:179], off offset:2048
	s_waitcnt lgkmcnt(5)
	v_mfma_f32_32x32x16_f16 v[34:49], v[110:113], v[130:133], v[34:49]
	s_waitcnt lgkmcnt(4)
	v_mfma_f32_32x32x16_f16 v[18:33], v[170:173], v[130:133], v[18:33]
	s_waitcnt lgkmcnt(2)
	v_mfma_f32_32x32x16_f16 v[2:17], v[98:101], v[130:133], v[2:17]
	global_load_dwordx4 v[70:73], v[178:179], off offset:3072
	s_waitcnt vmcnt(12)
	v_mfma_f32_32x32x16_f16 v[50:65], v[182:185], v[106:109], v[50:65]
	s_waitcnt lgkmcnt(0)
	s_barrier
	ds_read_b128 v[98:101], v134
	ds_read_b128 v[126:129], v134 offset:4096
	v_mfma_f32_32x32x16_f16 v[34:49], v[186:189], v[106:109], v[34:49]
	ds_read_b128 v[130:133], v134 offset:8192
	v_mfma_f32_32x32x16_f16 v[18:33], v[190:193], v[106:109], v[18:33]
	ds_read_b128 v[174:177], v134 offset:12288
	v_mfma_f32_32x32x16_f16 v[2:17], v[194:197], v[106:109], v[2:17]
	ds_read_b128 v[106:109], v134 offset:1024
	s_waitcnt vmcnt(11) lgkmcnt(4)
	v_mfma_f32_32x32x16_f16 v[50:65], v[98:101], v[74:77], v[50:65]
	s_mov_b32 s9, 0xa000
	v_add_co_u32_e32 v178, vcc, s9, v168
	ds_read_b128 v[98:101], v134 offset:5120
	s_nop 0
	v_addc_co_u32_e32 v179, vcc, 0, v169, vcc
	global_load_dwordx4 v[110:113], v[178:179], off offset:-4096
	s_mov_b32 s9, 0x9000
	v_add_co_u32_e32 v180, vcc, s9, v168
	s_waitcnt lgkmcnt(4)
	v_mfma_f32_32x32x16_f16 v[34:49], v[126:129], v[74:77], v[34:49]
	v_addc_co_u32_e32 v181, vcc, 0, v169, vcc
	ds_read_b128 v[170:173], v134 offset:9216
	s_waitcnt lgkmcnt(4)
	v_mfma_f32_32x32x16_f16 v[18:33], v[130:133], v[74:77], v[18:33]
	ds_read_b128 v[130:133], v134 offset:13312
	s_waitcnt lgkmcnt(4)
	v_mfma_f32_32x32x16_f16 v[2:17], v[174:177], v[74:77], v[2:17]
	ds_read_b128 v[74:77], v134 offset:2048
	s_waitcnt vmcnt(11) lgkmcnt(4)
	v_mfma_f32_32x32x16_f16 v[50:65], v[106:109], v[78:81], v[50:65]
	ds_read_b128 v[182:185], v134 offset:3072
	global_load_dwordx4 v[126:129], v[180:181], off offset:1024
	ds_read_b128 v[106:109], v134 offset:6144
	s_waitcnt lgkmcnt(5)
	v_mfma_f32_32x32x16_f16 v[34:49], v[98:101], v[78:81], v[34:49]
	ds_read_b128 v[98:101], v134 offset:10240
	ds_read_b128 v[186:189], v134 offset:7168
	s_waitcnt lgkmcnt(6)
	v_mfma_f32_32x32x16_f16 v[18:33], v[170:173], v[78:81], v[18:33]
	ds_read_b128 v[170:173], v134 offset:14336
	ds_read_b128 v[190:193], v134 offset:11264
	s_waitcnt lgkmcnt(7)
	v_mfma_f32_32x32x16_f16 v[2:17], v[130:133], v[78:81], v[2:17]
	ds_read_b128 v[194:197], v134 offset:15360
	s_waitcnt vmcnt(11) lgkmcnt(7)
	v_mfma_f32_32x32x16_f16 v[50:65], v[74:77], v[82:85], v[50:65]
	global_load_dwordx4 v[130:133], v[180:181], off offset:2048
	s_waitcnt lgkmcnt(5)
	v_mfma_f32_32x32x16_f16 v[34:49], v[106:109], v[82:85], v[34:49]
	s_waitcnt lgkmcnt(4)
	v_mfma_f32_32x32x16_f16 v[18:33], v[98:101], v[82:85], v[18:33]
	s_waitcnt lgkmcnt(2)
	v_mfma_f32_32x32x16_f16 v[2:17], v[170:173], v[82:85], v[2:17]
	global_load_dwordx4 v[106:109], v[180:181], off offset:3072
	s_waitcnt vmcnt(12)
	v_mfma_f32_32x32x16_f16 v[50:65], v[182:185], v[66:69], v[50:65]
	s_waitcnt lgkmcnt(0)
	s_barrier
	ds_read_b128 v[78:81], v134 offset:16384
	ds_read_b128 v[82:85], v134 offset:20480
	v_mfma_f32_32x32x16_f16 v[34:49], v[186:189], v[66:69], v[34:49]
	ds_read_b128 v[74:77], v134 offset:24576
	v_mfma_f32_32x32x16_f16 v[18:33], v[190:193], v[66:69], v[18:33]
	ds_read_b128 v[170:173], v134 offset:28672
	v_mfma_f32_32x32x16_f16 v[2:17], v[194:197], v[66:69], v[2:17]
	ds_read_b128 v[66:69], v134 offset:17408
	s_waitcnt vmcnt(11) lgkmcnt(4)
	v_mfma_f32_32x32x16_f16 v[50:65], v[78:81], v[114:117], v[50:65]
	global_load_dwordx4 v[78:81], v[178:179], off
	ds_read_b128 v[98:101], v134 offset:21504
	s_waitcnt lgkmcnt(4)
	v_mfma_f32_32x32x16_f16 v[34:49], v[82:85], v[114:117], v[34:49]
	ds_read_b128 v[174:177], v134 offset:25600
	s_waitcnt lgkmcnt(4)
	v_mfma_f32_32x32x16_f16 v[18:33], v[74:77], v[114:117], v[18:33]
	ds_read_b128 v[74:77], v134 offset:29696
	s_waitcnt lgkmcnt(4)
	v_mfma_f32_32x32x16_f16 v[2:17], v[170:173], v[114:117], v[2:17]
	ds_read_b128 v[114:117], v134 offset:18432
	s_waitcnt vmcnt(11) lgkmcnt(4)
	v_mfma_f32_32x32x16_f16 v[50:65], v[66:69], v[118:121], v[50:65]
	ds_read_b128 v[182:185], v134 offset:19456
	global_load_dwordx4 v[82:85], v[178:179], off offset:1024
	ds_read_b128 v[66:69], v134 offset:22528
	s_waitcnt lgkmcnt(5)
	v_mfma_f32_32x32x16_f16 v[34:49], v[98:101], v[118:121], v[34:49]
	ds_read_b128 v[170:173], v134 offset:26624
	ds_read_b128 v[186:189], v134 offset:23552
	s_waitcnt lgkmcnt(6)
	v_mfma_f32_32x32x16_f16 v[18:33], v[174:177], v[118:121], v[18:33]
	ds_read_b128 v[174:177], v134 offset:30720
	ds_read_b128 v[190:193], v134 offset:27648
	s_waitcnt lgkmcnt(7)
	v_mfma_f32_32x32x16_f16 v[2:17], v[74:77], v[118:121], v[2:17]
	ds_read_b128 v[194:197], v134 offset:31744
	s_waitcnt vmcnt(11) lgkmcnt(7)
	v_mfma_f32_32x32x16_f16 v[50:65], v[114:117], v[122:125], v[50:65]
	global_load_dwordx4 v[98:101], v[178:179], off offset:2048
	s_waitcnt lgkmcnt(5)
	v_mfma_f32_32x32x16_f16 v[34:49], v[66:69], v[122:125], v[34:49]
	s_waitcnt lgkmcnt(4)
	v_mfma_f32_32x32x16_f16 v[18:33], v[170:173], v[122:125], v[18:33]
	s_waitcnt lgkmcnt(2)
	v_mfma_f32_32x32x16_f16 v[2:17], v[174:177], v[122:125], v[2:17]
	global_load_dwordx4 v[74:77], v[178:179], off offset:3072
	s_waitcnt vmcnt(12)
	v_mfma_f32_32x32x16_f16 v[50:65], v[182:185], v[102:105], v[50:65]
	s_waitcnt lgkmcnt(0)
	s_barrier
	ds_read_b128 v[118:121], v134
	ds_read_b128 v[122:125], v134 offset:4096
	v_mfma_f32_32x32x16_f16 v[34:49], v[186:189], v[102:105], v[34:49]
	ds_read_b128 v[174:177], v134 offset:8192
	v_mfma_f32_32x32x16_f16 v[18:33], v[190:193], v[102:105], v[18:33]
	ds_read_b128 v[66:69], v134 offset:12288
	v_mfma_f32_32x32x16_f16 v[2:17], v[194:197], v[102:105], v[2:17]
	ds_read_b128 v[102:105], v134 offset:1024
	s_waitcnt vmcnt(11) lgkmcnt(4)
	v_mfma_f32_32x32x16_f16 v[50:65], v[118:121], v[86:89], v[50:65]
	s_mov_b32 s9, 0xc000
	v_add_co_u32_e32 v178, vcc, s9, v168
	s_waitcnt lgkmcnt(3)
	v_mfma_f32_32x32x16_f16 v[34:49], v[122:125], v[86:89], v[34:49]
	v_addc_co_u32_e32 v179, vcc, 0, v169, vcc
	global_load_dwordx4 v[114:117], v[178:179], off offset:-4096
	ds_read_b128 v[122:125], v134 offset:5120
	s_mov_b32 s9, 0xb000
	v_add_co_u32_e32 v180, vcc, s9, v168
	s_nop 1
	v_addc_co_u32_e32 v181, vcc, 0, v169, vcc
	ds_read_b128 v[170:173], v134 offset:9216
	s_waitcnt lgkmcnt(4)
	v_mfma_f32_32x32x16_f16 v[18:33], v[174:177], v[86:89], v[18:33]
	ds_read_b128 v[174:177], v134 offset:13312
	s_waitcnt lgkmcnt(4)
	v_mfma_f32_32x32x16_f16 v[2:17], v[66:69], v[86:89], v[2:17]
	ds_read_b128 v[66:69], v134 offset:2048
	s_waitcnt vmcnt(11) lgkmcnt(4)
	v_mfma_f32_32x32x16_f16 v[50:65], v[102:105], v[90:93], v[50:65]
	ds_read_b128 v[182:185], v134 offset:3072
	global_load_dwordx4 v[118:121], v[180:181], off offset:1024
	ds_read_b128 v[86:89], v134 offset:6144
	s_waitcnt lgkmcnt(5)
	v_mfma_f32_32x32x16_f16 v[34:49], v[122:125], v[90:93], v[34:49]
	ds_read_b128 v[102:105], v134 offset:10240
	ds_read_b128 v[186:189], v134 offset:7168
	s_waitcnt lgkmcnt(6)
	v_mfma_f32_32x32x16_f16 v[18:33], v[170:173], v[90:93], v[18:33]
	ds_read_b128 v[170:173], v134 offset:14336
	ds_read_b128 v[190:193], v134 offset:11264
	s_waitcnt lgkmcnt(7)
	v_mfma_f32_32x32x16_f16 v[2:17], v[174:177], v[90:93], v[2:17]
	ds_read_b128 v[194:197], v134 offset:15360
	s_waitcnt vmcnt(11) lgkmcnt(7)
	v_mfma_f32_32x32x16_f16 v[50:65], v[66:69], v[94:97], v[50:65]
	global_load_dwordx4 v[122:125], v[180:181], off offset:2048
	s_waitcnt lgkmcnt(5)
	v_mfma_f32_32x32x16_f16 v[34:49], v[86:89], v[94:97], v[34:49]
	s_waitcnt lgkmcnt(4)
	v_mfma_f32_32x32x16_f16 v[18:33], v[102:105], v[94:97], v[18:33]
	s_waitcnt lgkmcnt(2)
	v_mfma_f32_32x32x16_f16 v[2:17], v[170:173], v[94:97], v[2:17]
	global_load_dwordx4 v[94:97], v[180:181], off offset:3072
	s_waitcnt vmcnt(12)
	v_mfma_f32_32x32x16_f16 v[50:65], v[182:185], v[70:73], v[50:65]
	s_waitcnt lgkmcnt(0)
	s_barrier
	ds_read_b128 v[90:93], v134 offset:16384
	ds_read_b128 v[170:173], v134 offset:20480
	v_mfma_f32_32x32x16_f16 v[34:49], v[186:189], v[70:73], v[34:49]
	ds_read_b128 v[66:69], v134 offset:24576
	v_mfma_f32_32x32x16_f16 v[18:33], v[190:193], v[70:73], v[18:33]
	ds_read_b128 v[86:89], v134 offset:28672
	v_mfma_f32_32x32x16_f16 v[2:17], v[194:197], v[70:73], v[2:17]
	ds_read_b128 v[70:73], v134 offset:17408
	s_waitcnt vmcnt(11) lgkmcnt(4)
	v_mfma_f32_32x32x16_f16 v[50:65], v[90:93], v[110:113], v[50:65]
	global_load_dwordx4 v[102:105], v[178:179], off
	ds_read_b128 v[90:93], v134 offset:21504
	s_waitcnt lgkmcnt(4)
	v_mfma_f32_32x32x16_f16 v[34:49], v[170:173], v[110:113], v[34:49]
	ds_read_b128 v[170:173], v134 offset:25600
	s_waitcnt lgkmcnt(4)
	v_mfma_f32_32x32x16_f16 v[18:33], v[66:69], v[110:113], v[18:33]
	ds_read_b128 v[66:69], v134 offset:29696
	s_waitcnt lgkmcnt(4)
	v_mfma_f32_32x32x16_f16 v[2:17], v[86:89], v[110:113], v[2:17]
	ds_read_b128 v[110:113], v134 offset:18432
	s_waitcnt vmcnt(11) lgkmcnt(4)
	v_mfma_f32_32x32x16_f16 v[50:65], v[70:73], v[126:129], v[50:65]
	ds_read_b128 v[182:185], v134 offset:19456
	global_load_dwordx4 v[86:89], v[178:179], off offset:1024
	ds_read_b128 v[174:177], v134 offset:22528
	s_waitcnt lgkmcnt(5)
	v_mfma_f32_32x32x16_f16 v[34:49], v[90:93], v[126:129], v[34:49]
	ds_read_b128 v[90:93], v134 offset:26624
	ds_read_b128 v[186:189], v134 offset:23552
	s_waitcnt lgkmcnt(6)
	v_mfma_f32_32x32x16_f16 v[18:33], v[170:173], v[126:129], v[18:33]
	ds_read_b128 v[170:173], v134 offset:30720
	ds_read_b128 v[190:193], v134 offset:27648
	s_waitcnt lgkmcnt(7)
	v_mfma_f32_32x32x16_f16 v[2:17], v[66:69], v[126:129], v[2:17]
	ds_read_b128 v[194:197], v134 offset:31744
	s_waitcnt vmcnt(11) lgkmcnt(7)
	v_mfma_f32_32x32x16_f16 v[50:65], v[110:113], v[130:133], v[50:65]
	global_load_dwordx4 v[70:73], v[178:179], off offset:2048
	s_waitcnt lgkmcnt(5)
	v_mfma_f32_32x32x16_f16 v[34:49], v[174:177], v[130:133], v[34:49]
	s_waitcnt lgkmcnt(4)
	v_mfma_f32_32x32x16_f16 v[18:33], v[90:93], v[130:133], v[18:33]
	s_waitcnt lgkmcnt(2)
	v_mfma_f32_32x32x16_f16 v[2:17], v[170:173], v[130:133], v[2:17]
	global_load_dwordx4 v[66:69], v[178:179], off offset:3072
	s_waitcnt vmcnt(12)
	v_mfma_f32_32x32x16_f16 v[50:65], v[182:185], v[106:109], v[50:65]
	s_waitcnt lgkmcnt(0)
	s_barrier
	ds_read_b128 v[126:129], v134
	ds_read_b128 v[130:133], v134 offset:4096
	v_mfma_f32_32x32x16_f16 v[34:49], v[186:189], v[106:109], v[34:49]
	ds_read_b128 v[110:113], v134 offset:8192
	v_mfma_f32_32x32x16_f16 v[18:33], v[190:193], v[106:109], v[18:33]
	ds_read_b128 v[170:173], v134 offset:12288
	v_mfma_f32_32x32x16_f16 v[2:17], v[194:197], v[106:109], v[2:17]
	ds_read_b128 v[106:109], v134 offset:1024
	s_waitcnt vmcnt(11) lgkmcnt(4)
	v_mfma_f32_32x32x16_f16 v[50:65], v[126:129], v[78:81], v[50:65]
	s_mov_b32 s9, 0xe000
	v_add_co_u32_e32 v178, vcc, s9, v168
	ds_read_b128 v[126:129], v134 offset:5120
	s_nop 0
	v_addc_co_u32_e32 v179, vcc, 0, v169, vcc
	global_load_dwordx4 v[90:93], v[178:179], off offset:-4096
	s_mov_b32 s9, 0xd000
	v_add_co_u32_e32 v180, vcc, s9, v168
	s_waitcnt lgkmcnt(4)
	v_mfma_f32_32x32x16_f16 v[34:49], v[130:133], v[78:81], v[34:49]
	v_addc_co_u32_e32 v181, vcc, 0, v169, vcc
	ds_read_b128 v[130:133], v134 offset:9216
	s_waitcnt lgkmcnt(4)
	v_mfma_f32_32x32x16_f16 v[18:33], v[110:113], v[78:81], v[18:33]
	ds_read_b128 v[110:113], v134 offset:13312
	s_waitcnt lgkmcnt(4)
	v_mfma_f32_32x32x16_f16 v[2:17], v[170:173], v[78:81], v[2:17]
	ds_read_b128 v[78:81], v134 offset:2048
	s_waitcnt vmcnt(11) lgkmcnt(4)
	v_mfma_f32_32x32x16_f16 v[50:65], v[106:109], v[82:85], v[50:65]
	ds_read_b128 v[182:185], v134 offset:3072
	global_load_dwordx4 v[106:109], v[180:181], off offset:1024
	ds_read_b128 v[170:173], v134 offset:6144
	s_waitcnt lgkmcnt(5)
	v_mfma_f32_32x32x16_f16 v[34:49], v[126:129], v[82:85], v[34:49]
	ds_read_b128 v[126:129], v134 offset:10240
	ds_read_b128 v[186:189], v134 offset:7168
	s_waitcnt lgkmcnt(6)
	v_mfma_f32_32x32x16_f16 v[18:33], v[130:133], v[82:85], v[18:33]
	ds_read_b128 v[130:133], v134 offset:14336
	ds_read_b128 v[190:193], v134 offset:11264
	s_waitcnt lgkmcnt(7)
	v_mfma_f32_32x32x16_f16 v[2:17], v[110:113], v[82:85], v[2:17]
	ds_read_b128 v[194:197], v134 offset:15360
	s_waitcnt vmcnt(11) lgkmcnt(7)
	v_mfma_f32_32x32x16_f16 v[50:65], v[78:81], v[98:101], v[50:65]
	global_load_dwordx4 v[82:85], v[180:181], off offset:2048
	s_waitcnt lgkmcnt(5)
	v_mfma_f32_32x32x16_f16 v[34:49], v[170:173], v[98:101], v[34:49]
	s_waitcnt lgkmcnt(4)
	v_mfma_f32_32x32x16_f16 v[18:33], v[126:129], v[98:101], v[18:33]
	s_waitcnt lgkmcnt(2)
	v_mfma_f32_32x32x16_f16 v[2:17], v[130:133], v[98:101], v[2:17]
	global_load_dwordx4 v[78:81], v[180:181], off offset:3072
	s_waitcnt vmcnt(12)
	v_mfma_f32_32x32x16_f16 v[50:65], v[182:185], v[74:77], v[50:65]
	s_waitcnt lgkmcnt(0)
	s_barrier
	ds_read_b128 v[98:101], v134 offset:16384
	ds_read_b128 v[110:113], v134 offset:20480
	v_mfma_f32_32x32x16_f16 v[34:49], v[186:189], v[74:77], v[34:49]
	ds_read_b128 v[130:133], v134 offset:24576
	v_mfma_f32_32x32x16_f16 v[18:33], v[190:193], v[74:77], v[18:33]
	ds_read_b128 v[170:173], v134 offset:28672
	v_mfma_f32_32x32x16_f16 v[2:17], v[194:197], v[74:77], v[2:17]
	ds_read_b128 v[74:77], v134 offset:17408
	s_waitcnt vmcnt(11) lgkmcnt(4)
	v_mfma_f32_32x32x16_f16 v[50:65], v[98:101], v[114:117], v[50:65]
	global_load_dwordx4 v[98:101], v[178:179], off
	ds_read_b128 v[126:129], v134 offset:21504
	s_waitcnt lgkmcnt(4)
	v_mfma_f32_32x32x16_f16 v[34:49], v[110:113], v[114:117], v[34:49]
	ds_read_b128 v[174:177], v134 offset:25600
	s_waitcnt lgkmcnt(4)
	v_mfma_f32_32x32x16_f16 v[18:33], v[130:133], v[114:117], v[18:33]
	ds_read_b128 v[130:133], v134 offset:29696
	s_waitcnt lgkmcnt(4)
	v_mfma_f32_32x32x16_f16 v[2:17], v[170:173], v[114:117], v[2:17]
	ds_read_b128 v[114:117], v134 offset:18432
	s_waitcnt vmcnt(11) lgkmcnt(4)
	v_mfma_f32_32x32x16_f16 v[50:65], v[74:77], v[118:121], v[50:65]
	ds_read_b128 v[182:185], v134 offset:19456
	global_load_dwordx4 v[110:113], v[178:179], off offset:1024
	ds_read_b128 v[74:77], v134 offset:22528
	s_waitcnt lgkmcnt(5)
	v_mfma_f32_32x32x16_f16 v[34:49], v[126:129], v[118:121], v[34:49]
	ds_read_b128 v[126:129], v134 offset:26624
	ds_read_b128 v[186:189], v134 offset:23552
	s_waitcnt lgkmcnt(6)
	v_mfma_f32_32x32x16_f16 v[18:33], v[174:177], v[118:121], v[18:33]
	ds_read_b128 v[170:173], v134 offset:30720
	ds_read_b128 v[190:193], v134 offset:27648
	s_waitcnt lgkmcnt(7)
	v_mfma_f32_32x32x16_f16 v[2:17], v[130:133], v[118:121], v[2:17]
	ds_read_b128 v[194:197], v134 offset:31744
	s_waitcnt vmcnt(11) lgkmcnt(7)
	v_mfma_f32_32x32x16_f16 v[50:65], v[114:117], v[122:125], v[50:65]
	global_load_dwordx4 v[114:117], v[178:179], off offset:2048
	s_waitcnt lgkmcnt(5)
	v_mfma_f32_32x32x16_f16 v[34:49], v[74:77], v[122:125], v[34:49]
	s_waitcnt lgkmcnt(4)
	v_mfma_f32_32x32x16_f16 v[18:33], v[126:129], v[122:125], v[18:33]
	s_waitcnt lgkmcnt(2)
	v_mfma_f32_32x32x16_f16 v[2:17], v[170:173], v[122:125], v[2:17]
	global_load_dwordx4 v[74:77], v[178:179], off offset:3072
	s_waitcnt vmcnt(12)
	v_mfma_f32_32x32x16_f16 v[50:65], v[182:185], v[94:97], v[50:65]
	s_waitcnt lgkmcnt(0)
	s_barrier
	ds_read_b128 v[118:121], v134
	ds_read_b128 v[122:125], v134 offset:4096
	v_mfma_f32_32x32x16_f16 v[34:49], v[186:189], v[94:97], v[34:49]
	ds_read_b128 v[130:133], v134 offset:8192
	v_mfma_f32_32x32x16_f16 v[18:33], v[190:193], v[94:97], v[18:33]
	v_mfma_f32_32x32x16_f16 v[2:17], v[194:197], v[94:97], v[2:17]
	ds_read_b128 v[126:129], v134 offset:12288
	ds_read_b128 v[170:173], v134 offset:1024
	s_waitcnt vmcnt(11) lgkmcnt(4)
	v_mfma_f32_32x32x16_f16 v[50:65], v[118:121], v[102:105], v[50:65]
	s_mov_b32 s9, 0xf000
	v_add_co_u32_e32 v174, vcc, s9, v168
	ds_read_b128 v[118:121], v134 offset:5120
	s_nop 0
	v_addc_co_u32_e32 v175, vcc, 0, v169, vcc
	global_load_dwordx4 v[94:97], v[174:175], off
	s_waitcnt lgkmcnt(4)
	v_mfma_f32_32x32x16_f16 v[34:49], v[122:125], v[102:105], v[34:49]
	ds_read_b128 v[122:125], v134 offset:9216
	s_waitcnt lgkmcnt(4)
	v_mfma_f32_32x32x16_f16 v[18:33], v[130:133], v[102:105], v[18:33]
	s_waitcnt lgkmcnt(3)
	v_mfma_f32_32x32x16_f16 v[2:17], v[126:129], v[102:105], v[2:17]
	ds_read_b128 v[126:129], v134 offset:13312
	ds_read_b128 v[130:133], v134 offset:2048
	s_waitcnt vmcnt(11) lgkmcnt(4)
	v_mfma_f32_32x32x16_f16 v[50:65], v[170:173], v[86:89], v[50:65]
	ds_read_b128 v[182:185], v134 offset:3072
	global_load_dwordx4 v[102:105], v[174:175], off offset:1024
	s_waitcnt lgkmcnt(4)
	v_mfma_f32_32x32x16_f16 v[34:49], v[118:121], v[86:89], v[34:49]
	ds_read_b128 v[118:121], v134 offset:6144
	ds_read_b128 v[186:189], v134 offset:7168
	s_waitcnt lgkmcnt(5)
	v_mfma_f32_32x32x16_f16 v[18:33], v[122:125], v[86:89], v[18:33]
	ds_read_b128 v[122:125], v134 offset:10240
	ds_read_b128 v[190:193], v134 offset:11264
	s_waitcnt lgkmcnt(6)
	v_mfma_f32_32x32x16_f16 v[2:17], v[126:129], v[86:89], v[2:17]
	ds_read_b128 v[126:129], v134 offset:14336
	ds_read_b128 v[194:197], v134 offset:15360
	s_waitcnt vmcnt(11) lgkmcnt(7)
	v_mfma_f32_32x32x16_f16 v[50:65], v[130:133], v[70:73], v[50:65]
	global_load_dwordx4 v[86:89], v[174:175], off offset:2048
	s_waitcnt lgkmcnt(5)
	v_mfma_f32_32x32x16_f16 v[34:49], v[118:121], v[70:73], v[34:49]
	s_waitcnt lgkmcnt(3)
	v_mfma_f32_32x32x16_f16 v[18:33], v[122:125], v[70:73], v[18:33]
	s_waitcnt lgkmcnt(1)
	v_mfma_f32_32x32x16_f16 v[2:17], v[126:129], v[70:73], v[2:17]
	global_load_dwordx4 v[70:73], v[174:175], off offset:3072
	s_waitcnt vmcnt(12)
	v_mfma_f32_32x32x16_f16 v[50:65], v[182:185], v[66:69], v[50:65]
	s_waitcnt lgkmcnt(0)
	s_barrier
	ds_read_b128 v[130:133], v134 offset:16384
	v_mfma_f32_32x32x16_f16 v[34:49], v[186:189], v[66:69], v[34:49]
	ds_read_b128 v[118:121], v134 offset:20480
	v_mfma_f32_32x32x16_f16 v[18:33], v[190:193], v[66:69], v[18:33]
	ds_read_b128 v[122:125], v134 offset:24576
	v_mfma_f32_32x32x16_f16 v[2:17], v[194:197], v[66:69], v[2:17]
	ds_read_b128 v[66:69], v134 offset:28672
	ds_read_b128 v[126:129], v134 offset:17408
	s_waitcnt vmcnt(11) lgkmcnt(4)
	v_mfma_f32_32x32x16_f16 v[50:65], v[130:133], v[90:93], v[50:65]
	ds_read_b128 v[130:133], v134 offset:21504
	s_waitcnt lgkmcnt(4)
	v_mfma_f32_32x32x16_f16 v[34:49], v[118:121], v[90:93], v[34:49]
	ds_read_b128 v[118:121], v134 offset:25600
	s_waitcnt lgkmcnt(4)
	v_mfma_f32_32x32x16_f16 v[18:33], v[122:125], v[90:93], v[18:33]
	ds_read_b128 v[122:125], v134 offset:29696
	s_waitcnt lgkmcnt(4)
	v_mfma_f32_32x32x16_f16 v[2:17], v[66:69], v[90:93], v[2:17]
	ds_read_b128 v[66:69], v134 offset:18432
	s_waitcnt vmcnt(10) lgkmcnt(4)
	v_mfma_f32_32x32x16_f16 v[50:65], v[126:129], v[106:109], v[50:65]
	ds_read_b128 v[90:93], v134 offset:22528
	ds_read_b128 v[182:185], v134 offset:19456
	s_waitcnt lgkmcnt(5)
	v_mfma_f32_32x32x16_f16 v[34:49], v[130:133], v[106:109], v[34:49]
	ds_read_b128 v[126:129], v134 offset:26624
	ds_read_b128 v[186:189], v134 offset:23552
	s_waitcnt lgkmcnt(6)
	v_mfma_f32_32x32x16_f16 v[18:33], v[118:121], v[106:109], v[18:33]
	ds_read_b128 v[118:121], v134 offset:30720
	ds_read_b128 v[190:193], v134 offset:27648
	s_waitcnt lgkmcnt(7)
	v_mfma_f32_32x32x16_f16 v[2:17], v[122:125], v[106:109], v[2:17]
	ds_read_b128 v[194:197], v134 offset:31744
	s_waitcnt vmcnt(9) lgkmcnt(7)
	v_mfma_f32_32x32x16_f16 v[50:65], v[66:69], v[82:85], v[50:65]
	s_waitcnt lgkmcnt(6)
	v_mfma_f32_32x32x16_f16 v[34:49], v[90:93], v[82:85], v[34:49]
	s_waitcnt lgkmcnt(4)
	v_mfma_f32_32x32x16_f16 v[18:33], v[126:129], v[82:85], v[18:33]
	s_waitcnt lgkmcnt(2)
	v_mfma_f32_32x32x16_f16 v[2:17], v[118:121], v[82:85], v[2:17]
	s_waitcnt vmcnt(8)
	v_mfma_f32_32x32x16_f16 v[50:65], v[182:185], v[78:81], v[50:65]
	s_waitcnt lgkmcnt(0)
	s_barrier
	ds_read_b128 v[82:85], v134
	ds_read_b128 v[106:109], v134 offset:4096
	v_mfma_f32_32x32x16_f16 v[34:49], v[186:189], v[78:81], v[34:49]
	ds_read_b128 v[66:69], v134 offset:8192
	v_mfma_f32_32x32x16_f16 v[18:33], v[190:193], v[78:81], v[18:33]
	ds_read_b128 v[90:93], v134 offset:12288
	v_mfma_f32_32x32x16_f16 v[2:17], v[194:197], v[78:81], v[2:17]
	ds_read_b128 v[78:81], v134 offset:1024
	s_waitcnt vmcnt(7) lgkmcnt(4)
	v_mfma_f32_32x32x16_f16 v[50:65], v[82:85], v[98:101], v[50:65]
	ds_read_b128 v[82:85], v134 offset:5120
	s_waitcnt lgkmcnt(4)
	v_mfma_f32_32x32x16_f16 v[34:49], v[106:109], v[98:101], v[34:49]
	ds_read_b128 v[106:109], v134 offset:9216
	s_waitcnt lgkmcnt(4)
	v_mfma_f32_32x32x16_f16 v[18:33], v[66:69], v[98:101], v[18:33]
	ds_read_b128 v[66:69], v134 offset:13312
	s_waitcnt lgkmcnt(4)
	v_mfma_f32_32x32x16_f16 v[2:17], v[90:93], v[98:101], v[2:17]
	ds_read_b128 v[90:93], v134 offset:2048
	s_waitcnt vmcnt(6) lgkmcnt(4)
	v_mfma_f32_32x32x16_f16 v[50:65], v[78:81], v[110:113], v[50:65]
	ds_read_b128 v[78:81], v134 offset:6144
	ds_read_b128 v[182:185], v134 offset:3072
	s_waitcnt lgkmcnt(5)
	v_mfma_f32_32x32x16_f16 v[34:49], v[82:85], v[110:113], v[34:49]
	ds_read_b128 v[82:85], v134 offset:10240
	ds_read_b128 v[186:189], v134 offset:7168
	s_waitcnt lgkmcnt(6)
	v_mfma_f32_32x32x16_f16 v[18:33], v[106:109], v[110:113], v[18:33]
	ds_read_b128 v[98:101], v134 offset:14336
	ds_read_b128 v[190:193], v134 offset:11264
	s_waitcnt lgkmcnt(7)
	v_mfma_f32_32x32x16_f16 v[2:17], v[66:69], v[110:113], v[2:17]
	ds_read_b128 v[194:197], v134 offset:15360
	s_waitcnt vmcnt(5) lgkmcnt(7)
	v_mfma_f32_32x32x16_f16 v[50:65], v[90:93], v[114:117], v[50:65]
	s_waitcnt lgkmcnt(6)
	v_mfma_f32_32x32x16_f16 v[34:49], v[78:81], v[114:117], v[34:49]
	s_waitcnt lgkmcnt(4)
	v_mfma_f32_32x32x16_f16 v[18:33], v[82:85], v[114:117], v[18:33]
	s_waitcnt lgkmcnt(2)
	v_mfma_f32_32x32x16_f16 v[2:17], v[98:101], v[114:117], v[2:17]
	s_waitcnt vmcnt(4)
	v_mfma_f32_32x32x16_f16 v[50:65], v[182:185], v[74:77], v[50:65]
	s_waitcnt lgkmcnt(0)
	s_barrier
	ds_read_b128 v[66:69], v134 offset:16384
	ds_read_b128 v[98:101], v134 offset:20480
	v_mfma_f32_32x32x16_f16 v[34:49], v[186:189], v[74:77], v[34:49]
	ds_read_b128 v[90:93], v134 offset:24576
	v_mfma_f32_32x32x16_f16 v[18:33], v[190:193], v[74:77], v[18:33]
	ds_read_b128 v[78:81], v134 offset:28672
	v_mfma_f32_32x32x16_f16 v[2:17], v[194:197], v[74:77], v[2:17]
	ds_read_b128 v[74:77], v134 offset:17408
	s_waitcnt vmcnt(3) lgkmcnt(4)
	v_mfma_f32_32x32x16_f16 v[50:65], v[66:69], v[94:97], v[50:65]
	ds_read_b128 v[66:69], v134 offset:21504
	s_waitcnt lgkmcnt(4)
	v_mfma_f32_32x32x16_f16 v[34:49], v[98:101], v[94:97], v[34:49]
	ds_read_b128 v[82:85], v134 offset:25600
	s_waitcnt lgkmcnt(4)
	v_mfma_f32_32x32x16_f16 v[18:33], v[90:93], v[94:97], v[18:33]
	ds_read_b128 v[90:93], v134 offset:29696
	s_waitcnt lgkmcnt(4)
	v_mfma_f32_32x32x16_f16 v[2:17], v[78:81], v[94:97], v[2:17]
	s_waitcnt vmcnt(2) lgkmcnt(3)
	v_mfma_f32_32x32x16_f16 v[50:65], v[74:77], v[102:105], v[50:65]
	ds_read_b128 v[74:77], v134 offset:18432
	ds_read_b128 v[182:185], v134 offset:19456
	s_waitcnt lgkmcnt(4)
	v_mfma_f32_32x32x16_f16 v[34:49], v[66:69], v[102:105], v[34:49]
	ds_read_b128 v[66:69], v134 offset:22528
	ds_read_b128 v[78:81], v134 offset:26624
	ds_read_b128 v[186:189], v134 offset:23552
	s_waitcnt lgkmcnt(6)
	v_mfma_f32_32x32x16_f16 v[18:33], v[82:85], v[102:105], v[18:33]
	ds_read_b128 v[82:85], v134 offset:30720
	ds_read_b128 v[190:193], v134 offset:27648
	s_waitcnt lgkmcnt(7)
	v_mfma_f32_32x32x16_f16 v[2:17], v[90:93], v[102:105], v[2:17]
	ds_read_b128 v[194:197], v134 offset:31744
	s_waitcnt vmcnt(1) lgkmcnt(7)
	v_mfma_f32_32x32x16_f16 v[50:65], v[74:77], v[86:89], v[50:65]
	s_waitcnt lgkmcnt(5)
	v_mfma_f32_32x32x16_f16 v[34:49], v[66:69], v[86:89], v[34:49]
	s_waitcnt lgkmcnt(4)
	v_mfma_f32_32x32x16_f16 v[18:33], v[78:81], v[86:89], v[18:33]
	s_waitcnt lgkmcnt(2)
	v_mfma_f32_32x32x16_f16 v[2:17], v[82:85], v[86:89], v[2:17]
	s_waitcnt vmcnt(0)
	v_mfma_f32_32x32x16_f16 v[50:65], v[182:185], v[70:73], v[50:65]
	v_mfma_f32_32x32x16_f16 v[34:49], v[186:189], v[70:73], v[34:49]
	s_waitcnt lgkmcnt(1)
	v_mfma_f32_32x32x16_f16 v[18:33], v[190:193], v[70:73], v[18:33]
	s_waitcnt lgkmcnt(0)
	v_mfma_f32_32x32x16_f16 v[2:17], v[194:197], v[70:73], v[2:17]
	v_cvt_f32_f16_e32 v66, v166
	v_cvt_f32_f16_sdwa v67, v166 dst_sel:DWORD dst_unused:UNUSED_PAD src0_sel:WORD_1
	v_cvt_f32_f16_e32 v68, v167
	v_cvt_f32_f16_sdwa v69, v167 dst_sel:DWORD dst_unused:UNUSED_PAD src0_sel:WORD_1
	v_cvt_f32_f16_e32 v70, v164
	v_cvt_f32_f16_sdwa v71, v164 dst_sel:DWORD dst_unused:UNUSED_PAD src0_sel:WORD_1
	v_cvt_f32_f16_e32 v72, v165
	v_cvt_f32_f16_sdwa v73, v165 dst_sel:DWORD dst_unused:UNUSED_PAD src0_sel:WORD_1
	v_cvt_f32_f16_e32 v74, v162
	v_cvt_f32_f16_sdwa v75, v162 dst_sel:DWORD dst_unused:UNUSED_PAD src0_sel:WORD_1
	v_pk_fma_f32 v[66:67], v[66:67], v[66:67], 1.0 op_sel_hi:[1,1,0] neg_lo:[1,0,0] neg_hi:[1,0,0]
	v_cvt_f32_f16_e32 v76, v163
	v_cvt_f32_f16_sdwa v77, v163 dst_sel:DWORD dst_unused:UNUSED_PAD src0_sel:WORD_1
	v_pk_mul_f32 v[66:67], v[50:51], v[66:67]
	v_pk_fma_f32 v[50:51], v[68:69], v[68:69], 1.0 op_sel_hi:[1,1,0] neg_lo:[1,0,0] neg_hi:[1,0,0]
	s_nop 0
	v_pk_mul_f32 v[68:69], v[52:53], v[50:51]
	v_pk_fma_f32 v[50:51], v[70:71], v[70:71], 1.0 op_sel_hi:[1,1,0] neg_lo:[1,0,0] neg_hi:[1,0,0]
	s_barrier
	v_pk_mul_f32 v[54:55], v[54:55], v[50:51]
	v_pk_fma_f32 v[50:51], v[72:73], v[72:73], 1.0 op_sel_hi:[1,1,0] neg_lo:[1,0,0] neg_hi:[1,0,0]
	s_nop 0
	v_pk_mul_f32 v[56:57], v[56:57], v[50:51]
	v_pk_fma_f32 v[50:51], v[74:75], v[74:75], 1.0 op_sel_hi:[1,1,0] neg_lo:[1,0,0] neg_hi:[1,0,0]
	v_cvt_f32_f16_e32 v78, v160
	v_pk_mul_f32 v[90:91], v[58:59], v[50:51]
	v_pk_fma_f32 v[50:51], v[76:77], v[76:77], 1.0 op_sel_hi:[1,1,0] neg_lo:[1,0,0] neg_hi:[1,0,0]
	v_cvt_f32_f16_sdwa v79, v160 dst_sel:DWORD dst_unused:UNUSED_PAD src0_sel:WORD_1
	v_pk_mul_f32 v[92:93], v[60:61], v[50:51]
	ds_read_b128 v[50:53], v134 offset:33792
	v_cvt_f32_f16_e32 v86, v161
	v_cvt_f32_f16_sdwa v87, v161 dst_sel:DWORD dst_unused:UNUSED_PAD src0_sel:WORD_1
	v_cvt_pk_f16_f32 v57, v56, v57
	v_cvt_pk_f16_f32 v56, v54, v55
	v_cvt_pk_f16_f32 v55, v68, v69
	v_cvt_pk_f16_f32 v54, v66, v67
	v_pk_fma_f32 v[58:59], v[78:79], v[78:79], 1.0 op_sel_hi:[1,1,0] neg_lo:[1,0,0] neg_hi:[1,0,0]
	v_cvt_f32_f16_e32 v94, v152
	s_waitcnt lgkmcnt(0)
	v_mfma_f32_32x32x16_f16 v[66:81], v[50:53], v[54:57], 0
	v_fma_f32 v50, -v86, v86, 1.0
	v_fma_f32 v51, -v87, v87, 1.0
	v_mul_f32_e64 v62, v62, v58
	v_mul_f32_e64 v63, v63, v59
	ds_read_b128 v[58:61], v134 offset:34816
	ds_read_b128 v[82:85], v134 offset:35840
	v_pk_mul_f32 v[50:51], v[64:65], v[50:51]
	v_cvt_f32_f16_e32 v52, v159
	v_cvt_pk_f16_f32 v89, v50, v51
	v_cvt_f32_f16_e32 v50, v158
	v_cvt_f32_f16_sdwa v51, v158 dst_sel:DWORD dst_unused:UNUSED_PAD src0_sel:WORD_1
	v_cvt_f32_f16_sdwa v53, v159 dst_sel:DWORD dst_unused:UNUSED_PAD src0_sel:WORD_1
	v_cvt_pk_f16_f32 v88, v62, v63
	v_cvt_f32_f16_e32 v62, v156
	v_cvt_f32_f16_sdwa v63, v156 dst_sel:DWORD dst_unused:UNUSED_PAD src0_sel:WORD_1
	v_cvt_pk_f16_f32 v87, v92, v93
	v_cvt_pk_f16_f32 v86, v90, v91
	v_cvt_f32_f16_e32 v64, v157
	v_cvt_f32_f16_sdwa v65, v157 dst_sel:DWORD dst_unused:UNUSED_PAD src0_sel:WORD_1
	s_waitcnt lgkmcnt(0)
	v_mfma_f32_32x32x16_f16 v[66:81], v[82:85], v[86:89], v[66:81]
	v_cvt_f32_f16_e32 v82, v154
	v_cvt_f32_f16_sdwa v83, v154 dst_sel:DWORD dst_unused:UNUSED_PAD src0_sel:WORD_1
	v_fma_f32 v50, -v50, v50, 1.0
	v_fma_f32 v51, -v51, v51, 1.0
	v_cvt_f32_f16_e32 v84, v155
	v_cvt_f32_f16_sdwa v85, v155 dst_sel:DWORD dst_unused:UNUSED_PAD src0_sel:WORD_1
	v_pk_mul_f32 v[98:99], v[34:35], v[50:51]
	v_pk_fma_f32 v[34:35], v[52:53], v[52:53], 1.0 op_sel_hi:[1,1,0] neg_lo:[1,0,0] neg_hi:[1,0,0]
	v_cvt_f32_f16_sdwa v95, v152 dst_sel:DWORD dst_unused:UNUSED_PAD src0_sel:WORD_1
	v_pk_mul_f32 v[100:101], v[36:37], v[34:35]
	v_pk_fma_f32 v[34:35], v[62:63], v[62:63], 1.0 op_sel_hi:[1,1,0] neg_lo:[1,0,0] neg_hi:[1,0,0]
	ds_read_b128 v[90:93], v134 offset:36864
	v_pk_mul_f32 v[38:39], v[38:39], v[34:35]
	v_pk_fma_f32 v[34:35], v[64:65], v[64:65], 1.0 op_sel_hi:[1,1,0] neg_lo:[1,0,0] neg_hi:[1,0,0]
	v_mfma_f32_32x32x16_f16 v[50:65], v[58:61], v[54:57], 0
	v_mul_f32_e64 v40, v40, v34
	v_mul_f32_e64 v41, v41, v35
	v_fma_f32 v34, -v82, v82, 1.0
	v_fma_f32 v35, -v83, v83, 1.0
	v_cvt_pk_f16_f32 v41, v40, v41
	v_pk_mul_f32 v[82:83], v[42:43], v[34:35]
	v_pk_fma_f32 v[34:35], v[84:85], v[84:85], 1.0 op_sel_hi:[1,1,0] neg_lo:[1,0,0] neg_hi:[1,0,0]
	v_cvt_pk_f16_f32 v40, v38, v39
	v_pk_mul_f32 v[84:85], v[44:45], v[34:35]
	v_pk_fma_f32 v[34:35], v[94:95], v[94:95], 1.0 op_sel_hi:[1,1,0] neg_lo:[1,0,0] neg_hi:[1,0,0]
	v_cvt_pk_f16_f32 v39, v100, v101
	v_pk_mul_f32 v[46:47], v[46:47], v[34:35]
	ds_read_b128 v[34:37], v134 offset:37888
	v_cvt_pk_f16_f32 v38, v98, v99
	v_cvt_f32_f16_e32 v96, v153
	v_cvt_f32_f16_sdwa v97, v153 dst_sel:DWORD dst_unused:UNUSED_PAD src0_sel:WORD_1
	s_waitcnt lgkmcnt(0)
	v_mfma_f32_32x32x16_f16 v[66:81], v[34:37], v[38:41], v[66:81]
	v_cvt_f32_f16_e32 v34, v150
	v_cvt_f32_f16_sdwa v35, v150 dst_sel:DWORD dst_unused:UNUSED_PAD src0_sel:WORD_1
	v_cvt_f32_f16_e32 v36, v151
	v_cvt_f32_f16_sdwa v37, v151 dst_sel:DWORD dst_unused:UNUSED_PAD src0_sel:WORD_1
	v_fma_f32 v42, -v96, v96, 1.0
	v_fma_f32 v43, -v97, v97, 1.0
	v_pk_fma_f32 v[34:35], v[34:35], v[34:35], 1.0 op_sel_hi:[1,1,0] neg_lo:[1,0,0] neg_hi:[1,0,0]
	v_pk_mul_f32 v[48:49], v[48:49], v[42:43]
	v_mfma_f32_32x32x16_f16 v[50:65], v[90:93], v[86:89], v[50:65]
	v_cvt_f32_f16_e32 v86, v148
	v_cvt_f32_f16_sdwa v87, v148 dst_sel:DWORD dst_unused:UNUSED_PAD src0_sel:WORD_1
	v_cvt_f32_f16_e32 v88, v149
	v_cvt_f32_f16_sdwa v89, v149 dst_sel:DWORD dst_unused:UNUSED_PAD src0_sel:WORD_1
	v_cvt_f32_f16_e32 v90, v146
	v_cvt_f32_f16_sdwa v91, v146 dst_sel:DWORD dst_unused:UNUSED_PAD src0_sel:WORD_1
	ds_read_b128 v[42:45], v134 offset:38912
	v_cvt_f32_f16_e32 v92, v147
	v_cvt_f32_f16_sdwa v93, v147 dst_sel:DWORD dst_unused:UNUSED_PAD src0_sel:WORD_1
	v_pk_mul_f32 v[34:35], v[18:19], v[34:35]
	v_pk_fma_f32 v[18:19], v[36:37], v[36:37], 1.0 op_sel_hi:[1,1,0] neg_lo:[1,0,0] neg_hi:[1,0,0]
	v_cvt_f32_f16_e32 v94, v144
	v_cvt_f32_f16_sdwa v95, v144 dst_sel:DWORD dst_unused:UNUSED_PAD src0_sel:WORD_1
	v_pk_mul_f32 v[36:37], v[20:21], v[18:19]
	v_pk_fma_f32 v[18:19], v[86:87], v[86:87], 1.0 op_sel_hi:[1,1,0] neg_lo:[1,0,0] neg_hi:[1,0,0]
	v_cvt_f32_f16_e32 v96, v145
	v_pk_mul_f32 v[86:87], v[22:23], v[18:19]
	v_pk_fma_f32 v[18:19], v[88:89], v[88:89], 1.0 op_sel_hi:[1,1,0] neg_lo:[1,0,0] neg_hi:[1,0,0]
	v_cvt_f32_f16_sdwa v97, v145 dst_sel:DWORD dst_unused:UNUSED_PAD src0_sel:WORD_1
	v_pk_mul_f32 v[88:89], v[24:25], v[18:19]
	v_pk_fma_f32 v[18:19], v[90:91], v[90:91], 1.0 op_sel_hi:[1,1,0] neg_lo:[1,0,0] neg_hi:[1,0,0]
	v_cvt_pk_f16_f32 v25, v48, v49
	v_pk_mul_f32 v[90:91], v[26:27], v[18:19]
	v_pk_fma_f32 v[18:19], v[92:93], v[92:93], 1.0 op_sel_hi:[1,1,0] neg_lo:[1,0,0] neg_hi:[1,0,0]
	v_cvt_pk_f16_f32 v24, v46, v47
	v_pk_mul_f32 v[92:93], v[28:29], v[18:19]
	v_pk_fma_f32 v[18:19], v[94:95], v[94:95], 1.0 op_sel_hi:[1,1,0] neg_lo:[1,0,0] neg_hi:[1,0,0]
	ds_read_b128 v[26:29], v134 offset:40960
	v_pk_mul_f32 v[30:31], v[30:31], v[18:19]
	ds_read_b128 v[18:21], v134 offset:39936
	s_waitcnt lgkmcnt(2)
	v_mfma_f32_32x32x16_f16 v[50:65], v[42:45], v[38:41], v[50:65]
	v_cvt_f32_f16_e32 v40, v142
	v_cvt_f32_f16_sdwa v41, v142 dst_sel:DWORD dst_unused:UNUSED_PAD src0_sel:WORD_1
	v_fma_f32 v38, -v96, v96, 1.0
	v_fma_f32 v39, -v97, v97, 1.0
	v_cvt_pk_f16_f32 v23, v84, v85
	v_cvt_pk_f16_f32 v22, v82, v83
	v_pk_mul_f32 v[32:33], v[32:33], v[38:39]
	v_cvt_f32_f16_e32 v38, v143
	s_waitcnt lgkmcnt(0)
	v_mfma_f32_32x32x16_f16 v[66:81], v[18:21], v[22:25], v[66:81]
	v_cvt_f32_f16_sdwa v39, v143 dst_sel:DWORD dst_unused:UNUSED_PAD src0_sel:WORD_1
	v_fma_f32 v18, -v40, v40, 1.0
	v_fma_f32 v19, -v41, v41, 1.0
	s_or_b32 s6, s6, s7
	v_mul_f32_e64 v40, v2, v18
	v_mul_f32_e64 v41, v3, v19
	ds_read_b128 v[18:21], v134 offset:41984
	v_pk_fma_f32 v[2:3], v[38:39], v[38:39], 1.0 op_sel_hi:[1,1,0] neg_lo:[1,0,0] neg_hi:[1,0,0]
	v_cvt_f32_f16_e32 v38, v140
	v_mfma_f32_32x32x16_f16 v[50:65], v[26:29], v[22:25], v[50:65]
	ds_read_b128 v[26:29], v134 offset:43008
	v_cvt_f32_f16_sdwa v39, v140 dst_sel:DWORD dst_unused:UNUSED_PAD src0_sel:WORD_1
	v_cvt_pk_f16_f32 v22, v34, v35
	v_mul_f32_e64 v34, v4, v2
	v_mul_f32_e64 v35, v5, v3
	v_cvt_pk_f16_f32 v25, v88, v89
	v_pk_fma_f32 v[2:3], v[38:39], v[38:39], 1.0 op_sel_hi:[1,1,0] neg_lo:[1,0,0] neg_hi:[1,0,0]
	v_cvt_pk_f16_f32 v24, v86, v87
	v_cvt_pk_f16_f32 v23, v36, v37
	v_pk_mul_f32 v[6:7], v[6:7], v[2:3]
	ds_read_b128 v[2:5], v134 offset:44032
	s_waitcnt lgkmcnt(2)
	v_mfma_f32_32x32x16_f16 v[66:81], v[18:21], v[22:25], v[66:81]
	v_cvt_f32_f16_e32 v18, v141
	v_cvt_f32_f16_sdwa v19, v141 dst_sel:DWORD dst_unused:UNUSED_PAD src0_sel:WORD_1
	v_cvt_pk_f16_f32 v21, v32, v33
	v_cvt_pk_f16_f32 v20, v30, v31
	s_ashr_i32 s7, s6, 31
	s_lshl_b64 s[6:7], s[6:7], 12
	s_add_u32 s2, s2, s6
	s_waitcnt lgkmcnt(1)
	v_mfma_f32_32x32x16_f16 v[50:65], v[26:29], v[22:25], v[50:65]
	ds_read_b128 v[22:25], v134 offset:45056
	v_cvt_f32_f16_e32 v28, v138
	v_cvt_f32_f16_sdwa v29, v138 dst_sel:DWORD dst_unused:UNUSED_PAD src0_sel:WORD_1
	v_fma_f32 v26, -v18, v18, 1.0
	v_fma_f32 v27, -v19, v19, 1.0
	v_cvt_pk_f16_f32 v19, v92, v93
	v_cvt_pk_f16_f32 v18, v90, v91
	v_pk_mul_f32 v[8:9], v[8:9], v[26:27]
	v_cvt_f32_f16_e32 v26, v139
	s_waitcnt lgkmcnt(1)
	v_mfma_f32_32x32x16_f16 v[66:81], v[2:5], v[18:21], v[66:81]
	v_fma_f32 v2, -v28, v28, 1.0
	v_fma_f32 v3, -v29, v29, 1.0
	v_cvt_f32_f16_sdwa v27, v139 dst_sel:DWORD dst_unused:UNUSED_PAD src0_sel:WORD_1
	v_mul_f32_e64 v10, v10, v2
	v_mul_f32_e64 v11, v11, v3
	ds_read_b128 v[2:5], v134 offset:46080
	v_cvt_pk_f16_f32 v9, v8, v9
	v_cvt_pk_f16_f32 v8, v6, v7
	v_cvt_pk_f16_f32 v7, v34, v35
	s_waitcnt lgkmcnt(1)
	v_mfma_f32_32x32x16_f16 v[50:65], v[22:25], v[18:21], v[50:65]
	ds_read_b128 v[18:21], v134 offset:47104
	v_fma_f32 v22, -v26, v26, 1.0
	v_fma_f32 v23, -v27, v27, 1.0
	v_cvt_f32_f16_e32 v24, v136
	v_cvt_f32_f16_sdwa v25, v136 dst_sel:DWORD dst_unused:UNUSED_PAD src0_sel:WORD_1
	v_pk_mul_f32 v[12:13], v[12:13], v[22:23]
	v_cvt_f32_f16_e32 v22, v137
	v_cvt_f32_f16_sdwa v23, v137 dst_sel:DWORD dst_unused:UNUSED_PAD src0_sel:WORD_1
	v_cvt_pk_f16_f32 v6, v40, v41
	s_addc_u32 s3, s3, s7
	s_waitcnt lgkmcnt(1)
	v_mfma_f32_32x32x16_f16 v[66:81], v[2:5], v[6:9], v[66:81]
	v_fma_f32 v2, -v24, v24, 1.0
	v_fma_f32 v3, -v25, v25, 1.0
	v_mul_f32_e64 v14, v14, v2
	v_mul_f32_e64 v15, v15, v3
	ds_read_b128 v[2:5], v134 offset:48128
	s_waitcnt lgkmcnt(1)
	v_mfma_f32_32x32x16_f16 v[50:65], v[18:21], v[6:9], v[50:65]
	v_fma_f32 v6, -v22, v22, 1.0
	v_fma_f32 v7, -v23, v23, 1.0
	v_cvt_pk_f16_f32 v8, v14, v15
	v_mul_f32_e64 v6, v16, v6
	v_mul_f32_e64 v7, v17, v7
	v_cvt_pk_f16_f32 v9, v6, v7
	v_cvt_pk_f16_f32 v7, v12, v13
	v_cvt_pk_f16_f32 v6, v10, v11
	ds_read_b128 v[10:13], v134 offset:49152
	s_waitcnt lgkmcnt(1)
	v_mfma_f32_32x32x16_f16 v[66:81], v[2:5], v[6:9], v[66:81]
	s_waitcnt lgkmcnt(0)
	v_mfma_f32_32x32x16_f16 v[50:65], v[10:13], v[6:9], v[50:65]
	s_nop 9
	v_cvt_pk_f16_f32 v5, v72, v73
	v_cvt_pk_f16_f32 v4, v70, v71
	v_cvt_pk_f16_f32 v3, v68, v69
	v_cvt_pk_f16_f32 v2, v66, v67
	global_store_dwordx4 v134, v[2:5], s[2:3] sc1
	s_nop 1
	v_cvt_pk_f16_f32 v5, v80, v81
	v_cvt_pk_f16_f32 v4, v78, v79
	v_cvt_pk_f16_f32 v3, v76, v77
	v_cvt_pk_f16_f32 v2, v74, v75
	global_store_dwordx4 v134, v[2:5], s[2:3] offset:1024 sc1
	s_nop 1
	v_cvt_pk_f16_f32 v5, v56, v57
	v_cvt_pk_f16_f32 v4, v54, v55
	v_cvt_pk_f16_f32 v3, v52, v53
	v_cvt_pk_f16_f32 v2, v50, v51
	global_store_dwordx4 v134, v[2:5], s[2:3] offset:2048 sc1
	s_nop 1
	v_cvt_pk_f16_f32 v5, v64, v65
	v_cvt_pk_f16_f32 v4, v62, v63
	v_cvt_pk_f16_f32 v3, v60, v61
	v_cvt_pk_f16_f32 v2, v58, v59
	global_store_dwordx4 v134, v[2:5], s[2:3] offset:3072 sc1
	s_cbranch_execnz .LBB3_2
.LBB3_4:
	s_load_dwordx2 s[6:7], s[0:1], 0x0
	s_load_dwordx2 s[2:3], s[0:1], 0x38
	s_lshr_b32 s0, s8, 6
	s_lshl_b32 s1, s4, 8
	s_lshl_b32 s8, s5, 7
	s_add_i32 s8, s8, s1
	s_ashr_i32 s9, s8, 31
	s_lshl_b64 s[8:9], s[8:9], 10
	s_waitcnt lgkmcnt(0)
	s_add_u32 s6, s6, s8
	s_addc_u32 s7, s7, s9
	v_mov_b32_e32 v135, 0
	v_lshl_add_u64 v[2:3], s[6:7], 0, v[134:135]
	s_mov_b32 s1, 0x10000
	v_add_co_u32_e32 v36, vcc, s1, v2
	s_mov_b32 s1, 0x11000
	s_nop 0
	v_addc_co_u32_e32 v37, vcc, 0, v3, vcc
	v_add_co_u32_e32 v68, vcc, s1, v2
	global_load_dwordx4 v[4:7], v134, s[6:7]
	global_load_dwordx4 v[8:11], v134, s[6:7] offset:1024
	global_load_dwordx4 v[12:15], v134, s[6:7] offset:2048
	v_addc_co_u32_e32 v69, vcc, 0, v3, vcc
	global_load_dwordx4 v[16:19], v134, s[6:7] offset:3072
	global_load_dwordx4 v[20:23], v[68:69], off offset:-4096
	global_load_dwordx4 v[24:27], v[36:37], off offset:1024
	global_load_dwordx4 v[28:31], v[36:37], off offset:2048
	global_load_dwordx4 v[32:35], v[36:37], off offset:3072
	s_movk_i32 s7, 0x2000
	v_add_co_u32_e32 v100, vcc, s7, v2
	s_movk_i32 s6, 0x1000
	s_nop 0
	v_addc_co_u32_e32 v101, vcc, 0, v3, vcc
	v_add_co_u32_e32 v70, vcc, s6, v2
	global_load_dwordx4 v[36:39], v[100:101], off offset:-4096
	s_nop 0
	v_addc_co_u32_e32 v71, vcc, 0, v3, vcc
	global_load_dwordx4 v[40:43], v[70:71], off offset:1024
	global_load_dwordx4 v[44:47], v[70:71], off offset:2048
	global_load_dwordx4 v[48:51], v[70:71], off offset:3072
	global_load_dwordx4 v[52:55], v[68:69], off
	global_load_dwordx4 v[56:59], v[68:69], off offset:1024
	global_load_dwordx4 v[60:63], v[68:69], off offset:2048
	global_load_dwordx4 v[64:67], v[68:69], off offset:3072
	s_mov_b32 s1, 0x12000
	v_add_co_u32_e32 v102, vcc, s1, v2
	s_mov_b32 s8, 0x13000
	s_nop 0
	v_addc_co_u32_e32 v103, vcc, 0, v3, vcc
	v_add_co_u32_e32 v104, vcc, s8, v2
	s_movk_i32 s9, 0x4000
	s_nop 0
	v_addc_co_u32_e32 v105, vcc, 0, v3, vcc
	v_add_co_u32_e32 v106, vcc, s9, v2
	global_load_dwordx4 v[68:71], v[100:101], off
	global_load_dwordx4 v[72:75], v[100:101], off offset:1024
	global_load_dwordx4 v[76:79], v[100:101], off offset:2048
	global_load_dwordx4 v[80:83], v[100:101], off offset:3072
	global_load_dwordx4 v[84:87], v[104:105], off offset:-4096
	global_load_dwordx4 v[88:91], v[102:103], off offset:1024
	global_load_dwordx4 v[92:95], v[102:103], off offset:2048
	global_load_dwordx4 v[96:99], v[102:103], off offset:3072
	v_lshl_or_b32 v1, s5, 13, v134
	s_movk_i32 s5, 0x3000
	v_addc_co_u32_e32 v107, vcc, 0, v3, vcc
	v_add_co_u32_e32 v108, vcc, s5, v2
	s_mov_b32 s8, 0x14000
	s_nop 0
	v_addc_co_u32_e32 v109, vcc, 0, v3, vcc
	s_ashr_i32 s5, s4, 31
	s_lshl_b32 s10, s0, 13
	s_lshl_b64 s[0:1], s[4:5], 14
	v_add_co_u32_e32 v100, vcc, s8, v2
	s_mov_b32 s9, 0x15000
	s_add_u32 s0, s2, s0
	v_addc_co_u32_e32 v101, vcc, 0, v3, vcc
	s_addc_u32 s1, s3, s1
	s_and_b32 s2, s10, 0x6000
	v_add_co_u32_e32 v102, vcc, s9, v2
	s_movk_i32 s3, 0x5000
	s_nop 0
	v_addc_co_u32_e32 v103, vcc, 0, v3, vcc
	s_waitcnt vmcnt(23)
	ds_write_b128 v1, v[4:7]
	s_waitcnt vmcnt(22)
	ds_write_b128 v1, v[8:11] offset:1024
	s_waitcnt vmcnt(21)
	ds_write_b128 v1, v[12:15] offset:2048
	s_waitcnt vmcnt(20)
	ds_write_b128 v1, v[16:19] offset:3072
	s_waitcnt vmcnt(19)
	ds_write_b128 v1, v[20:23] offset:4096
	s_waitcnt vmcnt(18)
	ds_write_b128 v1, v[24:27] offset:5120
	s_waitcnt vmcnt(17)
	ds_write_b128 v1, v[28:31] offset:6144
	s_waitcnt vmcnt(16)
	ds_write_b128 v1, v[32:35] offset:7168
	s_waitcnt lgkmcnt(0)
	s_barrier
	global_load_dwordx4 v[4:7], v[106:107], off offset:-4096
	global_load_dwordx4 v[8:11], v[108:109], off offset:1024
	global_load_dwordx4 v[12:15], v[108:109], off offset:2048
	global_load_dwordx4 v[16:19], v[108:109], off offset:3072
	global_load_dwordx4 v[20:23], v[104:105], off
	global_load_dwordx4 v[24:27], v[104:105], off offset:1024
	global_load_dwordx4 v[28:31], v[104:105], off offset:2048
	global_load_dwordx4 v[32:35], v[104:105], off offset:3072
	v_or_b32_e32 v1, s2, v134
	s_waitcnt vmcnt(23)
	ds_write_b128 v1, v[36:39] offset:16384
	s_waitcnt vmcnt(22)
	ds_write_b128 v1, v[40:43] offset:17408
	s_waitcnt vmcnt(21)
	ds_write_b128 v1, v[44:47] offset:18432
	s_waitcnt vmcnt(20)
	ds_write_b128 v1, v[48:51] offset:19456
	s_waitcnt vmcnt(19)
	ds_write_b128 v1, v[52:55] offset:20480
	s_waitcnt vmcnt(18)
	ds_write_b128 v1, v[56:59] offset:21504
	s_waitcnt vmcnt(17)
	ds_write_b128 v1, v[60:63] offset:22528
	s_waitcnt vmcnt(16)
	ds_write_b128 v1, v[64:67] offset:23552
	s_waitcnt lgkmcnt(0)
	s_barrier
	global_load_dwordx4 v[36:39], v[106:107], off
	global_load_dwordx4 v[40:43], v[106:107], off offset:1024
	global_load_dwordx4 v[44:47], v[106:107], off offset:2048
	global_load_dwordx4 v[48:51], v[106:107], off offset:3072
	global_load_dwordx4 v[52:55], v[102:103], off offset:-4096
	global_load_dwordx4 v[56:59], v[100:101], off offset:1024
	global_load_dwordx4 v[60:63], v[100:101], off offset:2048
	global_load_dwordx4 v[64:67], v[100:101], off offset:3072
	s_movk_i32 s2, 0x6000
	v_add_co_u32_e32 v100, vcc, s2, v2
	s_waitcnt vmcnt(23)
	ds_write_b128 v1, v[68:71]
	s_waitcnt vmcnt(22)
	ds_write_b128 v1, v[72:75] offset:1024
	s_waitcnt vmcnt(21)
	ds_write_b128 v1, v[76:79] offset:2048
	s_waitcnt vmcnt(20)
	ds_write_b128 v1, v[80:83] offset:3072
	s_waitcnt vmcnt(19)
	ds_write_b128 v1, v[84:87] offset:4096
	s_waitcnt vmcnt(18)
	ds_write_b128 v1, v[88:91] offset:5120
	s_waitcnt vmcnt(17)
	ds_write_b128 v1, v[92:95] offset:6144
	s_waitcnt vmcnt(16)
	ds_write_b128 v1, v[96:99] offset:7168
	v_addc_co_u32_e32 v101, vcc, 0, v3, vcc
	v_add_co_u32_e32 v104, vcc, s3, v2
	s_waitcnt lgkmcnt(0)
	s_nop 0
	v_addc_co_u32_e32 v105, vcc, 0, v3, vcc
	s_barrier
	global_load_dwordx4 v[68:71], v[104:105], off offset:1024
	global_load_dwordx4 v[72:75], v[104:105], off offset:2048
	global_load_dwordx4 v[76:79], v[104:105], off offset:3072
	global_load_dwordx4 v[80:83], v[102:103], off
	global_load_dwordx4 v[84:87], v[102:103], off offset:1024
	global_load_dwordx4 v[88:91], v[102:103], off offset:2048
	global_load_dwordx4 v[92:95], v[100:101], off offset:-4096
	global_load_dwordx4 v[96:99], v[102:103], off offset:3072
	s_mov_b32 s2, 0x16000
	v_add_co_u32_e32 v102, vcc, s2, v2
	s_mov_b32 s3, 0x17000
	s_nop 0
	v_addc_co_u32_e32 v103, vcc, 0, v3, vcc
	v_add_co_u32_e32 v104, vcc, s3, v2
	s_mov_b32 s3, 0x8000
	s_nop 0
	v_addc_co_u32_e32 v105, vcc, 0, v3, vcc
	s_movk_i32 s2, 0x7000
	v_lshlrev_b32_e32 v134, 4, v0
	s_waitcnt vmcnt(23)
	ds_write_b128 v1, v[4:7] offset:16384
	s_waitcnt vmcnt(22)
	ds_write_b128 v1, v[8:11] offset:17408
	s_waitcnt vmcnt(21)
	ds_write_b128 v1, v[12:15] offset:18432
	s_waitcnt vmcnt(20)
	ds_write_b128 v1, v[16:19] offset:19456
	s_waitcnt vmcnt(19)
	ds_write_b128 v1, v[20:23] offset:20480
	s_waitcnt vmcnt(18)
	ds_write_b128 v1, v[24:27] offset:21504
	s_waitcnt vmcnt(17)
	ds_write_b128 v1, v[28:31] offset:22528
	s_waitcnt vmcnt(16)
	ds_write_b128 v1, v[32:35] offset:23552
	s_waitcnt lgkmcnt(0)
	s_barrier
	global_load_dwordx4 v[4:7], v[100:101], off
	global_load_dwordx4 v[8:11], v[100:101], off offset:1024
	global_load_dwordx4 v[12:15], v[100:101], off offset:2048
	global_load_dwordx4 v[16:19], v[100:101], off offset:3072
	global_load_dwordx4 v[20:23], v[104:105], off offset:-4096
	global_load_dwordx4 v[24:27], v[102:103], off offset:1024
	global_load_dwordx4 v[28:31], v[102:103], off offset:2048
	global_load_dwordx4 v[32:35], v[102:103], off offset:3072
	v_add_co_u32_e32 v100, vcc, s3, v2
	s_waitcnt vmcnt(23)
	ds_write_b128 v1, v[36:39]
	s_waitcnt vmcnt(22)
	ds_write_b128 v1, v[40:43] offset:1024
	s_waitcnt vmcnt(21)
	ds_write_b128 v1, v[44:47] offset:2048
	v_addc_co_u32_e32 v101, vcc, 0, v3, vcc
	v_add_co_u32_e32 v102, vcc, s2, v2
	s_waitcnt vmcnt(20)
	ds_write_b128 v1, v[48:51] offset:3072
	v_addc_co_u32_e32 v103, vcc, 0, v3, vcc
	s_waitcnt vmcnt(19)
	ds_write_b128 v1, v[52:55] offset:4096
	s_waitcnt vmcnt(18)
	ds_write_b128 v1, v[56:59] offset:5120
	s_waitcnt vmcnt(17)
	ds_write_b128 v1, v[60:63] offset:6144
	s_waitcnt vmcnt(16)
	ds_write_b128 v1, v[64:67] offset:7168
	s_waitcnt lgkmcnt(0)
	s_barrier
	global_load_dwordx4 v[36:39], v[100:101], off offset:-4096
	global_load_dwordx4 v[40:43], v[102:103], off offset:1024
	global_load_dwordx4 v[44:47], v[102:103], off offset:2048
	global_load_dwordx4 v[48:51], v[102:103], off offset:3072
	global_load_dwordx4 v[52:55], v[104:105], off
	global_load_dwordx4 v[56:59], v[104:105], off offset:1024
	global_load_dwordx4 v[60:63], v[104:105], off offset:2048
	global_load_dwordx4 v[64:67], v[104:105], off offset:3072
	s_mov_b32 s2, 0x18000
	v_add_co_u32_e32 v102, vcc, s2, v2
	s_mov_b32 s3, 0x19000
	s_nop 0
	v_addc_co_u32_e32 v103, vcc, 0, v3, vcc
	v_add_co_u32_e32 v104, vcc, s3, v2
	s_waitcnt vmcnt(17)
	ds_write_b128 v1, v[92:95] offset:16384
	ds_write_b128 v1, v[68:71] offset:17408
	ds_write_b128 v1, v[72:75] offset:18432
	ds_write_b128 v1, v[76:79] offset:19456
	ds_write_b128 v1, v[80:83] offset:20480
	ds_write_b128 v1, v[84:87] offset:21504
	ds_write_b128 v1, v[88:91] offset:22528
	s_waitcnt vmcnt(16)
	ds_write_b128 v1, v[96:99] offset:23552
	v_addc_co_u32_e32 v105, vcc, 0, v3, vcc
	s_waitcnt lgkmcnt(0)
	s_barrier
	global_load_dwordx4 v[68:71], v[100:101], off
	global_load_dwordx4 v[72:75], v[100:101], off offset:1024
	global_load_dwordx4 v[76:79], v[100:101], off offset:2048
	global_load_dwordx4 v[80:83], v[100:101], off offset:3072
	global_load_dwordx4 v[84:87], v[104:105], off offset:-4096
	global_load_dwordx4 v[88:91], v[102:103], off offset:1024
	global_load_dwordx4 v[92:95], v[102:103], off offset:2048
	s_mov_b32 s3, 0xa000
	v_add_co_u32_e32 v100, vcc, s3, v2
	s_mov_b32 s2, 0x9000
	s_nop 0
	v_addc_co_u32_e32 v101, vcc, 0, v3, vcc
	s_mov_b32 s3, 0xc000
	s_waitcnt vmcnt(22)
	ds_write_b128 v1, v[4:7]
	s_waitcnt vmcnt(21)
	ds_write_b128 v1, v[8:11] offset:1024
	s_waitcnt vmcnt(20)
	ds_write_b128 v1, v[12:15] offset:2048
	global_load_dwordx4 v[4:7], v[102:103], off offset:3072
	s_waitcnt vmcnt(20)
	ds_write_b128 v1, v[16:19] offset:3072
	s_waitcnt vmcnt(19)
	ds_write_b128 v1, v[20:23] offset:4096
	s_waitcnt vmcnt(18)
	ds_write_b128 v1, v[24:27] offset:5120
	s_waitcnt vmcnt(17)
	ds_write_b128 v1, v[28:31] offset:6144
	s_waitcnt vmcnt(16)
	ds_write_b128 v1, v[32:35] offset:7168
	s_waitcnt lgkmcnt(0)
	s_barrier
	global_load_dwordx4 v[8:11], v[100:101], off offset:-4096
	v_add_co_u32_e32 v102, vcc, s2, v2
	s_mov_b32 s2, 0x1a000
	s_nop 0
	v_addc_co_u32_e32 v103, vcc, 0, v3, vcc
	global_load_dwordx4 v[12:15], v[102:103], off offset:1024
	global_load_dwordx4 v[16:19], v[102:103], off offset:2048
	global_load_dwordx4 v[20:23], v[102:103], off offset:3072
	global_load_dwordx4 v[24:27], v[104:105], off
	global_load_dwordx4 v[28:31], v[104:105], off offset:1024
	global_load_dwordx4 v[32:35], v[104:105], off offset:2048
	global_load_dwordx4 v[96:99], v[104:105], off offset:3072
	v_add_co_u32_e32 v102, vcc, s2, v2
	s_mov_b32 s2, 0x1b000
	s_nop 0
	v_addc_co_u32_e32 v103, vcc, 0, v3, vcc
	s_waitcnt vmcnt(23)
	ds_write_b128 v1, v[36:39] offset:16384
	s_waitcnt vmcnt(22)
	ds_write_b128 v1, v[40:43] offset:17408
	s_waitcnt vmcnt(21)
	ds_write_b128 v1, v[44:47] offset:18432
	s_waitcnt vmcnt(20)
	ds_write_b128 v1, v[48:51] offset:19456
	s_waitcnt vmcnt(19)
	ds_write_b128 v1, v[52:55] offset:20480
	s_waitcnt vmcnt(18)
	ds_write_b128 v1, v[56:59] offset:21504
	s_waitcnt vmcnt(17)
	ds_write_b128 v1, v[60:63] offset:22528
	s_waitcnt vmcnt(16)
	ds_write_b128 v1, v[64:67] offset:23552
	s_waitcnt lgkmcnt(0)
	s_barrier
	global_load_dwordx4 v[36:39], v[100:101], off
	global_load_dwordx4 v[40:43], v[100:101], off offset:1024
	global_load_dwordx4 v[44:47], v[100:101], off offset:2048
	v_add_co_u32_e32 v104, vcc, s2, v2
	s_mov_b32 s2, 0xb000
	s_nop 0
	v_addc_co_u32_e32 v105, vcc, 0, v3, vcc
	global_load_dwordx4 v[48:51], v[100:101], off offset:3072
	global_load_dwordx4 v[52:55], v[104:105], off offset:-4096
	global_load_dwordx4 v[56:59], v[102:103], off offset:1024
	global_load_dwordx4 v[60:63], v[102:103], off offset:2048
	global_load_dwordx4 v[64:67], v[102:103], off offset:3072
	s_waitcnt vmcnt(23)
	ds_write_b128 v1, v[68:71]
	s_waitcnt vmcnt(22)
	ds_write_b128 v1, v[72:75] offset:1024
	s_waitcnt vmcnt(21)
	ds_write_b128 v1, v[76:79] offset:2048
	s_waitcnt vmcnt(20)
	ds_write_b128 v1, v[80:83] offset:3072
	s_waitcnt vmcnt(19)
	ds_write_b128 v1, v[84:87] offset:4096
	s_waitcnt vmcnt(18)
	ds_write_b128 v1, v[88:91] offset:5120
	s_waitcnt vmcnt(17)
	ds_write_b128 v1, v[92:95] offset:6144
	s_waitcnt vmcnt(16)
	ds_write_b128 v1, v[4:7] offset:7168
	v_add_co_u32_e32 v84, vcc, s3, v2
	s_waitcnt lgkmcnt(0)
	s_nop 0
	v_addc_co_u32_e32 v85, vcc, 0, v3, vcc
	v_add_co_u32_e32 v80, vcc, s2, v2
	s_barrier
	s_nop 0
	v_addc_co_u32_e32 v81, vcc, 0, v3, vcc
	global_load_dwordx4 v[4:7], v[84:85], off offset:-4096
	global_load_dwordx4 v[68:71], v[80:81], off offset:1024
	global_load_dwordx4 v[72:75], v[80:81], off offset:2048
	s_waitcnt vmcnt(18)
	ds_write_b128 v1, v[8:11] offset:16384
	global_load_dwordx4 v[8:11], v[80:81], off offset:3072
	global_load_dwordx4 v[76:79], v[104:105], off
	s_waitcnt vmcnt(19)
	ds_write_b128 v1, v[12:15] offset:17408
	s_waitcnt vmcnt(18)
	ds_write_b128 v1, v[16:19] offset:18432
	s_mov_b32 s2, 0x1c000
	global_load_dwordx4 v[12:15], v[104:105], off offset:1024
	global_load_dwordx4 v[16:19], v[104:105], off offset:2048
	global_load_dwordx4 v[80:83], v[104:105], off offset:3072
	v_add_co_u32_e32 v88, vcc, s2, v2
	s_mov_b32 s2, 0x1d000
	s_nop 0
	v_addc_co_u32_e32 v89, vcc, 0, v3, vcc
	v_add_co_u32_e32 v100, vcc, s2, v2
	s_mov_b32 s3, 0xe000
	s_nop 0
	v_addc_co_u32_e32 v101, vcc, 0, v3, vcc
	s_waitcnt vmcnt(20)
	ds_write_b128 v1, v[20:23] offset:19456
	s_waitcnt vmcnt(19)
	ds_write_b128 v1, v[24:27] offset:20480
	s_waitcnt vmcnt(18)
	ds_write_b128 v1, v[28:31] offset:21504
	s_waitcnt vmcnt(17)
	ds_write_b128 v1, v[32:35] offset:22528
	s_waitcnt vmcnt(16)
	ds_write_b128 v1, v[96:99] offset:23552
	s_waitcnt lgkmcnt(0)
	s_barrier
	global_load_dwordx4 v[20:23], v[84:85], off
	global_load_dwordx4 v[24:27], v[84:85], off offset:1024
	global_load_dwordx4 v[28:31], v[84:85], off offset:2048
	s_waitcnt vmcnt(18)
	ds_write_b128 v1, v[36:39]
	v_add_co_u32_e32 v102, vcc, s3, v2
	global_load_dwordx4 v[32:35], v[84:85], off offset:3072
	global_load_dwordx4 v[36:39], v[100:101], off offset:-4096
	s_waitcnt vmcnt(19)
	ds_write_b128 v1, v[40:43] offset:1024
	s_waitcnt vmcnt(18)
	ds_write_b128 v1, v[44:47] offset:2048
	s_mov_b32 s2, 0xd000
	v_addc_co_u32_e32 v103, vcc, 0, v3, vcc
	global_load_dwordx4 v[40:43], v[88:89], off offset:1024
	global_load_dwordx4 v[44:47], v[88:89], off offset:2048
	global_load_dwordx4 v[84:87], v[88:89], off offset:3072
	s_waitcnt vmcnt(20)
	ds_write_b128 v1, v[48:51] offset:3072
	s_waitcnt vmcnt(19)
	ds_write_b128 v1, v[52:55] offset:4096
	s_waitcnt vmcnt(18)
	ds_write_b128 v1, v[56:59] offset:5120
	s_waitcnt vmcnt(17)
	ds_write_b128 v1, v[60:63] offset:6144
	s_waitcnt vmcnt(16)
	ds_write_b128 v1, v[64:67] offset:7168
	s_waitcnt lgkmcnt(0)
	s_barrier
	global_load_dwordx4 v[48:51], v[102:103], off offset:-4096
	v_add_co_u32_e32 v104, vcc, s2, v2
	s_mov_b32 s2, 0x1e000
	s_nop 0
	v_addc_co_u32_e32 v105, vcc, 0, v3, vcc
	global_load_dwordx4 v[52:55], v[104:105], off offset:1024
	global_load_dwordx4 v[56:59], v[104:105], off offset:2048
	global_load_dwordx4 v[60:63], v[104:105], off offset:3072
	global_load_dwordx4 v[64:67], v[100:101], off
	global_load_dwordx4 v[88:91], v[100:101], off offset:1024
	global_load_dwordx4 v[92:95], v[100:101], off offset:2048
	global_load_dwordx4 v[96:99], v[100:101], off offset:3072
	v_add_u32_e32 v100, 0xffffff00, v0
	v_ashrrev_i32_e32 v101, 31, v100
	v_lshlrev_b32_e32 v0, 4, v100
	s_waitcnt vmcnt(23)
	ds_write_b128 v1, v[4:7] offset:16384
	s_waitcnt vmcnt(22)
	ds_write_b128 v1, v[68:71] offset:17408
	s_waitcnt vmcnt(21)
	ds_write_b128 v1, v[72:75] offset:18432
	s_waitcnt vmcnt(20)
	ds_write_b128 v1, v[8:11] offset:19456
	s_waitcnt vmcnt(19)
	ds_write_b128 v1, v[76:79] offset:20480
	s_waitcnt vmcnt(18)
	ds_write_b128 v1, v[12:15] offset:21504
	s_waitcnt vmcnt(17)
	ds_write_b128 v1, v[16:19] offset:22528
	s_waitcnt vmcnt(16)
	ds_write_b128 v1, v[80:83] offset:23552
	v_add_co_u32_e32 v68, vcc, s2, v2
	s_mov_b32 s2, 0x1f000
	s_nop 0
	v_addc_co_u32_e32 v69, vcc, 0, v3, vcc
	v_add_co_u32_e32 v76, vcc, s2, v2
	s_waitcnt lgkmcnt(0)
	s_barrier
	global_load_dwordx4 v[4:7], v[102:103], off offset:1024
	global_load_dwordx4 v[8:11], v[102:103], off offset:2048
	v_addc_co_u32_e32 v77, vcc, 0, v3, vcc
	s_waitcnt vmcnt(17)
	ds_write_b128 v1, v[20:23]
	s_mov_b32 s2, 0xf000
	global_load_dwordx4 v[12:15], v[102:103], off offset:3072
	global_load_dwordx4 v[16:19], v[76:77], off offset:-4096
	s_waitcnt vmcnt(18)
	ds_write_b128 v1, v[24:27] offset:1024
	s_waitcnt vmcnt(17)
	ds_write_b128 v1, v[28:31] offset:2048
	v_add_co_u32_e32 v2, vcc, s2, v2
	global_load_dwordx4 v[20:23], v[68:69], off offset:1024
	global_load_dwordx4 v[24:27], v[68:69], off offset:2048
	s_waitcnt vmcnt(18)
	ds_write_b128 v1, v[32:35] offset:3072
	v_addc_co_u32_e32 v3, vcc, 0, v3, vcc
	global_load_dwordx4 v[28:31], v[102:103], off
	global_load_dwordx4 v[32:35], v[68:69], off offset:3072
	s_waitcnt vmcnt(19)
	ds_write_b128 v1, v[36:39] offset:4096
	s_waitcnt vmcnt(18)
	ds_write_b128 v1, v[40:43] offset:5120
	s_waitcnt vmcnt(17)
	ds_write_b128 v1, v[44:47] offset:6144
	s_waitcnt vmcnt(16)
	ds_write_b128 v1, v[84:87] offset:7168
	s_waitcnt lgkmcnt(0)
	s_barrier
	global_load_dwordx4 v[36:39], v[2:3], off
	global_load_dwordx4 v[40:43], v[2:3], off offset:1024
	global_load_dwordx4 v[44:47], v[2:3], off offset:2048
	global_load_dwordx4 v[68:71], v[2:3], off offset:3072
	s_waitcnt vmcnt(19)
	ds_write_b128 v1, v[48:51] offset:16384
	global_load_dwordx4 v[48:51], v[76:77], off
	global_load_dwordx4 v[72:75], v[76:77], off offset:1024
	s_waitcnt vmcnt(20)
	ds_write_b128 v1, v[52:55] offset:17408
	s_waitcnt vmcnt(19)
	ds_write_b128 v1, v[56:59] offset:18432
	v_lshl_add_u64 v[2:3], v[100:101], 4, s[0:1]
	global_load_dwordx4 v[52:55], v[76:77], off offset:2048
	global_load_dwordx4 v[56:59], v[76:77], off offset:3072
	s_waitcnt vmcnt(20)
	ds_write_b128 v1, v[60:63] offset:19456
	s_waitcnt vmcnt(19)
	ds_write_b128 v1, v[64:67] offset:20480
	s_waitcnt vmcnt(18)
	ds_write_b128 v1, v[88:91] offset:21504
	s_waitcnt vmcnt(17)
	ds_write_b128 v1, v[92:95] offset:22528
	s_waitcnt vmcnt(16)
	ds_write_b128 v1, v[96:99] offset:23552
	s_waitcnt lgkmcnt(0)
	s_barrier
	global_load_dwordx4 v[60:63], v[2:3], off
	v_lshl_add_u64 v[2:3], s[0:1], 0, v[134:135]
	v_add_co_u32_e32 v102, vcc, s6, v2
	global_load_dwordx4 v[64:67], v134, s[0:1] offset:-2048
	global_load_dwordx4 v[76:79], v134, s[0:1]
	v_addc_co_u32_e32 v103, vcc, 0, v3, vcc
	v_add_co_u32_e32 v2, vcc, s7, v2
	s_nop 1
	v_addc_co_u32_e32 v3, vcc, 0, v3, vcc
	global_load_dwordx4 v[80:83], v134, s[0:1] offset:2048
	global_load_dwordx4 v[84:87], v[2:3], off offset:-4096
	global_load_dwordx4 v[88:91], v[102:103], off offset:2048
	global_load_dwordx4 v[92:95], v[2:3], off
	global_load_dwordx4 v[96:99], v[2:3], off offset:2048
	s_waitcnt vmcnt(17)
	ds_write_b128 v1, v[28:31]
	ds_write_b128 v1, v[4:7] offset:1024
	ds_write_b128 v1, v[8:11] offset:2048
	ds_write_b128 v1, v[12:15] offset:3072
	ds_write_b128 v1, v[16:19] offset:4096
	ds_write_b128 v1, v[20:23] offset:5120
	ds_write_b128 v1, v[24:27] offset:6144
	s_waitcnt vmcnt(16)
	ds_write_b128 v1, v[32:35] offset:7168
	s_waitcnt lgkmcnt(0)
	s_barrier
	s_waitcnt vmcnt(15)
	ds_write_b128 v1, v[36:39] offset:16384
	s_waitcnt vmcnt(14)
	ds_write_b128 v1, v[40:43] offset:17408
	s_waitcnt vmcnt(13)
	ds_write_b128 v1, v[44:47] offset:18432
	s_waitcnt vmcnt(12)
	ds_write_b128 v1, v[68:71] offset:19456
	s_waitcnt vmcnt(11)
	ds_write_b128 v1, v[48:51] offset:20480
	s_waitcnt vmcnt(10)
	ds_write_b128 v1, v[72:75] offset:21504
	s_waitcnt vmcnt(9)
	ds_write_b128 v1, v[52:55] offset:22528
	s_waitcnt vmcnt(8)
	ds_write_b128 v1, v[56:59] offset:23552
	s_waitcnt lgkmcnt(0)
	s_barrier
	s_waitcnt vmcnt(7)
	ds_write_b128 v0, v[60:63] offset:33792
	s_waitcnt vmcnt(6)
	ds_write_b128 v0, v[64:67] offset:35840
	s_waitcnt vmcnt(5)
	ds_write_b128 v0, v[76:79] offset:37888
	s_waitcnt vmcnt(4)
	ds_write_b128 v0, v[80:83] offset:39936
	s_waitcnt vmcnt(3)
	ds_write_b128 v0, v[84:87] offset:41984
	s_waitcnt vmcnt(2)
	ds_write_b128 v0, v[88:91] offset:44032
	s_waitcnt vmcnt(1)
	ds_write_b128 v0, v[92:95] offset:46080
	s_waitcnt vmcnt(0)
	ds_write_b128 v0, v[96:99] offset:48128
	s_waitcnt lgkmcnt(0)
	s_barrier
	s_endpgm
	s_nop 0
	s_nop 0
	s_nop 0
	s_nop 0
	s_nop 0
	s_nop 0
	s_nop 0
	s_nop 0
	s_nop 0
	s_nop 0
	s_nop 0
	s_nop 0
	s_nop 0
	s_nop 0
	s_nop 0
	s_nop 0
	s_nop 0
	s_nop 0
	s_nop 0
	s_nop 0
	s_nop 0
	s_nop 0
	s_nop 0
	s_nop 0
	s_nop 0
	s_nop 0
	s_endpgm

	.amdhsa_kernel _Z6k_gemmILi1EEvPKDF16_S1_PKfS3_S1_PDF16_PfS1_S5_
		.amdhsa_group_segment_fixed_size 50176
		.amdhsa_private_segment_fixed_size 0
		.amdhsa_kernarg_size 72
		.amdhsa_user_sgpr_count 2
		.amdhsa_user_sgpr_dispatch_ptr 0
		.amdhsa_user_sgpr_queue_ptr 0
		.amdhsa_user_sgpr_kernarg_segment_ptr 1
		.amdhsa_user_sgpr_dispatch_id 0
		.amdhsa_user_sgpr_kernarg_preload_length 0
		.amdhsa_user_sgpr_kernarg_preload_offset 0
		.amdhsa_user_sgpr_private_segment_size 0
		.amdhsa_uses_dynamic_stack 0
		.amdhsa_enable_private_segment 0
		.amdhsa_system_sgpr_workgroup_id_x 1
		.amdhsa_system_sgpr_workgroup_id_y 0
		.amdhsa_system_sgpr_workgroup_id_z 0
		.amdhsa_system_sgpr_workgroup_info 0
		.amdhsa_system_vgpr_workitem_id 0
		.amdhsa_next_free_vgpr 198
		.amdhsa_next_free_sgpr 96
		.amdhsa_accum_offset 200
		.amdhsa_reserve_vcc 1
		.amdhsa_float_round_mode_32 0
		.amdhsa_float_round_mode_16_64 0
		.amdhsa_float_denorm_mode_32 3
		.amdhsa_float_denorm_mode_16_64 3
		.amdhsa_dx10_clamp 1
		.amdhsa_ieee_mode 1
		.amdhsa_fp16_overflow 0
		.amdhsa_tg_split 0
		.amdhsa_exception_fp_ieee_invalid_op 0
		.amdhsa_exception_fp_denorm_src 0
		.amdhsa_exception_fp_ieee_div_zero 0
		.amdhsa_exception_fp_ieee_overflow 0
		.amdhsa_exception_fp_ieee_underflow 0
		.amdhsa_exception_fp_ieee_inexact 0
		.amdhsa_exception_int_div_zero 0
	.end_amdhsa_kernel

amdhsa.kernels:
  - .agpr_count:     16
    .args:
      - .actual_access:  read_only
        .address_space:  global
        .offset:         0
        .size:           8
        .value_kind:     global_buffer
      - .actual_access:  read_only
        .address_space:  global
        .offset:         8
        .size:           8
        .value_kind:     global_buffer
      - .actual_access:  read_only
        .address_space:  global
        .offset:         16
        .size:           8
        .value_kind:     global_buffer
      - .actual_access:  read_only
        .address_space:  global
        .offset:         24
        .size:           8
        .value_kind:     global_buffer
      - .actual_access:  write_only
        .address_space:  global
        .offset:         32
        .size:           8
        .value_kind:     global_buffer
      - .actual_access:  write_only
        .address_space:  global
        .offset:         40
        .size:           8
        .value_kind:     global_buffer
      - .actual_access:  write_only
        .address_space:  global
        .offset:         48
        .size:           8
        .value_kind:     global_buffer
      - .actual_access:  write_only
        .address_space:  global
        .offset:         56
        .size:           8
        .value_kind:     global_buffer
      - .actual_access:  read_only
        .address_space:  global
        .offset:         64
        .size:           8
        .value_kind:     global_buffer
      - .actual_access:  read_only
        .address_space:  global
        .offset:         72
        .size:           8
        .value_kind:     global_buffer
      - .actual_access:  read_only
        .address_space:  global
        .offset:         80
        .size:           8
        .value_kind:     global_buffer
    .group_segment_fixed_size: 33792
    .kernarg_segment_align: 8
    .kernarg_segment_size: 88
    .language:       OpenCL C
    .language_version:
      - 2
      - 0
    .max_flat_workgroup_size: 256
    .name:           _Z6k_prepPKfS0_S0_S0_PDF16_S1_S1_S1_S0_S0_S0_
    .private_segment_fixed_size: 0
    .sgpr_count:     22
    .sgpr_spill_count: 0
    .symbol:         _Z6k_prepPKfS0_S0_S0_PDF16_S1_S1_S1_S0_S0_S0_.kd
    .uniform_work_group_size: 1
    .uses_dynamic_stack: false
    .vgpr_count:     184
    .vgpr_spill_count: 0
    .wavefront_size: 64
  - .agpr_count:     0
    .args:
      - .actual_access:  read_only
        .address_space:  global
        .offset:         0
        .size:           8
        .value_kind:     global_buffer
      - .actual_access:  read_only
        .address_space:  global
        .offset:         8
        .size:           8
        .value_kind:     global_buffer
      - .actual_access:  read_only
        .address_space:  global
        .offset:         16
        .size:           8
        .value_kind:     global_buffer
      - .actual_access:  write_only
        .address_space:  global
        .offset:         24
        .size:           8
        .value_kind:     global_buffer
    .group_segment_fixed_size: 0
    .kernarg_segment_align: 8
    .kernarg_segment_size: 32
    .language:       OpenCL C
    .language_version:
      - 2
      - 0
    .max_flat_workgroup_size: 128
    .name:           _Z7k_finalPKfS0_S0_Pf
    .private_segment_fixed_size: 0
    .sgpr_count:     18
    .sgpr_spill_count: 0
    .symbol:         _Z7k_finalPKfS0_S0_Pf.kd
    .uniform_work_group_size: 1
    .uses_dynamic_stack: false
    .vgpr_count:     62
    .vgpr_spill_count: 0
    .wavefront_size: 64
  - .agpr_count:     0
    .args:
      - .actual_access:  read_only
        .address_space:  global
        .offset:         0
        .size:           8
        .value_kind:     global_buffer
      - .actual_access:  read_only
        .address_space:  global
        .offset:         8
        .size:           8
        .value_kind:     global_buffer
      - .actual_access:  read_only
        .address_space:  global
        .offset:         16
        .size:           8
        .value_kind:     global_buffer
      - .actual_access:  read_only
        .address_space:  global
        .offset:         24
        .size:           8
        .value_kind:     global_buffer
      - .actual_access:  read_only
        .address_space:  global
        .offset:         32
        .size:           8
        .value_kind:     global_buffer
      - .actual_access:  write_only
        .address_space:  global
        .offset:         40
        .size:           8
        .value_kind:     global_buffer
      - .actual_access:  write_only
        .address_space:  global
        .offset:         48
        .size:           8
        .value_kind:     global_buffer
      - .actual_access:  read_only
        .address_space:  global
        .offset:         56
        .size:           8
        .value_kind:     global_buffer
      - .actual_access:  read_only
        .address_space:  global
        .offset:         64
        .size:           8
        .value_kind:     global_buffer
    .group_segment_fixed_size: 33808
    .kernarg_segment_align: 8
    .kernarg_segment_size: 72
    .language:       OpenCL C
    .language_version:
      - 2
      - 0
    .max_flat_workgroup_size: 384
    .name:           _Z6k_gemmILi0EEvPKDF16_S1_PKfS3_S1_PDF16_PfS1_S5_
    .private_segment_fixed_size: 0
    .sgpr_count:     20
    .sgpr_spill_count: 0
    .symbol:         _Z6k_gemmILi0EEvPKDF16_S1_PKfS3_S1_PDF16_PfS1_S5_.kd
    .uniform_work_group_size: 1
    .uses_dynamic_stack: false
    .vgpr_count:     166
    .vgpr_spill_count: 0
    .wavefront_size: 64
  - .agpr_count:     0
    .args:
      - .actual_access:  read_only
        .address_space:  global
        .offset:         0
        .size:           8
        .value_kind:     global_buffer
      - .actual_access:  read_only
        .address_space:  global
        .offset:         8
        .size:           8
        .value_kind:     global_buffer
      - .actual_access:  read_only
        .address_space:  global
        .offset:         16
        .size:           8
        .value_kind:     global_buffer
      - .actual_access:  read_only
        .address_space:  global
        .offset:         24
        .size:           8
        .value_kind:     global_buffer
      - .actual_access:  read_only
        .address_space:  global
        .offset:         32
        .size:           8
        .value_kind:     global_buffer
      - .actual_access:  read_only
        .address_space:  global
        .offset:         40
        .size:           8
        .value_kind:     global_buffer
      - .actual_access:  read_only
        .address_space:  global
        .offset:         48
        .size:           8
        .value_kind:     global_buffer
      - .actual_access:  read_only
        .address_space:  global
        .offset:         56
        .size:           8
        .value_kind:     global_buffer
      - .actual_access:  write_only
        .address_space:  global
        .offset:         64
        .size:           8
        .value_kind:     global_buffer
    .group_segment_fixed_size: 50176
    .kernarg_segment_align: 8
    .kernarg_segment_size: 72
    .language:       OpenCL C
    .language_version:
      - 2
      - 0
    .max_flat_workgroup_size: 384
    .name:           _Z6k_gemmILi1EEvPKDF16_S1_PKfS3_S1_PDF16_PfS1_S5_
    .private_segment_fixed_size: 0
    .sgpr_count:     20
    .sgpr_spill_count: 0
    .symbol:         _Z6k_gemmILi1EEvPKDF16_S1_PKfS3_S1_PDF16_PfS1_S5_.kd
    .uniform_work_group_size: 1
    .uses_dynamic_stack: false
    .vgpr_count:     198
    .vgpr_spill_count: 0
    .wavefront_size: 64
